# T5 extended: s_setprio flips also around the memory-attention unit's MFMA clusters and the attention prologue/tail clusters
# speedup vs baseline: 1.0067x; 1.0048x over previous
; #define LAS __attribute__((address_space(3)))
; __device__ __forceinline__ int v_st(int k, int c) { const int kk = (k & ~0xC) | ((k & 4) << 1) | ((k & 8) >> 1); return ((kk >> 3) * 4 + (c >> 5)) * 512 + ((kk & 7) * 32 + (c & 31)) * 2; }
; __device__ __forceinline__ int v_rd_base(int lane) { return ((lane & 3) << 3) | (((lane >> 2) & 3) << 6) | (((lane >> 4) & 1) << 5) | (((lane >> 5) & 1) << 8); }
; #define ATT_SLOAD(S, k0) do { S##_v0 = *(const bf16x8*)(Vh + (size_t)(k0) * NC); S##_v1 = *(const bf16x8*)(Vh + (size_t)((k0) + 32) * NC); \
;     S##_k0 = *(const bf16x8*)(Kh + (size_t)(k0) * NC); S##_k1 = *(const bf16x8*)(Kh + (size_t)((k0) + 32) * NC); } while (0)
; #define ATT_SWAIT() asm volatile("s_waitcnt vmcnt(4)" ::: "memory")
; __device__ __forceinline__ void qkt(f32x16& p0, f32x16& p1, LAS const unsigned char* Ks, const bf16x8* qr, int r32, int hi) {
;     p0 = f32x16{}; p1 = f32x16{};
; #pragma unroll
;     for (int d0 = 0; d0 < 8; ++d0) { const int cb = (d0 * 16 + hi * 8) * 2;
;         const bf16x8 b0 = *(LAS const bf16x8*)(Ks + ATT_KSWZ(r32, cb));
;         const bf16x8 b1 = *(LAS const bf16x8*)(Ks + ATT_KSWZ(32 + r32, cb));
;         p0 = __builtin_amdgcn_mfma_f32_32x32x16_bf16(b0, qr[d0], p0, 0, 0, 0);
;         p1 = __builtin_amdgcn_mfma_f32_32x32x16_bf16(b1, qr[d0], p1, 0, 0, 0); }
; }
; template <bool MOBA>
; __device__ __forceinline__ void run_unit(const UnitDesc& U, LAS unsigned char* lds, f32x16 (&o)[4], float (&rli)[16]) {
;     ...
;     const int sr = tid >> 4, sc = (tid & 15) * 8, vst0 = v_st(sr, sc), vst1 = v_st(32 + sr, sc), kst0 = ATT_KSWZ(sr, sc * 2), kst1 = ATT_KSWZ(32 + sr, sc * 2);
;     LAS const unsigned char* vb0 = V_lds + v_rd_base(lane);
;     const bf16_t* Kh = U.K + (size_t)(sr + kt0 * KVBLK) * NC + sc; const bf16_t* Vh = U.V + (size_t)(sr + kt0 * KVBLK) * NC + sc;
;     qpos -= kt0 * KVBLK; qlo -= kt0 * KVBLK;
;     bf16x8 sA_v0, sA_v1, sA_k0, sA_k1, sB_v0, sB_v1, sB_k0, sB_k1;
;     ...
;     f32x16 pA0, pA1, pB0, pB1; float mnA, mnB, alA, alB; bf16x8 pa0, pa1, pa2, pa3; const int NT = U.nt - kt0;
;     ATT_SLOAD(sA, 0); ATT_SLOAD(sB, KVBLK); ATT_SWAIT(); ATT_SWRITE(0, sA); __syncthreads();
;     qkt(pA0, pA1, K_lds, qr, r32, hi); ATT_PSM(pA0, pA1, mnA, alA, 0);
.LBB0_626:
	s_lshl_b32 s2, s21, 7
	s_and_b32 s67, s23, 0xffffffe0
	s_mul_hi_u32 s0, s22, 0xe800
	s_mul_i32 s22, s22, 0xe800
	v_readlane_b32 s4, v253, 48
	v_readlane_b32 s5, v253, 49
	s_add_u32 s1, s4, s22
	s_addc_u32 s4, s5, s0
	v_writelane_b32 v254, s2, 51
	s_lshl_b32 s2, s2, 1
	s_add_u32 s0, s1, s2
	v_lshlrev_b32_e32 v24, 3, v4
	s_addc_u32 s1, s4, 0
	v_and_b32_e32 v6, 0x78, v24
	s_add_u32 s4, s0, 0x1000
	v_ashrrev_i32_e32 v5, 4, v4
	v_lshlrev_b32_e32 v22, 1, v6
	v_mov_b64_e32 v[6:7], s[0:1]
	s_mov_b32 s6, 0xe800
	s_addc_u32 s5, s1, 0
	v_mad_i64_i32 v[6:7], s[0:1], v5, s6, v[6:7]
	v_mov_b32_e32 v23, v3
	v_lshl_add_u64 v[188:189], v[6:7], 0, v[22:23]
	v_mov_b64_e32 v[6:7], s[4:5]
	v_mad_i64_i32 v[6:7], s[0:1], v5, s6, v[6:7]
	v_lshl_add_u64 v[190:191], v[6:7], 0, v[22:23]
	s_mov_b32 s0, 0x1d0000
	v_add_co_u32_e32 v6, vcc, s0, v190
	v_and_b32_e32 v23, 0xfffff0, v5
	s_nop 0
	v_addc_co_u32_e32 v7, vcc, 0, v191, vcc
	global_load_dwordx4 v[6:9], v[6:7], off
	s_nop 0
	global_load_dwordx4 v[10:13], v[190:191], off
	global_load_dwordx4 v[14:17], v[188:189], off offset:2048
	v_add_co_u32_e32 v18, vcc, s0, v188
	v_lshlrev_b32_e32 v25, 1, v5
	s_nop 0
	v_addc_co_u32_e32 v19, vcc, 0, v189, vcc
	global_load_dwordx4 v[18:21], v[18:19], off offset:2048
	v_lshrrev_b32_e32 v26, 1, v5
	v_and_b32_e32 v27, 3, v5
	v_add_u32_e32 v28, 32, v5
	v_and_or_b32 v23, v25, 8, v23
	v_and_b32_e32 v52, 31, v4
	v_and_b32_e32 v53, 63, v4
	v_and_b32_e32 v4, 0xf0, v4
	v_bfe_u32 v24, v24, 5, 2
	v_lshlrev_b32_e32 v5, 8, v5
	v_and_or_b32 v25, v26, 4, v27
	v_and_b32_e32 v26, 0xfffff0, v28
	v_lshlrev_b32_e32 v27, 1, v28
	v_lshlrev_b32_e32 v28, 8, v28
	v_lshrrev_b32_e32 v23, 1, v23
	v_and_b32_e32 v29, 48, v22
	v_and_or_b32 v26, v27, 8, v26
	v_bitop3_b32 v5, v22, v5, v4 bitop3:0xde
	v_bitop3_b32 v4, v22, v28, v4 bitop3:0xde
	v_or_b32_e32 v22, v23, v24
	v_lshlrev_b32_e32 v25, 6, v25
	v_lshrrev_b32_e32 v23, 1, v26
	v_add_u32_e32 v214, 0, v4
	v_lshlrev_b32_e32 v4, 9, v22
	v_add_u32_e32 v213, 0, v5
	v_or_b32_e32 v5, v23, v24
	v_or3_b32 v4, v4, v25, v29
	s_mov_b32 s0, 0x3a0000
	v_lshlrev_b32_e32 v5, 9, v5
	v_add_u32_e32 v215, 0, v4
	v_add_co_u32_e32 v4, vcc, s0, v188
	v_or3_b32 v24, v5, v25, v29
	s_nop 0
	v_addc_co_u32_e32 v5, vcc, 0, v189, vcc
	s_mov_b32 s1, 0x570000
	v_add_co_u32_e32 v22, vcc, s1, v188
	v_add_u32_e32 v216, 0, v24
	s_nop 0
	v_addc_co_u32_e32 v23, vcc, 0, v189, vcc
	global_load_dwordx4 v[36:39], v[4:5], off offset:2048
	global_load_dwordx4 v[40:43], v[22:23], off offset:2048
	v_add_co_u32_e32 v4, vcc, s0, v190
	s_movk_i32 s0, 0xf0
	s_nop 0
	v_addc_co_u32_e32 v5, vcc, 0, v191, vcc
	v_add_co_u32_e32 v22, vcc, s1, v190
	v_lshl_add_u32 v62, v52, 8, 0
	s_nop 0
	v_addc_co_u32_e32 v23, vcc, 0, v191, vcc
	global_load_dwordx4 v[44:47], v[4:5], off
	global_load_dwordx4 v[48:51], v[22:23], off
	s_waitcnt vmcnt(4)
	s_waitcnt vmcnt(6)
	ds_write_b128 v215, v[10:13]
	ds_write_b128 v216, v[6:9]
	s_waitcnt vmcnt(5)
	ds_write_b128 v213, v[14:17] offset:32768
	s_waitcnt vmcnt(4)
	ds_write_b128 v214, v[18:21] offset:32768
	v_lshlrev_b32_e32 v12, 4, v52
	v_bitop3_b32 v4, v2, v12, s0 bitop3:0x78
	v_add_u32_e32 v204, v62, v4
	s_waitcnt lgkmcnt(0)
	s_barrier
	ds_read_b128 v[4:7], v204 offset:32768
	ds_read_b128 v[8:11], v204 offset:40960
	s_waitcnt lgkmcnt(1)
	s_setprio 1
	v_mfma_f32_32x32x16_bf16 v[20:35], v[4:7], v[144:147], 0
	v_and_b32_e32 v63, 0xf0, v12
	v_bitop3_b32 v54, v2, v63, 32 bitop3:0x36
	v_add_u32_e32 v208, v62, v54
	ds_read_b128 v[54:57], v208 offset:32768
	ds_read_b128 v[58:61], v208 offset:40960
	s_movk_i32 s0, 0x60
	s_mov_b32 s4, 0x41400000
	v_lshlrev_b32_e32 v201, 2, v1
	s_waitcnt lgkmcnt(2)
	v_mfma_f32_32x32x16_bf16 v[4:19], v[8:11], v[144:147], 0
	s_waitcnt lgkmcnt(1)
	v_mfma_f32_32x32x16_bf16 v[20:35], v[54:57], v[140:143], v[20:35]
	v_bitop3_b32 v54, v2, v63, 64 bitop3:0x36
	v_add_u32_e32 v209, v62, v54
	s_waitcnt lgkmcnt(0)
	v_mfma_f32_32x32x16_bf16 v[4:19], v[58:61], v[140:143], v[4:19]
	ds_read_b128 v[54:57], v209 offset:32768
	ds_read_b128 v[58:61], v209 offset:40960
	s_waitcnt lgkmcnt(1)
	v_mfma_f32_32x32x16_bf16 v[20:35], v[54:57], v[136:139], v[20:35]
	v_bitop3_b32 v54, v2, v63, s0 bitop3:0x36
	v_add_u32_e32 v210, v62, v54
	s_movk_i32 s0, 0x80
	s_waitcnt lgkmcnt(0)
	v_mfma_f32_32x32x16_bf16 v[4:19], v[58:61], v[136:139], v[4:19]
	ds_read_b128 v[54:57], v210 offset:32768
	ds_read_b128 v[58:61], v210 offset:40960
	s_waitcnt lgkmcnt(1)
	v_mfma_f32_32x32x16_bf16 v[20:35], v[54:57], v[132:135], v[20:35]
	v_bitop3_b32 v54, v2, v63, s0 bitop3:0x36
	v_add_u32_e32 v202, v62, v54
	s_movk_i32 s0, 0xa0
	s_waitcnt lgkmcnt(0)
	v_mfma_f32_32x32x16_bf16 v[4:19], v[58:61], v[132:135], v[4:19]
	ds_read_b128 v[54:57], v202 offset:32768
	ds_read_b128 v[58:61], v202 offset:40960
	s_waitcnt lgkmcnt(1)
	v_mfma_f32_32x32x16_bf16 v[20:35], v[54:57], v[128:131], v[20:35]
	v_bitop3_b32 v54, v2, v63, s0 bitop3:0x36
	v_add_u32_e32 v206, v62, v54
	ds_read_b128 v[54:57], v206 offset:32768
	s_lshl_b32 s0, s21, 3
	s_sub_i32 s0, 0xffffffd8, s0
	v_cvt_f32_i32_e32 v64, s0
	s_movk_i32 s0, 0xc0
	s_waitcnt lgkmcnt(1)
	v_mfma_f32_32x32x16_bf16 v[4:19], v[58:61], v[128:131], v[4:19]
	ds_read_b128 v[58:61], v206 offset:40960
	v_div_scale_f32 v67, vcc, v64, s4, v64
	s_waitcnt lgkmcnt(1)
	v_mfma_f32_32x32x16_bf16 v[20:35], v[54:57], v[124:127], v[20:35]
	v_bitop3_b32 v54, v2, v63, s0 bitop3:0x36
	v_add_u32_e32 v212, v62, v54
	v_div_scale_f32 v65, s[0:1], s4, s4, v64
	v_rcp_f32_e32 v66, v65
	ds_read_b128 v[54:57], v212 offset:32768
	s_movk_i32 s0, 0xe0
	s_waitcnt lgkmcnt(1)
; #define LAS __attribute__((address_space(3)))
; __device__ __forceinline__ void qkt(f32x16& p0, f32x16& p1, LAS const unsigned char* Ks, const bf16x8* qr, int r32, int hi) {
;     p0 = f32x16{}; p1 = f32x16{};
; #pragma unroll
;     for (int d0 = 0; d0 < 8; ++d0) { const int cb = (d0 * 16 + hi * 8) * 2;
;         const bf16x8 b0 = *(LAS const bf16x8*)(Ks + ATT_KSWZ(r32, cb));
;         const bf16x8 b1 = *(LAS const bf16x8*)(Ks + ATT_KSWZ(32 + r32, cb));
;         p0 = __builtin_amdgcn_mfma_f32_32x32x16_bf16(b0, qr[d0], p0, 0, 0, 0);
;         p1 = __builtin_amdgcn_mfma_f32_32x32x16_bf16(b1, qr[d0], p1, 0, 0, 0); }
; }
; __device__ __forceinline__ void partialSM(f32x16& p0, f32x16& p1, float& m_reg, float& mn, float& alpha, int dq, float slopeL, bool diag, bool rowmasked) {
;     const float NEG = -__builtin_inff(); const float a0 = -slopeL * (float)dq;
; #pragma unroll
;     for (int r = 0; r < 16; ++r) { const int c = (r & 3) + 8 * (r >> 2);
;         p0[r] = fmaf(p0[r], CS, fmaf(slopeL, (float)c, a0)); p1[r] = fmaf(p1[r], CS, fmaf(slopeL, (float)(c + 32), a0)); }
	v_mfma_f32_32x32x16_bf16 v[4:19], v[58:61], v[124:127], v[4:19]
	v_fma_f32 v58, -v65, v66, 1.0
	v_fmac_f32_e32 v66, v58, v66
	v_mul_f32_e32 v68, v67, v66
	v_fma_f32 v58, -v65, v68, v67
	v_fmac_f32_e32 v68, v58, v66
	ds_read_b128 v[58:61], v212 offset:40960
	v_bitop3_b32 v2, v2, v63, s0 bitop3:0x36
	s_waitcnt lgkmcnt(1)
	v_mfma_f32_32x32x16_bf16 v[20:35], v[54:57], v[120:123], v[20:35]
	s_setprio 0
	v_fma_f32 v54, -v65, v68, v67
	v_div_fmas_f32 v54, v54, v66, v68
	v_add_u32_e32 v211, v62, v2
	v_div_fixup_f32 v64, v54, s4, v64
	ds_read_b128 v[54:57], v211 offset:32768
	s_mov_b32 s0, 0xc2fc0000
	v_cmp_gt_f32_e32 vcc, s0, v64
	v_mov_b32_e32 v2, 0x42800000
	s_and_b64 s[0:1], vcc, exec
	v_cndmask_b32_e32 v2, 0, v2, vcc
	v_add_f32_e32 v2, v64, v2
	s_cselect_b32 s0, 0xffffffc0, 0
	s_add_i32 s13, s67, s20
	s_waitcnt lgkmcnt(1)
	s_setprio 1
	v_mfma_f32_32x32x16_bf16 v[4:19], v[58:61], v[120:123], v[4:19]
	v_exp_f32_e32 v2, v2
	ds_read_b128 v[58:61], v211 offset:40960
	v_or_b32_e32 v200, s13, v52
	v_sub_u32_e32 v1, v200, v201
	v_ldexp_f32 v2, v2, s0
	v_mul_f32_e32 v182, 0x3fb8aa3b, v2
	s_mov_b32 s0, 2.0
	s_waitcnt lgkmcnt(1)
	v_mfma_f32_32x32x16_bf16 v[20:35], v[54:57], v[116:119], v[20:35]
	v_cvt_f32_i32_e32 v54, v1
	s_mov_b32 s1, 0x40400000
	s_cmp_gt_i32 s13, 62
	v_mul_f32_e64 v2, -v182, v54
	v_fma_f32 v56, v182, s0, v2
	v_fma_f32 v57, v182, s1, v2
	s_mov_b32 s0, 0x41000000
	s_mov_b32 s1, 0x41100000
	s_waitcnt lgkmcnt(0)
	v_mfma_f32_32x32x16_bf16 v[4:19], v[58:61], v[116:119], v[4:19]
	s_setprio 0
	v_fma_f32 v58, v182, s0, v2
	v_fma_f32 v59, v182, s1, v2
	s_mov_b32 s0, 0x41200000
	s_mov_b32 s1, 0x41300000
	v_fma_f32 v60, v182, s0, v2
	v_fma_f32 v61, v182, s1, v2
	s_mov_b32 s0, 0x41800000
	s_mov_b32 s1, 0x41880000
	v_pk_fma_f32 v[62:63], v[182:183], s[0:1], v[2:3] op_sel_hi:[0,1,0]
	s_mov_b32 s0, 0x41900000
	v_fma_f32 v55, -v182, v54, v182
	v_mov_b32_e32 v54, v2
	s_mov_b32 s1, 0x41980000
	v_fmac_f32_e32 v54, 0, v182
	v_pk_fma_f32 v[64:65], v[182:183], s[0:1], v[2:3] op_sel_hi:[0,1,0]
	v_pk_fma_f32 v[66:67], v[182:183], s[86:87], v[2:3] op_sel_hi:[0,1,0]
	v_pk_fma_f32 v[68:69], v[182:183], s[88:89], v[2:3] op_sel_hi:[0,1,0]
	v_pk_fma_f32 v[20:21], v[20:21], s[96:97], v[54:55] op_sel_hi:[1,0,1]
	v_pk_fma_f32 v[34:35], v[34:35], s[96:97], v[68:69] op_sel_hi:[1,0,1]
	v_pk_fma_f32 v[32:33], v[32:33], s[96:97], v[66:67] op_sel_hi:[1,0,1]
	v_pk_fma_f32 v[30:31], v[30:31], s[96:97], v[64:65] op_sel_hi:[1,0,1]
	v_pk_fma_f32 v[28:29], v[28:29], s[96:97], v[62:63] op_sel_hi:[1,0,1]
	v_pk_fma_f32 v[26:27], v[26:27], s[96:97], v[60:61] op_sel_hi:[1,0,1]
	v_pk_fma_f32 v[24:25], v[24:25], s[96:97], v[58:59] op_sel_hi:[1,0,1]
	v_pk_fma_f32 v[22:23], v[22:23], s[96:97], v[56:57] op_sel_hi:[1,0,1]
	v_pk_fma_f32 v[54:55], v[182:183], s[90:91], v[2:3] op_sel_hi:[0,1,0]
	v_pk_fma_f32 v[56:57], v[182:183], s[92:93], v[2:3] op_sel_hi:[0,1,0]
	v_pk_fma_f32 v[58:59], v[182:183], s[94:95], v[2:3] op_sel_hi:[0,1,0]
	v_pk_fma_f32 v[60:61], v[182:183], s[68:69], v[2:3] op_sel_hi:[0,1,0]
	v_pk_fma_f32 v[62:63], v[182:183], s[70:71], v[2:3] op_sel_hi:[0,1,0]
	v_pk_fma_f32 v[64:65], v[182:183], s[72:73], v[2:3] op_sel_hi:[0,1,0]
	v_pk_fma_f32 v[66:67], v[182:183], s[74:75], v[2:3] op_sel_hi:[0,1,0]
	v_pk_fma_f32 v[68:69], v[182:183], s[76:77], v[2:3] op_sel_hi:[0,1,0]
	v_pk_fma_f32 v[4:5], v[4:5], s[96:97], v[68:69] op_sel_hi:[1,0,1]
	v_pk_fma_f32 v[18:19], v[18:19], s[96:97], v[66:67] op_sel_hi:[1,0,1]
	v_pk_fma_f32 v[16:17], v[16:17], s[96:97], v[64:65] op_sel_hi:[1,0,1]
	v_pk_fma_f32 v[14:15], v[14:15], s[96:97], v[62:63] op_sel_hi:[1,0,1]
	v_pk_fma_f32 v[12:13], v[12:13], s[96:97], v[60:61] op_sel_hi:[1,0,1]
	v_pk_fma_f32 v[10:11], v[10:11], s[96:97], v[58:59] op_sel_hi:[1,0,1]
	v_pk_fma_f32 v[8:9], v[8:9], s[96:97], v[56:57] op_sel_hi:[1,0,1]
	v_pk_fma_f32 v[6:7], v[6:7], s[96:97], v[54:55] op_sel_hi:[1,0,1]
	s_cbranch_scc1 .LBB0_630
; __device__ __forceinline__ void partialSM(f32x16& p0, f32x16& p1, float& m_reg, float& mn, float& alpha, int dq, float slopeL, bool diag, bool rowmasked) {
;     ...
;     for (int r = 0; r < 16; ++r) { const int c = (r & 3) + 8 * (r >> 2);
;         p0[r] = fmaf(p0[r], CS, fmaf(slopeL, (float)c, a0)); p1[r] = fmaf(p1[r], CS, fmaf(slopeL, (float)(c + 32), a0)); }
;     if (diag) { asm volatile("" ::: "memory");
; #pragma unroll
;         for (int r = 0; r < 16; ++r) { const int c = (r & 3) + 8 * (r >> 2); if (c > dq) p0[r] = NEG; if (c + 32 > dq) p1[r] = NEG; } }
	v_cmp_gt_i32_e64 s[62:63], 57, v1
	v_cmp_gt_i32_e64 s[64:65], 58, v1
	v_cmp_gt_i32_e64 s[60:61], 56, v1
	s_and_b64 s[62:63], s[64:65], s[62:63]
	v_cmp_gt_i32_e64 s[58:59], 51, v1
	s_and_b64 s[60:61], s[62:63], s[60:61]
	v_cmp_gt_i32_e64 s[56:57], 50, v1
	s_and_b64 s[58:59], s[60:61], s[58:59]
	v_cmp_gt_i32_e64 s[54:55], 49, v1
	s_and_b64 s[56:57], s[58:59], s[56:57]
	v_cmp_gt_i32_e64 s[52:53], 48, v1
	s_and_b64 s[54:55], s[56:57], s[54:55]
	v_cmp_gt_i32_e64 s[50:51], 43, v1
	s_and_b64 s[52:53], s[54:55], s[52:53]
	v_cmp_gt_i32_e64 s[48:49], 42, v1
	s_and_b64 s[50:51], s[52:53], s[50:51]
	v_cmp_gt_i32_e64 s[46:47], 41, v1
	s_and_b64 s[48:49], s[50:51], s[48:49]
	v_cmp_gt_i32_e64 s[44:45], 40, v1
	s_and_b64 s[46:47], s[48:49], s[46:47]
	v_cmp_gt_i32_e64 s[42:43], 35, v1
	s_and_b64 s[44:45], s[46:47], s[44:45]
	v_cmp_gt_i32_e64 s[40:41], 34, v1
	s_and_b64 s[42:43], s[44:45], s[42:43]
	v_cmp_gt_i32_e64 s[38:39], 33, v1
	s_and_b64 s[40:41], s[42:43], s[40:41]
	v_cmp_gt_i32_e64 s[36:37], 32, v1
	s_and_b64 s[38:39], s[40:41], s[38:39]
	s_and_b64 s[36:37], s[38:39], s[36:37]
	v_cmp_gt_i32_e32 vcc, 0, v1
	v_cmp_gt_i32_e64 s[0:1], 1, v1
	v_cmp_gt_i32_e64 s[6:7], 2, v1
	v_cmp_gt_i32_e64 s[8:9], 3, v1
	v_cmp_gt_i32_e64 s[10:11], 8, v1
	v_cmp_gt_i32_e64 s[14:15], 9, v1
	v_cmp_gt_i32_e64 s[16:17], 10, v1
	v_cmp_gt_i32_e64 s[18:19], 11, v1
	v_cmp_gt_i32_e64 s[20:21], 16, v1
	v_cmp_gt_i32_e64 s[22:23], 17, v1
	v_cmp_gt_i32_e64 s[24:25], 18, v1
	v_cmp_gt_i32_e64 s[26:27], 19, v1
	v_cmp_gt_i32_e64 s[28:29], 24, v1
	v_cmp_gt_i32_e64 s[30:31], 25, v1
	v_cmp_gt_i32_e64 s[34:35], 26, v1
	v_cndmask_b32_e64 v18, v18, v241, s[64:65]
	v_cndmask_b32_e64 v17, v17, v241, s[62:63]
	v_cndmask_b32_e64 v16, v16, v241, s[60:61]
	v_cndmask_b32_e64 v15, v15, v241, s[58:59]
	v_cndmask_b32_e64 v14, v14, v241, s[56:57]
	v_cndmask_b32_e64 v13, v13, v241, s[54:55]
	v_cndmask_b32_e64 v12, v12, v241, s[52:53]
	v_cndmask_b32_e64 v11, v11, v241, s[50:51]
	v_cndmask_b32_e64 v10, v10, v241, s[48:49]
	v_cndmask_b32_e64 v9, v9, v241, s[46:47]
	v_cndmask_b32_e64 v8, v8, v241, s[44:45]
	v_cndmask_b32_e64 v7, v7, v241, s[42:43]
	v_cndmask_b32_e64 v6, v6, v241, s[40:41]
	v_cndmask_b32_e64 v5, v5, v241, s[38:39]
	v_cndmask_b32_e64 v4, v4, v241, s[36:37]
	v_cmp_gt_i32_e64 s[36:37], 27, v1
	v_cmp_gt_i32_e64 s[38:39], 59, v1
	s_and_saveexec_b64 s[4:5], s[38:39]
	v_mov_b32_e32 v19, s85
	s_or_b64 exec, exec, s[4:5]
	s_and_b64 s[34:35], s[36:37], s[34:35]
	s_and_b64 s[30:31], s[34:35], s[30:31]
	s_and_b64 s[28:29], s[30:31], s[28:29]
	s_and_b64 s[26:27], s[28:29], s[26:27]
	s_and_b64 s[24:25], s[26:27], s[24:25]
	s_and_b64 s[22:23], s[24:25], s[22:23]
	s_and_b64 s[20:21], s[22:23], s[20:21]
	s_and_b64 s[18:19], s[20:21], s[18:19]
	s_and_b64 s[16:17], s[18:19], s[16:17]
	s_and_b64 s[14:15], s[16:17], s[14:15]
	s_and_b64 s[10:11], s[14:15], s[10:11]
	s_and_b64 s[8:9], s[10:11], s[8:9]
	s_and_b64 s[6:7], s[8:9], s[6:7]
	s_and_b64 s[0:1], s[6:7], s[0:1]
	s_and_b64 vcc, s[0:1], vcc
	v_cndmask_b32_e64 v34, v34, v241, s[34:35]
	v_cndmask_b32_e64 v33, v33, v241, s[30:31]
	v_cndmask_b32_e64 v32, v32, v241, s[28:29]
	v_cndmask_b32_e64 v31, v31, v241, s[26:27]
	v_cndmask_b32_e64 v30, v30, v241, s[24:25]
	v_cndmask_b32_e64 v29, v29, v241, s[22:23]
	v_cndmask_b32_e64 v28, v28, v241, s[20:21]
	v_cndmask_b32_e64 v27, v27, v241, s[18:19]
	v_cndmask_b32_e64 v26, v26, v241, s[16:17]
	v_cndmask_b32_e64 v25, v25, v241, s[14:15]
	v_cndmask_b32_e64 v24, v24, v241, s[10:11]
	v_cndmask_b32_e64 v23, v23, v241, s[8:9]
	v_cndmask_b32_e64 v22, v22, v241, s[6:7]
	v_cndmask_b32_e64 v21, v21, v241, s[0:1]
	v_cndmask_b32_e32 v20, v20, v241, vcc
	v_cndmask_b32_e64 v35, v35, v241, s[36:37]

; __device__ __forceinline__ void qkt(f32x16& p0, f32x16& p1, LAS const unsigned char* Ks, const bf16x8* qr, int r32, int hi) {
;     p0 = f32x16{}; p1 = f32x16{};
; #pragma unroll
;     for (int d0 = 0; d0 < 8; ++d0) { const int cb = (d0 * 16 + hi * 8) * 2;
;         const bf16x8 b0 = *(LAS const bf16x8*)(Ks + ATT_KSWZ(r32, cb));
;         const bf16x8 b1 = *(LAS const bf16x8*)(Ks + ATT_KSWZ(32 + r32, cb));
;         p0 = __builtin_amdgcn_mfma_f32_32x32x16_bf16(b0, qr[d0], p0, 0, 0, 0);
;         p1 = __builtin_amdgcn_mfma_f32_32x32x16_bf16(b1, qr[d0], p1, 0, 0, 0); }
; }
; __device__ __forceinline__ void partialSM(f32x16& p0, f32x16& p1, float& m_reg, float& mn, float& alpha, int dq, float slopeL, bool diag, bool rowmasked) {
;     const float NEG = -__builtin_inff(); const float a0 = -slopeL * (float)dq;
; #pragma unroll
;     for (int r = 0; r < 16; ++r) { const int c = (r & 3) + 8 * (r >> 2);
;         p0[r] = fmaf(p0[r], CS, fmaf(slopeL, (float)c, a0)); p1[r] = fmaf(p1[r], CS, fmaf(slopeL, (float)(c + 32), a0)); }
;     if (diag) { asm volatile("" ::: "memory");
; #pragma unroll
;         for (int r = 0; r < 16; ++r) { const int c = (r & 3) + 8 * (r >> 2); if (c > dq) p0[r] = NEG; if (c + 32 > dq) p1[r] = NEG; } }
;     if (rowmasked) {
; #pragma unroll
;         for (int r = 0; r < 16; ++r) { p0[r] = NEG; p1[r] = NEG; } }
;     float pmax = p0[0];
; #pragma unroll
;     for (int r = 1; r < 16; ++r) pmax = fmaxf(pmax, p0[r]);
; #pragma unroll
;     for (int r = 0; r < 16; ++r) pmax = fmaxf(pmax, p1[r]);
;     { auto rr = __builtin_amdgcn_permlane32_swap(__float_as_uint(pmax), __float_as_uint(pmax), false, false);
;       pmax = fmaxf(__uint_as_float(rr[0]), __uint_as_float(rr[1])); }
;     if (__builtin_expect(__all(pmax - m_reg <= THRL), 1)) { mn = m_reg; alpha = 1.f; }
;     else { mn = fmaxf(m_reg, pmax); alpha = __builtin_amdgcn_exp2f(m_reg - mn); m_reg = mn; }
; #pragma unroll
;     for (int r = 0; r < 16; ++r) { p0[r] = p0[r] - mn; p1[r] = p1[r] - mn; }
; #pragma unroll
;     for (int r = 0; r < 16; ++r) p0[r] = __builtin_amdgcn_exp2f(p0[r]);
; }
; __device__ __forceinline__ void finishSM(f32x16& p0, f32x16& p1, float alpha, float& l_reg, bf16x8& pa0, bf16x8& pa1, bf16x8& pa2, bf16x8& pa3) {
; #pragma unroll
;     for (int r = 0; r < 16; ++r) p1[r] = __builtin_amdgcn_exp2f(p1[r]);
;     float ps = 0;
; #pragma unroll
.LBB0_657:
	ds_read_b128 v[76:79], v204 offset:49152
	v_add_f32_e32 v2, 0, v114
	v_cvt_pk_bf16_f32 v148, v114, v1
	v_add_f32_e32 v1, v1, v2
	v_add_f32_e32 v1, v112, v1
	v_add_f32_e32 v1, v113, v1
	v_add_f32_e32 v1, v110, v1
	v_cvt_pk_bf16_f32 v149, v112, v113
	v_cvt_pk_bf16_f32 v150, v110, v111
	v_add_f32_e32 v1, v111, v1
	ds_read_b128 v[110:113], v208 offset:57344
	s_waitcnt lgkmcnt(1)
	s_setprio 1
	v_mfma_f32_32x32x16_bf16 v[92:107], v[76:79], v[144:147], 0
	ds_read_b128 v[76:79], v208 offset:49152
	v_add_f32_e32 v1, v108, v1
	v_add_f32_e32 v1, v109, v1
	v_add_f32_e32 v1, v68, v1
	v_add_f32_e32 v1, v69, v1
	v_add_f32_e32 v1, v70, v1
	v_add_f32_e32 v1, v75, v1
	s_waitcnt lgkmcnt(0)
	v_mfma_f32_32x32x16_bf16 v[92:107], v[76:79], v[140:143], v[92:107]
	ds_read_b128 v[76:79], v204 offset:57344
	v_exp_f32_e32 v114, v164
	v_add_f32_e32 v1, v72, v1
	v_exp_f32_e32 v115, v165
	v_add_f32_e32 v1, v71, v1
	v_add_f32_e32 v1, v74, v1
	v_add_f32_e32 v1, v73, v1
	s_waitcnt lgkmcnt(0)
	v_mfma_f32_32x32x16_bf16 v[76:91], v[76:79], v[144:147], 0
	v_exp_f32_e32 v144, v166
	v_exp_f32_e32 v145, v167
	v_exp_f32_e32 v146, v168
	v_add_f32_e32 v1, v114, v1
	v_exp_f32_e32 v147, v169
	v_add_f32_e32 v1, v115, v1
	v_exp_f32_e32 v152, v170
	v_mfma_f32_32x32x16_bf16 v[76:91], v[110:113], v[140:143], v[76:91]
	ds_read_b128 v[110:113], v209 offset:49152
	v_add_f32_e32 v1, v144, v1
	v_exp_f32_e32 v153, v171
	v_add_f32_e32 v1, v145, v1
	v_exp_f32_e32 v154, v172
	v_add_f32_e32 v1, v146, v1
	v_exp_f32_e32 v155, v173
	s_waitcnt lgkmcnt(0)
	v_mfma_f32_32x32x16_bf16 v[92:107], v[110:113], v[136:139], v[92:107]
	ds_read_b128 v[110:113], v209 offset:57344
	v_add_f32_e32 v1, v147, v1
	v_exp_f32_e32 v156, v174
	v_add_f32_e32 v1, v152, v1
	v_exp_f32_e32 v157, v175
	v_add_f32_e32 v1, v153, v1
	v_exp_f32_e32 v158, v176
	s_waitcnt lgkmcnt(0)
	v_mfma_f32_32x32x16_bf16 v[76:91], v[110:113], v[136:139], v[76:91]
	ds_read_b128 v[110:113], v210 offset:49152
	v_add_f32_e32 v1, v154, v1
	v_exp_f32_e32 v159, v177
	v_add_f32_e32 v1, v155, v1
	v_exp_f32_e32 v160, v178
	v_add_f32_e32 v1, v156, v1
	v_exp_f32_e32 v161, v179
	s_waitcnt lgkmcnt(0)
	v_mfma_f32_32x32x16_bf16 v[92:107], v[110:113], v[132:135], v[92:107]
	ds_read_b128 v[110:113], v210 offset:57344
	v_add_f32_e32 v1, v157, v1
	v_add_f32_e32 v1, v158, v1
	v_add_f32_e32 v1, v159, v1
	v_add_f32_e32 v1, v160, v1
	v_add_f32_e32 v1, v161, v1
	v_mov_b32_e32 v2, v1
	s_waitcnt lgkmcnt(0)
	v_mfma_f32_32x32x16_bf16 v[76:91], v[110:113], v[132:135], v[76:91]
	ds_read_b128 v[110:113], v202 offset:49152
	v_cvt_pk_bf16_f32 v151, v108, v109
	v_cvt_pk_bf16_f32 v68, v68, v69
	v_cvt_pk_bf16_f32 v69, v70, v75
	v_cvt_pk_bf16_f32 v70, v72, v71
	v_cvt_pk_bf16_f32 v71, v74, v73
	v_cvt_pk_bf16_f32 v72, v114, v115
	s_waitcnt lgkmcnt(0)
	v_mfma_f32_32x32x16_bf16 v[92:107], v[110:113], v[128:131], v[92:107]
	ds_read_b128 v[110:113], v202 offset:57344
	v_cvt_pk_bf16_f32 v73, v144, v145
	v_cvt_pk_bf16_f32 v74, v146, v147
	v_cvt_pk_bf16_f32 v75, v152, v153
	v_cvt_pk_bf16_f32 v108, v154, v155
	v_permlane32_swap_b32_e32 v1, v2
	s_waitcnt lgkmcnt(0)
	v_mfma_f32_32x32x16_bf16 v[76:91], v[110:113], v[128:131], v[76:91]
	ds_read_b128 v[110:113], v206 offset:49152
	ds_read_b128 v[128:131], v206 offset:57344
	ds_read_b128 v[132:135], v212 offset:49152
	ds_read_b128 v[136:139], v212 offset:57344
	ds_read_b128 v[140:143], v211 offset:57344
	v_permlane32_swap_b32_e32 v68, v70
	v_permlane32_swap_b32_e32 v69, v71
	v_permlane32_swap_b32_e32 v72, v74
	s_waitcnt lgkmcnt(4)
	v_mfma_f32_32x32x16_bf16 v[92:107], v[110:113], v[124:127], v[92:107]
	ds_read_b128 v[110:113], v211 offset:49152
	v_permlane32_swap_b32_e32 v73, v75
	v_cvt_pk_bf16_f32 v109, v156, v157
	v_permlane32_swap_b32_e32 v148, v150
	v_permlane32_swap_b32_e32 v149, v151
	s_waitcnt lgkmcnt(4)
	v_mfma_f32_32x32x16_bf16 v[76:91], v[128:131], v[124:127], v[76:91]
	s_waitcnt lgkmcnt(3)
	v_mfma_f32_32x32x16_bf16 v[92:107], v[132:135], v[120:123], v[92:107]
	s_waitcnt lgkmcnt(2)
	v_mfma_f32_32x32x16_bf16 v[76:91], v[136:139], v[120:123], v[76:91]
	s_waitcnt lgkmcnt(0)
	v_mfma_f32_32x32x16_bf16 v[92:107], v[110:113], v[116:119], v[92:107]
	v_cvt_pk_bf16_f32 v110, v158, v159
	v_cvt_pk_bf16_f32 v111, v160, v161
	s_nop 0
	v_permlane32_swap_b32_e32 v108, v110
	v_permlane32_swap_b32_e32 v109, v111
	v_mfma_f32_32x32x16_bf16 v[76:91], v[140:143], v[116:119], v[76:91]
	ds_read_b64_tr_b16 v[112:113], v196
	ds_read_b64_tr_b16 v[114:115], v196 offset:2048
	ds_read_b64_tr_b16 v[116:117], v196 offset:4096
	ds_read_b64_tr_b16 v[118:119], v196 offset:6144
	ds_read_b64_tr_b16 v[120:121], v196 offset:8192
	ds_read_b64_tr_b16 v[122:123], v196 offset:10240
	ds_read_b64_tr_b16 v[124:125], v196 offset:12288
	ds_read_b64_tr_b16 v[126:127], v196 offset:14336
	s_waitcnt lgkmcnt(6)
	v_mfma_f32_32x32x16_bf16 v[52:67], v[148:151], v[112:115], v[52:67]
	v_readlane_b32 s83, v254, 59
	s_add_i32 s82, s83, 31
	s_lshl_b32 s0, s82, 6
	v_mov_b32_e32 v183, v182
	s_mov_b32 s84, 0x10000
	s_waitcnt lgkmcnt(4)
	v_mfma_f32_32x32x16_bf16 v[52:67], v[68:71], v[116:119], v[52:67]
	s_waitcnt lgkmcnt(2)
	v_mfma_f32_32x32x16_bf16 v[52:67], v[72:75], v[120:123], v[52:67]
	s_waitcnt lgkmcnt(0)
	v_mfma_f32_32x32x16_bf16 v[52:67], v[108:111], v[124:127], v[52:67]
	ds_read_b64_tr_b16 v[112:113], v196 offset:512
	ds_read_b64_tr_b16 v[114:115], v196 offset:2560
	ds_read_b64_tr_b16 v[116:117], v196 offset:4608
	ds_read_b64_tr_b16 v[118:119], v196 offset:6656
	ds_read_b64_tr_b16 v[120:121], v196 offset:8704
	ds_read_b64_tr_b16 v[122:123], v196 offset:10752
	ds_read_b64_tr_b16 v[124:125], v196 offset:12800
	ds_read_b64_tr_b16 v[126:127], v196 offset:14848
	s_waitcnt lgkmcnt(6)
; #define LAS __attribute__((address_space(3)))
; __device__ __forceinline__ s16x4 tr_read(LAS const unsigned char* p) { return __builtin_bit_cast(s16x4, __builtin_amdgcn_ds_read_tr16_b64_v4i16((LAS v4i16_t*)p)); }
; __device__ __forceinline__ void partialSM(f32x16& p0, f32x16& p1, float& m_reg, float& mn, float& alpha, int dq, float slopeL, bool diag, bool rowmasked) {
;     const float NEG = -__builtin_inff(); const float a0 = -slopeL * (float)dq;
; #pragma unroll
;     for (int r = 0; r < 16; ++r) { const int c = (r & 3) + 8 * (r >> 2);
;         p0[r] = fmaf(p0[r], CS, fmaf(slopeL, (float)c, a0)); p1[r] = fmaf(p1[r], CS, fmaf(slopeL, (float)(c + 32), a0)); }
; template <int D0> __device__ __forceinline__ void pv_one(f32x16& od, LAS const unsigned char* vb, bf16x8 pa0, bf16x8 pa1, bf16x8 pa2, bf16x8 pa3) {
;     const s16x4 l0 = tr_read(vb + v_rd_off(D0, 0, 0)), h0 = tr_read(vb + v_rd_off(D0, 0, 1)), l1 = tr_read(vb + v_rd_off(D0, 1, 0)), h1 = tr_read(vb + v_rd_off(D0, 1, 1));
;     const s16x4 l2 = tr_read(vb + v_rd_off(D0, 2, 0)), h2 = tr_read(vb + v_rd_off(D0, 2, 1)), l3 = tr_read(vb + v_rd_off(D0, 3, 0)), h3 = tr_read(vb + v_rd_off(D0, 3, 1));
;     ...
;     od = __builtin_amdgcn_mfma_f32_32x32x16_bf16(pa0, ATT_PK(l0, h0), od, 0, 0, 0);
;     od = __builtin_amdgcn_mfma_f32_32x32x16_bf16(pa1, ATT_PK(l1, h1), od, 0, 0, 0);
;     od = __builtin_amdgcn_mfma_f32_32x32x16_bf16(pa2, ATT_PK(l2, h2), od, 0, 0, 0);
;     od = __builtin_amdgcn_mfma_f32_32x32x16_bf16(pa3, ATT_PK(l3, h3), od, 0, 0, 0);
;     ...
; }
; __device__ __forceinline__ void pv_d0(f32x16* o, LAS const unsigned char* vb, bf16x8 pa0, bf16x8 pa1, bf16x8 pa2, bf16x8 pa3) {
;     pv_one<0>(o[0], vb, pa0, pa1, pa2, pa3); pv_one<1>(o[1], vb, pa0, pa1, pa2, pa3); pv_one<2>(o[2], vb, pa0, pa1, pa2, pa3); pv_one<3>(o[3], vb, pa0, pa1, pa2, pa3);
; }
	v_mfma_f32_32x32x16_bf16 v[36:51], v[148:151], v[112:115], v[36:51]
	s_waitcnt lgkmcnt(4)
	v_mfma_f32_32x32x16_bf16 v[36:51], v[68:71], v[116:119], v[36:51]
	s_waitcnt lgkmcnt(2)
	v_mfma_f32_32x32x16_bf16 v[36:51], v[72:75], v[120:123], v[36:51]
	s_waitcnt lgkmcnt(0)
	v_mfma_f32_32x32x16_bf16 v[36:51], v[108:111], v[124:127], v[36:51]
	ds_read_b64_tr_b16 v[112:113], v196 offset:1024
	ds_read_b64_tr_b16 v[114:115], v196 offset:3072
	ds_read_b64_tr_b16 v[116:117], v196 offset:5120
	ds_read_b64_tr_b16 v[118:119], v196 offset:7168
	ds_read_b64_tr_b16 v[120:121], v196 offset:9216
	ds_read_b64_tr_b16 v[122:123], v196 offset:11264
	ds_read_b64_tr_b16 v[124:125], v196 offset:13312
	ds_read_b64_tr_b16 v[126:127], v196 offset:15360
	s_waitcnt lgkmcnt(6)
	v_mfma_f32_32x32x16_bf16 v[20:35], v[148:151], v[112:115], v[20:35]
	s_waitcnt lgkmcnt(4)
	v_mfma_f32_32x32x16_bf16 v[20:35], v[68:71], v[116:119], v[20:35]
	s_waitcnt lgkmcnt(2)
	v_mfma_f32_32x32x16_bf16 v[20:35], v[72:75], v[120:123], v[20:35]
	s_waitcnt lgkmcnt(0)
	v_mfma_f32_32x32x16_bf16 v[20:35], v[108:111], v[124:127], v[20:35]
	ds_read_b64_tr_b16 v[112:113], v196 offset:1536
	ds_read_b64_tr_b16 v[114:115], v196 offset:3584
	ds_read_b64_tr_b16 v[116:117], v196 offset:5632
	ds_read_b64_tr_b16 v[118:119], v196 offset:7680
	ds_read_b64_tr_b16 v[120:121], v196 offset:9728
	ds_read_b64_tr_b16 v[122:123], v196 offset:11776
	ds_read_b64_tr_b16 v[124:125], v196 offset:13824
	ds_read_b64_tr_b16 v[126:127], v196 offset:15872
	s_waitcnt lgkmcnt(6)
	v_mfma_f32_32x32x16_bf16 v[4:19], v[148:151], v[112:115], v[4:19]
	s_waitcnt lgkmcnt(4)
	v_mfma_f32_32x32x16_bf16 v[4:19], v[68:71], v[116:119], v[4:19]
	v_or_b32_e32 v68, s0, v201
	s_or_b32 s0, s0, 63
	s_cmp_le_i32 s0, s13
	s_mov_b32 s0, 2.0
	s_mov_b32 s1, 0x40400000
	s_waitcnt lgkmcnt(2)
	v_mfma_f32_32x32x16_bf16 v[4:19], v[72:75], v[120:123], v[4:19]
	s_waitcnt lgkmcnt(0)
	v_mfma_f32_32x32x16_bf16 v[4:19], v[108:111], v[124:127], v[4:19]
	s_setprio 0
	v_sub_u32_e32 v108, v200, v68
	v_cvt_f32_i32_e32 v68, v108
	v_mul_f32_e64 v110, -v182, v68
	v_fma_f32 v112, v186, s0, v110
	v_fma_f32 v113, v187, s1, v110
	s_mov_b32 s0, 0x41000000
	s_mov_b32 s1, 0x41100000
	v_pk_fma_f32 v[114:115], v[186:187], s[0:1], v[110:111] op_sel_hi:[1,1,0]
	s_mov_b32 s0, 0x41200000
	s_mov_b32 s1, 0x41300000
	v_pk_fma_f32 v[116:117], v[186:187], s[0:1], v[110:111] op_sel_hi:[1,1,0]
	s_mov_b32 s0, 0x41800000
	s_mov_b32 s1, 0x41880000
	v_pk_fma_f32 v[118:119], v[186:187], s[0:1], v[110:111] op_sel_hi:[1,1,0]
	s_mov_b32 s0, 0x41900000
	v_fma_f32 v69, -v182, v68, v182
	v_mov_b32_e32 v68, v110
	s_mov_b32 s1, 0x41980000
	v_fmac_f32_e32 v68, 0, v182
	v_pk_fma_f32 v[74:75], v[186:187], s[0:1], v[110:111] op_sel_hi:[1,1,0]
	v_pk_fma_f32 v[72:73], v[186:187], s[86:87], v[110:111] op_sel_hi:[1,1,0]
	v_pk_fma_f32 v[70:71], v[186:187], s[88:89], v[110:111] op_sel_hi:[1,1,0]
	v_pk_fma_f32 v[68:69], v[92:93], s[96:97], v[68:69] op_sel_hi:[1,0,1]
	v_pk_fma_f32 v[70:71], v[106:107], s[96:97], v[70:71] op_sel_hi:[1,0,1]
	v_pk_fma_f32 v[72:73], v[104:105], s[96:97], v[72:73] op_sel_hi:[1,0,1]
	v_pk_fma_f32 v[74:75], v[102:103], s[96:97], v[74:75] op_sel_hi:[1,0,1]
	v_pk_fma_f32 v[92:93], v[100:101], s[96:97], v[118:119] op_sel_hi:[1,0,1]
	v_pk_fma_f32 v[98:99], v[98:99], s[96:97], v[116:117] op_sel_hi:[1,0,1]
	v_pk_fma_f32 v[96:97], v[96:97], s[96:97], v[114:115] op_sel_hi:[1,0,1]
	v_pk_fma_f32 v[94:95], v[94:95], s[96:97], v[112:113] op_sel_hi:[1,0,1]
	v_pk_fma_f32 v[100:101], v[182:183], s[90:91], v[110:111] op_sel_hi:[1,1,0]
	v_pk_fma_f32 v[102:103], v[182:183], s[92:93], v[110:111] op_sel_hi:[1,1,0]
	v_pk_fma_f32 v[104:105], v[182:183], s[94:95], v[110:111] op_sel_hi:[1,1,0]
	v_pk_fma_f32 v[106:107], v[182:183], s[68:69], v[110:111] op_sel_hi:[1,1,0]
	v_pk_fma_f32 v[112:113], v[182:183], s[70:71], v[110:111] op_sel_hi:[1,1,0]
	v_pk_fma_f32 v[114:115], v[182:183], s[72:73], v[110:111] op_sel_hi:[1,1,0]
	v_pk_fma_f32 v[116:117], v[182:183], s[74:75], v[110:111] op_sel_hi:[1,1,0]
	v_pk_fma_f32 v[110:111], v[184:185], s[76:77], v[110:111] op_sel_hi:[1,1,0]
	v_pk_fma_f32 v[90:91], v[90:91], s[96:97], v[116:117] op_sel_hi:[1,0,1]
	v_pk_fma_f32 v[88:89], v[88:89], s[96:97], v[114:115] op_sel_hi:[1,0,1]
	v_pk_fma_f32 v[86:87], v[86:87], s[96:97], v[112:113] op_sel_hi:[1,0,1]
	v_pk_fma_f32 v[84:85], v[84:85], s[96:97], v[106:107] op_sel_hi:[1,0,1]
	v_pk_fma_f32 v[82:83], v[82:83], s[96:97], v[104:105] op_sel_hi:[1,0,1]
	v_pk_fma_f32 v[80:81], v[80:81], s[96:97], v[102:103] op_sel_hi:[1,0,1]
	v_pk_fma_f32 v[78:79], v[78:79], s[96:97], v[100:101] op_sel_hi:[1,0,1]
	v_pk_fma_f32 v[76:77], v[76:77], s[96:97], v[110:111] op_sel_hi:[1,0,1]
	s_cbranch_scc1 .LBB0_661
; __device__ __forceinline__ void partialSM(f32x16& p0, f32x16& p1, float& m_reg, float& mn, float& alpha, int dq, float slopeL, bool diag, bool rowmasked) {
;     ...
;     for (int r = 0; r < 16; ++r) { const int c = (r & 3) + 8 * (r >> 2);
;         p0[r] = fmaf(p0[r], CS, fmaf(slopeL, (float)c, a0)); p1[r] = fmaf(p1[r], CS, fmaf(slopeL, (float)(c + 32), a0)); }
;     if (diag) { asm volatile("" ::: "memory");
; #pragma unroll
;         for (int r = 0; r < 16; ++r) { const int c = (r & 3) + 8 * (r >> 2); if (c > dq) p0[r] = NEG; if (c + 32 > dq) p1[r] = NEG; } }
	v_cmp_gt_i32_e64 s[64:65], 57, v108
	v_cmp_gt_i32_e64 s[66:67], 58, v108
	v_cmp_gt_i32_e64 s[62:63], 56, v108
	s_and_b64 s[64:65], s[66:67], s[64:65]
	v_cmp_gt_i32_e64 s[60:61], 51, v108
	s_and_b64 s[62:63], s[64:65], s[62:63]
	v_cmp_gt_i32_e64 s[58:59], 50, v108
	s_and_b64 s[60:61], s[62:63], s[60:61]
	v_cmp_gt_i32_e64 s[56:57], 49, v108
	s_and_b64 s[58:59], s[60:61], s[58:59]
	v_cmp_gt_i32_e64 s[54:55], 48, v108
	s_and_b64 s[56:57], s[58:59], s[56:57]
	v_cmp_gt_i32_e64 s[52:53], 43, v108
	s_and_b64 s[54:55], s[56:57], s[54:55]
	v_cmp_gt_i32_e64 s[50:51], 42, v108
	s_and_b64 s[52:53], s[54:55], s[52:53]
	v_cmp_gt_i32_e64 s[48:49], 41, v108
	s_and_b64 s[50:51], s[52:53], s[50:51]
	v_cmp_gt_i32_e64 s[46:47], 40, v108
	s_and_b64 s[48:49], s[50:51], s[48:49]
	v_cmp_gt_i32_e64 s[44:45], 35, v108
	s_and_b64 s[46:47], s[48:49], s[46:47]
	v_cmp_gt_i32_e64 s[42:43], 34, v108
	s_and_b64 s[44:45], s[46:47], s[44:45]
	v_cmp_gt_i32_e64 s[40:41], 33, v108
	s_and_b64 s[42:43], s[44:45], s[42:43]
	v_cmp_gt_i32_e64 s[38:39], 32, v108
	s_and_b64 s[40:41], s[42:43], s[40:41]
	s_and_b64 s[38:39], s[40:41], s[38:39]
	v_cmp_gt_i32_e32 vcc, 0, v108
	v_cmp_gt_i32_e64 s[0:1], 1, v108
	v_cmp_gt_i32_e64 s[8:9], 2, v108
	v_cmp_gt_i32_e64 s[10:11], 3, v108
	v_cmp_gt_i32_e64 s[14:15], 8, v108
	v_cmp_gt_i32_e64 s[16:17], 9, v108
	v_cmp_gt_i32_e64 s[18:19], 10, v108
	v_cmp_gt_i32_e64 s[20:21], 11, v108
	v_cmp_gt_i32_e64 s[22:23], 16, v108
	v_cmp_gt_i32_e64 s[24:25], 17, v108
	v_cmp_gt_i32_e64 s[26:27], 18, v108
	v_cmp_gt_i32_e64 s[28:29], 19, v108
	v_cmp_gt_i32_e64 s[30:31], 24, v108
	v_cmp_gt_i32_e64 s[34:35], 25, v108
	v_cmp_gt_i32_e64 s[36:37], 26, v108
	v_cndmask_b32_e64 v90, v90, v241, s[66:67]
	v_cndmask_b32_e64 v89, v89, v241, s[64:65]
	v_cndmask_b32_e64 v88, v88, v241, s[62:63]
	v_cndmask_b32_e64 v87, v87, v241, s[60:61]
	v_cndmask_b32_e64 v86, v86, v241, s[58:59]
	v_cndmask_b32_e64 v85, v85, v241, s[56:57]
	v_cndmask_b32_e64 v84, v84, v241, s[54:55]
	v_cndmask_b32_e64 v83, v83, v241, s[52:53]
	v_cndmask_b32_e64 v82, v82, v241, s[50:51]
	v_cndmask_b32_e64 v81, v81, v241, s[48:49]
	v_cndmask_b32_e64 v80, v80, v241, s[46:47]
	v_cndmask_b32_e64 v79, v79, v241, s[44:45]
	v_cndmask_b32_e64 v78, v78, v241, s[42:43]
	v_cndmask_b32_e64 v77, v77, v241, s[40:41]
	v_cndmask_b32_e64 v76, v76, v241, s[38:39]
	v_cmp_gt_i32_e64 s[38:39], 27, v108
	v_cmp_gt_i32_e64 s[40:41], 59, v108
	s_and_saveexec_b64 s[4:5], s[40:41]
	v_mov_b32_e32 v91, s12
	s_or_b64 exec, exec, s[4:5]
	s_and_b64 s[36:37], s[38:39], s[36:37]
	s_and_b64 s[34:35], s[36:37], s[34:35]
	s_and_b64 s[30:31], s[34:35], s[30:31]
	s_and_b64 s[28:29], s[30:31], s[28:29]
	s_and_b64 s[26:27], s[28:29], s[26:27]
	s_and_b64 s[24:25], s[26:27], s[24:25]
	s_and_b64 s[22:23], s[24:25], s[22:23]
	s_and_b64 s[20:21], s[22:23], s[20:21]
	s_and_b64 s[18:19], s[20:21], s[18:19]
	s_and_b64 s[16:17], s[18:19], s[16:17]
	s_and_b64 s[14:15], s[16:17], s[14:15]
	s_and_b64 s[10:11], s[14:15], s[10:11]
	s_and_b64 s[8:9], s[10:11], s[8:9]
	s_and_b64 s[0:1], s[8:9], s[0:1]
	s_and_b64 vcc, s[0:1], vcc
	v_cndmask_b32_e64 v70, v70, v241, s[36:37]
	v_cndmask_b32_e64 v73, v73, v241, s[34:35]
	v_cndmask_b32_e64 v72, v72, v241, s[30:31]
	v_cndmask_b32_e64 v75, v75, v241, s[28:29]
	v_cndmask_b32_e64 v74, v74, v241, s[26:27]
	v_cndmask_b32_e64 v93, v93, v241, s[24:25]
	v_cndmask_b32_e64 v92, v92, v241, s[22:23]
	v_cndmask_b32_e64 v99, v99, v241, s[20:21]
	v_cndmask_b32_e64 v98, v98, v241, s[18:19]
	v_cndmask_b32_e64 v97, v97, v241, s[16:17]
	v_cndmask_b32_e64 v96, v96, v241, s[14:15]
	v_cndmask_b32_e64 v95, v95, v241, s[10:11]
	v_cndmask_b32_e64 v94, v94, v241, s[8:9]
	v_cndmask_b32_e64 v69, v69, v241, s[0:1]
	v_cndmask_b32_e32 v68, v68, v241, vcc
	v_cndmask_b32_e64 v71, v71, v241, s[38:39]

; #define LAS __attribute__((address_space(3)))
; __device__ __forceinline__ s16x4 tr_read(LAS const unsigned char* p) { return __builtin_bit_cast(s16x4, __builtin_amdgcn_ds_read_tr16_b64_v4i16((LAS v4i16_t*)p)); }
; __device__ __forceinline__ void partialSM(f32x16& p0, f32x16& p1, float& m_reg, float& mn, float& alpha, int dq, float slopeL, bool diag, bool rowmasked) {
;     ...
;     for (int r = 0; r < 16; ++r) { p0[r] = p0[r] - mn; p1[r] = p1[r] - mn; }
; #pragma unroll
;     for (int r = 0; r < 16; ++r) p0[r] = __builtin_amdgcn_exp2f(p0[r]);
; }
; __device__ __forceinline__ void finishSM(f32x16& p0, f32x16& p1, float alpha, float& l_reg, bf16x8& pa0, bf16x8& pa1, bf16x8& pa2, bf16x8& pa3) {
; #pragma unroll
;     for (int r = 0; r < 16; ++r) p1[r] = __builtin_amdgcn_exp2f(p1[r]);
;     float ps = 0;
; #pragma unroll
;     for (int r = 0; r < 16; ++r) ps += p0[r];
; #pragma unroll
;     for (int r = 0; r < 16; ++r) ps += p1[r];
;     { auto rr = __builtin_amdgcn_permlane32_swap(__float_as_uint(ps), __float_as_uint(ps), false, false);
;       ps = __uint_as_float(rr[0]) + __uint_as_float(rr[1]); }
;     l_reg = l_reg * alpha + ps;
;     ...
;     ATT_PK4(p0, 0, pa0); ATT_PK4(p0, 8, pa1); ATT_PK4(p1, 0, pa2); ATT_PK4(p1, 8, pa3);
;     ...
; }
; template <int D0> __device__ __forceinline__ void pv_one(f32x16& od, LAS const unsigned char* vb, bf16x8 pa0, bf16x8 pa1, bf16x8 pa2, bf16x8 pa3) {
;     const s16x4 l0 = tr_read(vb + v_rd_off(D0, 0, 0)), h0 = tr_read(vb + v_rd_off(D0, 0, 1)), l1 = tr_read(vb + v_rd_off(D0, 1, 0)), h1 = tr_read(vb + v_rd_off(D0, 1, 1));
;     const s16x4 l2 = tr_read(vb + v_rd_off(D0, 2, 0)), h2 = tr_read(vb + v_rd_off(D0, 2, 1)), l3 = tr_read(vb + v_rd_off(D0, 3, 0)), h3 = tr_read(vb + v_rd_off(D0, 3, 1));
;     ...
;     od = __builtin_amdgcn_mfma_f32_32x32x16_bf16(pa0, ATT_PK(l0, h0), od, 0, 0, 0);
;     od = __builtin_amdgcn_mfma_f32_32x32x16_bf16(pa1, ATT_PK(l1, h1), od, 0, 0, 0);
;     od = __builtin_amdgcn_mfma_f32_32x32x16_bf16(pa2, ATT_PK(l2, h2), od, 0, 0, 0);
;     od = __builtin_amdgcn_mfma_f32_32x32x16_bf16(pa3, ATT_PK(l3, h3), od, 0, 0, 0);
;     ...
; }
; __device__ __forceinline__ void pv_d0(f32x16* o, LAS const unsigned char* vb, bf16x8 pa0, bf16x8 pa1, bf16x8 pa2, bf16x8 pa3) {
;     pv_one<0>(o[0], vb, pa0, pa1, pa2, pa3); pv_one<1>(o[1], vb, pa0, pa1, pa2, pa3); pv_one<2>(o[2], vb, pa0, pa1, pa2, pa3); pv_one<3>(o[3], vb, pa0, pa1, pa2, pa3);
; }
.LBB0_666:
	v_sub_f32_e32 v85, v106, v180
	v_sub_f32_e32 v86, v107, v180
	v_sub_f32_e32 v88, v95, v180
	v_exp_f32_e32 v95, v85
	v_sub_f32_e32 v87, v94, v180
	v_sub_f32_e32 v89, v96, v180
	v_exp_f32_e32 v96, v86
	v_sub_f32_e32 v90, v97, v180
	v_exp_f32_e32 v97, v87
	v_sub_f32_e32 v91, v98, v180
	v_exp_f32_e32 v98, v88
	v_sub_f32_e32 v68, v68, v180
	v_sub_f32_e32 v94, v99, v180
	v_exp_f32_e32 v99, v89
	v_exp_f32_e32 v115, v68
	v_add_f32_e32 v68, 0, v95
	v_sub_f32_e32 v107, v100, v180
	v_exp_f32_e32 v100, v90
	v_add_f32_e32 v68, v96, v68
	v_sub_f32_e32 v108, v101, v180
	v_exp_f32_e32 v101, v91
	v_add_f32_e32 v68, v97, v68
	v_sub_f32_e32 v92, v92, v180
	v_sub_f32_e32 v106, v102, v180
	v_exp_f32_e32 v102, v94
	v_add_f32_e32 v68, v98, v68
	v_sub_f32_e32 v93, v93, v180
	v_exp_f32_e32 v87, v92
	v_add_f32_e32 v68, v99, v68
	v_sub_f32_e32 v104, v104, v180
	v_exp_f32_e32 v88, v93
	v_add_f32_e32 v68, v100, v68
	v_sub_f32_e32 v105, v105, v180
	v_exp_f32_e32 v89, v104
	v_add_f32_e32 v68, v101, v68
	v_exp_f32_e32 v90, v105
	v_add_f32_e32 v68, v102, v68
	v_sub_f32_e32 v103, v103, v180
	v_exp_f32_e32 v91, v106
	v_add_f32_e32 v68, v87, v68
	v_exp_f32_e32 v92, v103
	v_add_f32_e32 v68, v88, v68
	v_exp_f32_e32 v93, v107
	v_add_f32_e32 v68, v89, v68
	v_exp_f32_e32 v94, v108
	v_sub_f32_e32 v76, v76, v180
	v_add_f32_e32 v68, v90, v68
	v_sub_f32_e32 v77, v77, v180
	v_exp_f32_e32 v103, v76
	v_add_f32_e32 v68, v91, v68
	v_sub_f32_e32 v78, v78, v180
	v_exp_f32_e32 v104, v77
	v_add_f32_e32 v68, v92, v68
	v_sub_f32_e32 v79, v79, v180
	v_exp_f32_e32 v105, v78
	v_add_f32_e32 v68, v93, v68
	v_sub_f32_e32 v80, v80, v180
	v_exp_f32_e32 v106, v79
	v_add_f32_e32 v68, v94, v68
	v_sub_f32_e32 v81, v81, v180
	v_exp_f32_e32 v107, v80
	v_add_f32_e32 v68, v103, v68
	v_sub_f32_e32 v82, v82, v180
	v_exp_f32_e32 v108, v81
	v_add_f32_e32 v68, v104, v68
	v_sub_f32_e32 v83, v83, v180
	v_exp_f32_e32 v109, v82
	v_add_f32_e32 v68, v105, v68
	v_sub_f32_e32 v74, v74, v180
	v_exp_f32_e32 v110, v83
	v_add_f32_e32 v68, v106, v68
	v_sub_f32_e32 v75, v75, v180
	v_exp_f32_e32 v111, v74
	v_add_f32_e32 v68, v107, v68
	v_sub_f32_e32 v72, v72, v180
	v_exp_f32_e32 v112, v75
	v_add_f32_e32 v68, v108, v68
	v_sub_f32_e32 v73, v73, v180
	v_exp_f32_e32 v113, v72
	v_add_f32_e32 v68, v109, v68
	v_sub_f32_e32 v70, v70, v180
	v_exp_f32_e32 v114, v73
	v_add_f32_e32 v68, v110, v68
	v_sub_f32_e32 v71, v71, v180
	v_exp_f32_e32 v70, v70
	v_add_f32_e32 v68, v111, v68
	v_exp_f32_e32 v71, v71
	v_add_f32_e32 v68, v112, v68
	v_sub_f32_e32 v69, v69, v180
	v_add_f32_e32 v68, v113, v68
	v_exp_f32_e32 v116, v69
	v_add_f32_e32 v68, v114, v68
	v_add_f32_e32 v68, v70, v68
	v_add_f32_e32 v68, v71, v68
	v_add_f32_e32 v68, v115, v68
	v_add_f32_e32 v85, v116, v68
	v_mov_b32_e32 v86, v85
	s_nop 1
	v_permlane32_swap_b32_e32 v85, v86
	v_cvt_pk_bf16_f32 v80, v95, v96
	v_cvt_pk_bf16_f32 v81, v97, v98
	v_cvt_pk_bf16_f32 v82, v99, v100
	v_cvt_pk_bf16_f32 v83, v101, v102
	v_cvt_pk_bf16_f32 v76, v87, v88
	v_cvt_pk_bf16_f32 v77, v89, v90
	v_cvt_pk_bf16_f32 v78, v91, v92
	v_cvt_pk_bf16_f32 v79, v93, v94
	v_cvt_pk_bf16_f32 v72, v103, v104
	v_cvt_pk_bf16_f32 v73, v105, v106
	v_cvt_pk_bf16_f32 v74, v107, v108
	v_cvt_pk_bf16_f32 v75, v109, v110
	v_cvt_pk_bf16_f32 v68, v111, v112
	v_cvt_pk_bf16_f32 v69, v113, v114
	v_cvt_pk_bf16_f32 v70, v70, v71
	v_cvt_pk_bf16_f32 v71, v115, v116
	v_permlane32_swap_b32_e32 v80, v82
	v_permlane32_swap_b32_e32 v81, v83
	v_permlane32_swap_b32_e32 v76, v78
	v_permlane32_swap_b32_e32 v77, v79
	v_permlane32_swap_b32_e32 v72, v74
	v_permlane32_swap_b32_e32 v73, v75
	v_permlane32_swap_b32_e32 v68, v70
	v_permlane32_swap_b32_e32 v69, v71
	ds_read_b64_tr_b16 v[88:89], v196 offset:16384
	ds_read_b64_tr_b16 v[90:91], v196 offset:18432
	s_waitcnt lgkmcnt(0)
	s_setprio 1
	v_mfma_f32_32x32x16_bf16 v[52:67], v[80:83], v[88:91], v[52:67]
	ds_read_b64_tr_b16 v[88:89], v196 offset:20480
	ds_read_b64_tr_b16 v[90:91], v196 offset:22528
	s_waitcnt lgkmcnt(0)
	v_mfma_f32_32x32x16_bf16 v[52:67], v[76:79], v[88:91], v[52:67]
	ds_read_b64_tr_b16 v[88:89], v196 offset:24576
	ds_read_b64_tr_b16 v[90:91], v196 offset:26624
	s_waitcnt lgkmcnt(0)
	v_mfma_f32_32x32x16_bf16 v[52:67], v[72:75], v[88:91], v[52:67]
	ds_read_b64_tr_b16 v[88:89], v196 offset:28672
	ds_read_b64_tr_b16 v[90:91], v196 offset:30720
	s_waitcnt lgkmcnt(0)
	v_mfma_f32_32x32x16_bf16 v[52:67], v[68:71], v[88:91], v[52:67]
	ds_read_b64_tr_b16 v[88:89], v196 offset:16896
	ds_read_b64_tr_b16 v[90:91], v196 offset:18944
	s_waitcnt lgkmcnt(0)
	v_mfma_f32_32x32x16_bf16 v[36:51], v[80:83], v[88:91], v[36:51]
	ds_read_b64_tr_b16 v[88:89], v196 offset:20992
	ds_read_b64_tr_b16 v[90:91], v196 offset:23040
	s_waitcnt lgkmcnt(0)
	v_mfma_f32_32x32x16_bf16 v[36:51], v[76:79], v[88:91], v[36:51]
	ds_read_b64_tr_b16 v[88:89], v196 offset:25088
	ds_read_b64_tr_b16 v[90:91], v196 offset:27136
	s_waitcnt lgkmcnt(0)
	v_mfma_f32_32x32x16_bf16 v[36:51], v[72:75], v[88:91], v[36:51]
	ds_read_b64_tr_b16 v[88:89], v196 offset:29184
	ds_read_b64_tr_b16 v[90:91], v196 offset:31232
	s_waitcnt lgkmcnt(0)
	v_mfma_f32_32x32x16_bf16 v[36:51], v[68:71], v[88:91], v[36:51]
	ds_read_b64_tr_b16 v[88:89], v196 offset:17408
	ds_read_b64_tr_b16 v[90:91], v196 offset:19456
	s_waitcnt lgkmcnt(0)
	v_mfma_f32_32x32x16_bf16 v[20:35], v[80:83], v[88:91], v[20:35]
	ds_read_b64_tr_b16 v[88:89], v196 offset:21504
	ds_read_b64_tr_b16 v[90:91], v196 offset:23552
	s_waitcnt lgkmcnt(0)
	v_mfma_f32_32x32x16_bf16 v[20:35], v[76:79], v[88:91], v[20:35]
	ds_read_b64_tr_b16 v[88:89], v196 offset:25600
	ds_read_b64_tr_b16 v[90:91], v196 offset:27648
	s_waitcnt lgkmcnt(0)
; __device__ __forceinline__ int crow(int r, int hi) { return (r & 3) + 8 * (r >> 2) + 4 * hi; }
; template <bool MOBA>
; __device__ __forceinline__ void run_unit(const UnitDesc& U, LAS unsigned char* lds, f32x16 (&o)[4], float (&rli)[16]) {
;     ...
;     if (hi == 0) li_l[r32] = l_reg;
;     asm volatile("s_waitcnt lgkmcnt(0)" ::: "memory");
; #pragma unroll
;     for (int r = 0; r < 16; ++r) rli[r] = 1.0f / li_l[crow(r, hi)];
;     __syncthreads();
; __global__ void __launch_bounds__(NWAVES * 64, 2) mega_fwd(Args args) {
;     ...
;                     { unsigned zz[64];
; #pragma unroll
;                       for (int r = 0; r < 16; ++r) { const int bt = b * SEQ + L * 256 + wave * 32 + att::crow(r, hi);
; #pragma unroll
;                           for (int d0 = 0; d0 < 4; ++d0) zz[r * 4 + d0] = *(const unsigned*)(PROJ + (size_t)bt * NC + C_ZA + h * 128 + d0 * 32 + (r32 & ~1)); }
	v_mfma_f32_32x32x16_bf16 v[20:35], v[72:75], v[88:91], v[20:35]
	ds_read_b64_tr_b16 v[88:89], v196 offset:29696
	ds_read_b64_tr_b16 v[90:91], v196 offset:31744
	s_waitcnt lgkmcnt(0)
	v_mfma_f32_32x32x16_bf16 v[20:35], v[68:71], v[88:91], v[20:35]
	ds_read_b64_tr_b16 v[88:89], v196 offset:17920
	ds_read_b64_tr_b16 v[90:91], v196 offset:19968
	s_waitcnt lgkmcnt(0)
	v_mfma_f32_32x32x16_bf16 v[4:19], v[80:83], v[88:91], v[4:19]
	ds_read_b64_tr_b16 v[80:81], v196 offset:22016
	ds_read_b64_tr_b16 v[82:83], v196 offset:24064
	s_waitcnt lgkmcnt(0)
	v_mfma_f32_32x32x16_bf16 v[4:19], v[76:79], v[80:83], v[4:19]
	ds_read_b64_tr_b16 v[76:77], v196 offset:26112
	ds_read_b64_tr_b16 v[78:79], v196 offset:28160
	s_waitcnt lgkmcnt(0)
	v_mfma_f32_32x32x16_bf16 v[4:19], v[72:75], v[76:79], v[4:19]
	ds_read_b64_tr_b16 v[72:73], v196 offset:30208
	ds_read_b64_tr_b16 v[74:75], v196 offset:32256
	s_waitcnt lgkmcnt(0)
	v_mfma_f32_32x32x16_bf16 v[4:19], v[68:71], v[72:75], v[4:19]
	s_setprio 0
	s_and_saveexec_b64 s[0:1], s[6:7]
	v_add_f32_e32 v1, v1, v2
	v_fmac_f32_e32 v1, v199, v222
	v_add_f32_e32 v2, v85, v86
	v_fmac_f32_e32 v2, v1, v84
	ds_write_b32 v198, v2
	s_or_b64 exec, exec, s[0:1]
	s_waitcnt lgkmcnt(0)
	ds_read_b128 v[80:83], v197
	ds_read_b128 v[76:79], v197 offset:32
	v_mov_b32_e32 v167, v219
	s_mov_b32 s4, 0xe800
	s_mov_b64 s[6:7], 0x1800
	s_waitcnt lgkmcnt(1)
	v_div_scale_f32 v1, s[0:1], v80, v80, 1.0
	v_rcp_f32_e32 v2, v1
	v_readlane_b32 s0, v254, 25
	v_readlane_b32 s1, v254, 50
	s_add_i32 s0, s1, s0
	v_fma_f32 v68, -v1, v2, 1.0
	v_fmac_f32_e32 v2, v68, v2
	v_div_scale_f32 v68, vcc, 1.0, v80, 1.0
	v_mul_f32_e32 v69, v68, v2
	v_fma_f32 v70, -v1, v69, v68
	v_fmac_f32_e32 v69, v70, v2
	v_fma_f32 v1, -v1, v69, v68
	v_div_fmas_f32 v1, v1, v2, v69
	v_div_fixup_f32 v111, v1, v80, 1.0
	ds_read_b128 v[72:75], v197 offset:64
	ds_read_b128 v[68:71], v197 offset:96
	s_waitcnt lgkmcnt(0)
	s_barrier
	s_movk_i32 s5, 0x1000
	v_ashrrev_i32_e32 v1, 3, v167
	v_and_b32_e32 v1, -4, v1
	v_add_u32_e32 v112, s0, v1
	v_readlane_b32 s0, v253, 48
	v_readlane_b32 s1, v253, 49
	v_and_b32_e32 v170, 30, v167
	v_lshlrev_b32_e32 v2, 1, v170
	v_mov_b64_e32 v[114:115], s[0:1]
	v_mad_i64_i32 v[84:85], s[0:1], v112, s4, v[114:115]
	v_lshl_add_u64 v[84:85], v[84:85], 0, s[2:3]
	v_lshl_add_u64 v[84:85], v[84:85], 0, v[2:3]
	v_lshl_add_u64 v[86:87], v[84:85], 0, s[6:7]
	v_add_co_u32_e32 v84, vcc, s5, v84
	v_or_b32_e32 v110, 1, v112
	s_nop 0
	v_addc_co_u32_e32 v85, vcc, 0, v85, vcc
	global_load_dword v166, v[84:85], off offset:2048
	global_load_dword v165, v[86:87], off offset:64
	global_load_dword v164, v[86:87], off offset:128
	global_load_dword v163, v[86:87], off offset:192
	v_mad_i64_i32 v[84:85], s[0:1], v110, s4, v[114:115]
	v_lshl_add_u64 v[84:85], v[84:85], 0, s[2:3]
	v_lshl_add_u64 v[84:85], v[84:85], 0, v[2:3]
	v_lshl_add_u64 v[86:87], v[84:85], 0, s[6:7]
	v_add_co_u32_e32 v84, vcc, s5, v84
	v_or_b32_e32 v108, 2, v112
	s_nop 0
	v_addc_co_u32_e32 v85, vcc, 0, v85, vcc
	global_load_dword v162, v[84:85], off offset:2048
	global_load_dword v161, v[86:87], off offset:64
	global_load_dword v160, v[86:87], off offset:128
	global_load_dword v109, v[86:87], off offset:192
	v_mad_i64_i32 v[84:85], s[0:1], v108, s4, v[114:115]
	v_lshl_add_u64 v[84:85], v[84:85], 0, s[2:3]
	v_lshl_add_u64 v[84:85], v[84:85], 0, v[2:3]
	v_lshl_add_u64 v[86:87], v[84:85], 0, s[6:7]
	v_add_co_u32_e32 v84, vcc, s5, v84
	v_or_b32_e32 v106, 3, v112
	s_nop 0
	v_addc_co_u32_e32 v85, vcc, 0, v85, vcc
	global_load_dword v159, v[84:85], off offset:2048
	global_load_dword v158, v[86:87], off offset:64
	global_load_dword v157, v[86:87], off offset:128
	global_load_dword v107, v[86:87], off offset:192
	v_mad_i64_i32 v[84:85], s[0:1], v106, s4, v[114:115]
	v_lshl_add_u64 v[84:85], v[84:85], 0, s[2:3]
	v_lshl_add_u64 v[84:85], v[84:85], 0, v[2:3]
	v_lshl_add_u64 v[86:87], v[84:85], 0, s[6:7]
	v_add_co_u32_e32 v84, vcc, s5, v84
	v_add_u32_e32 v104, 8, v112
	s_nop 0
	v_addc_co_u32_e32 v85, vcc, 0, v85, vcc
	global_load_dword v156, v[84:85], off offset:2048
	global_load_dword v155, v[86:87], off offset:64
	global_load_dword v154, v[86:87], off offset:128
	global_load_dword v105, v[86:87], off offset:192
	v_mad_i64_i32 v[84:85], s[0:1], v104, s4, v[114:115]
	v_lshl_add_u64 v[84:85], v[84:85], 0, s[2:3]
	v_lshl_add_u64 v[84:85], v[84:85], 0, v[2:3]
	v_lshl_add_u64 v[86:87], v[84:85], 0, s[6:7]
	v_add_co_u32_e32 v84, vcc, s5, v84
	v_add_u32_e32 v102, 9, v112
	s_nop 0
	v_addc_co_u32_e32 v85, vcc, 0, v85, vcc
	global_load_dword v153, v[84:85], off offset:2048
	global_load_dword v152, v[86:87], off offset:64
	global_load_dword v151, v[86:87], off offset:128
	global_load_dword v103, v[86:87], off offset:192
	v_mad_i64_i32 v[84:85], s[0:1], v102, s4, v[114:115]
	v_lshl_add_u64 v[84:85], v[84:85], 0, s[2:3]
	v_lshl_add_u64 v[84:85], v[84:85], 0, v[2:3]
	v_lshl_add_u64 v[86:87], v[84:85], 0, s[6:7]
	v_add_co_u32_e32 v84, vcc, s5, v84
	v_add_u32_e32 v100, 10, v112
	s_nop 0
	v_addc_co_u32_e32 v85, vcc, 0, v85, vcc
	global_load_dword v150, v[84:85], off offset:2048
	global_load_dword v149, v[86:87], off offset:64
	global_load_dword v148, v[86:87], off offset:128
	global_load_dword v101, v[86:87], off offset:192
	v_mad_i64_i32 v[84:85], s[0:1], v100, s4, v[114:115]
	v_lshl_add_u64 v[84:85], v[84:85], 0, s[2:3]
	v_lshl_add_u64 v[84:85], v[84:85], 0, v[2:3]
	v_lshl_add_u64 v[86:87], v[84:85], 0, s[6:7]
	v_add_co_u32_e32 v84, vcc, s5, v84
	v_add_u32_e32 v98, 11, v112
	s_nop 0
	v_addc_co_u32_e32 v85, vcc, 0, v85, vcc
	global_load_dword v147, v[84:85], off offset:2048
	global_load_dword v146, v[86:87], off offset:64
; __device__ __forceinline__ float bflo(unsigned w) { return __uint_as_float(w << 16); }
; __device__ __forceinline__ float bfhi(unsigned w) { return __uint_as_float(w & 0xffff0000u); }
; __device__ __forceinline__ unsigned pk2(float lo, float hi) { return f2bf(lo) | (f2bf(hi) << 16); }
; __device__ __forceinline__ int crow(int r, int hi) { return (r & 3) + 8 * (r >> 2) + 4 * hi; }
; __global__ void __launch_bounds__(NWAVES * 64, 2) mega_fwd(Args args) {
;     ...
;                     { unsigned zz[64];
; #pragma unroll
;                       for (int r = 0; r < 16; ++r) { const int bt = b * SEQ + L * 256 + wave * 32 + att::crow(r, hi);
; #pragma unroll
;                           for (int d0 = 0; d0 < 4; ++d0) zz[r * 4 + d0] = *(const unsigned*)(PROJ + (size_t)bt * NC + C_ZA + h * 128 + d0 * 32 + (r32 & ~1)); }
;                       asm volatile("" ::: "memory");
; #pragma unroll
;                       for (int r = 0; r < 16; ++r) { const int bt = b * SEQ + L * 256 + wave * 32 + att::crow(r, hi);
; #pragma unroll
;                           for (int d0 = 0; d0 < 4; ++d0) { const float val = o[d0][r] * rli[r], vn = __shfl_xor(val, 1); const int col = h * 128 + d0 * 32 + r32;
;                               if ((r32 & 1) == 0) *(unsigned*)(Y + (size_t)bt * YS + col) = pk2(val * bflo(zz[r * 4 + d0]), vn * bfhi(zz[r * 4 + d0])); } } }
	global_load_dword v145, v[86:87], off offset:128
	global_load_dword v99, v[86:87], off offset:192
	v_mad_i64_i32 v[84:85], s[0:1], v98, s4, v[114:115]
	v_lshl_add_u64 v[84:85], v[84:85], 0, s[2:3]
	v_lshl_add_u64 v[84:85], v[84:85], 0, v[2:3]
	v_lshl_add_u64 v[86:87], v[84:85], 0, s[6:7]
	v_add_co_u32_e32 v84, vcc, s5, v84
	v_add_u32_e32 v96, 16, v112
	s_nop 0
	v_addc_co_u32_e32 v85, vcc, 0, v85, vcc
	global_load_dword v144, v[84:85], off offset:2048
	global_load_dword v143, v[86:87], off offset:64
	global_load_dword v142, v[86:87], off offset:128
	global_load_dword v97, v[86:87], off offset:192
	v_mad_i64_i32 v[84:85], s[0:1], v96, s4, v[114:115]
	v_lshl_add_u64 v[84:85], v[84:85], 0, s[2:3]
	v_lshl_add_u64 v[84:85], v[84:85], 0, v[2:3]
	v_lshl_add_u64 v[86:87], v[84:85], 0, s[6:7]
	v_add_co_u32_e32 v84, vcc, s5, v84
	v_add_u32_e32 v94, 17, v112
	s_nop 0
	v_addc_co_u32_e32 v85, vcc, 0, v85, vcc
	global_load_dword v141, v[84:85], off offset:2048
	global_load_dword v140, v[86:87], off offset:64
	global_load_dword v139, v[86:87], off offset:128
	global_load_dword v95, v[86:87], off offset:192
	v_mad_i64_i32 v[84:85], s[0:1], v94, s4, v[114:115]
	v_lshl_add_u64 v[84:85], v[84:85], 0, s[2:3]
	v_lshl_add_u64 v[84:85], v[84:85], 0, v[2:3]
	v_lshl_add_u64 v[86:87], v[84:85], 0, s[6:7]
	v_add_co_u32_e32 v84, vcc, s5, v84
	v_add_u32_e32 v92, 18, v112
	s_nop 0
	v_addc_co_u32_e32 v85, vcc, 0, v85, vcc
	global_load_dword v138, v[84:85], off offset:2048
	global_load_dword v137, v[86:87], off offset:64
	global_load_dword v136, v[86:87], off offset:128
	global_load_dword v93, v[86:87], off offset:192
	v_mad_i64_i32 v[84:85], s[0:1], v92, s4, v[114:115]
	v_lshl_add_u64 v[84:85], v[84:85], 0, s[2:3]
	v_lshl_add_u64 v[84:85], v[84:85], 0, v[2:3]
	v_lshl_add_u64 v[86:87], v[84:85], 0, s[6:7]
	v_add_co_u32_e32 v84, vcc, s5, v84
	v_add_u32_e32 v90, 19, v112
	s_nop 0
	v_addc_co_u32_e32 v85, vcc, 0, v85, vcc
	global_load_dword v135, v[84:85], off offset:2048
	global_load_dword v134, v[86:87], off offset:64
	global_load_dword v133, v[86:87], off offset:128
	global_load_dword v91, v[86:87], off offset:192
	v_mad_i64_i32 v[84:85], s[0:1], v90, s4, v[114:115]
	v_lshl_add_u64 v[84:85], v[84:85], 0, s[2:3]
	v_lshl_add_u64 v[84:85], v[84:85], 0, v[2:3]
	v_lshl_add_u64 v[86:87], v[84:85], 0, s[6:7]
	v_add_co_u32_e32 v84, vcc, s5, v84
	v_add_u32_e32 v88, 24, v112
	s_nop 0
	v_addc_co_u32_e32 v85, vcc, 0, v85, vcc
	global_load_dword v132, v[84:85], off offset:2048
	global_load_dword v131, v[86:87], off offset:64
	global_load_dword v130, v[86:87], off offset:128
	global_load_dword v89, v[86:87], off offset:192
	v_mad_i64_i32 v[84:85], s[0:1], v88, s4, v[114:115]
	v_lshl_add_u64 v[84:85], v[84:85], 0, s[2:3]
	v_lshl_add_u64 v[84:85], v[84:85], 0, v[2:3]
	v_lshl_add_u64 v[86:87], v[84:85], 0, s[6:7]
	v_add_co_u32_e32 v84, vcc, s5, v84
	v_add_u32_e32 v80, 27, v112
	s_nop 0
	v_addc_co_u32_e32 v85, vcc, 0, v85, vcc
	global_load_dword v129, v[84:85], off offset:2048
	global_load_dword v128, v[86:87], off offset:64
	global_load_dword v127, v[86:87], off offset:128
	s_nop 0
	global_load_dword v87, v[86:87], off offset:192
	v_add_u32_e32 v86, 25, v112
	v_mad_i64_i32 v[84:85], s[0:1], v86, s4, v[114:115]
	v_lshl_add_u64 v[84:85], v[84:85], 0, s[2:3]
	v_lshl_add_u64 v[84:85], v[84:85], 0, v[2:3]
	v_lshl_add_u64 v[116:117], v[84:85], 0, s[6:7]
	v_add_co_u32_e32 v84, vcc, s5, v84
	v_ashrrev_i32_e32 v113, 31, v112
	s_nop 0
	v_addc_co_u32_e32 v85, vcc, 0, v85, vcc
	global_load_dword v126, v[84:85], off offset:2048
	global_load_dword v125, v[116:117], off offset:64
	global_load_dword v124, v[116:117], off offset:128
	s_nop 0
	global_load_dword v85, v[116:117], off offset:192
	v_add_u32_e32 v84, 26, v112
	v_mad_i64_i32 v[116:117], s[0:1], v84, s4, v[114:115]
	v_lshl_add_u64 v[116:117], v[116:117], 0, s[2:3]
	v_lshl_add_u64 v[116:117], v[116:117], 0, v[2:3]
	v_mad_i64_i32 v[114:115], s[0:1], v80, s4, v[114:115]
	v_lshl_add_u64 v[118:119], v[116:117], 0, s[6:7]
	v_add_co_u32_e32 v116, vcc, s5, v116
	v_lshl_add_u64 v[114:115], v[114:115], 0, s[2:3]
	s_nop 0
	v_addc_co_u32_e32 v117, vcc, 0, v117, vcc
	v_lshl_add_u64 v[114:115], v[114:115], 0, v[2:3]
	v_lshl_add_u64 v[168:169], v[114:115], 0, s[6:7]
	v_add_co_u32_e32 v114, vcc, s5, v114
	global_load_dword v123, v[116:117], off offset:2048
	global_load_dword v122, v[118:119], off offset:64
	global_load_dword v121, v[118:119], off offset:128
	global_load_dword v120, v[118:119], off offset:192
	v_addc_co_u32_e32 v115, vcc, 0, v115, vcc
	global_load_dword v119, v[114:115], off offset:2048
	global_load_dword v117, v[168:169], off offset:64
	global_load_dword v116, v[168:169], off offset:128
	global_load_dword v1, v[168:169], off offset:192
	v_and_b32_e32 v114, 64, v229
	v_xor_b32_e32 v2, 1, v229
	v_add_u32_e32 v114, 64, v114
	v_cmp_lt_i32_e32 vcc, v2, v114
	v_mul_f32_e32 v115, v111, v52
	v_readlane_b32 s2, v254, 51
	v_cndmask_b32_e32 v2, v229, v2, vcc
	v_lshlrev_b32_e32 v118, 2, v2
	ds_bpermute_b32 v114, v118, v115
	v_and_b32_e32 v2, 1, v167
	v_readlane_b32 s4, v253, 57
	v_cmp_eq_u32_e64 s[0:1], 0, v2
	v_or_b32_e32 v2, s2, v170
	v_lshlrev_b64 v[112:113], 13, v[112:113]
	v_readlane_b32 s5, v253, 58
	v_lshlrev_b32_e32 v2, 1, v2
	s_nop 0
	v_lshl_add_u64 v[112:113], s[4:5], 0, v[112:113]
	s_and_saveexec_b64 s[4:5], s[0:1]
	s_cbranch_execz .LBB0_670
	s_waitcnt vmcnt(62)
	v_lshlrev_b32_e32 v167, 16, v166
	v_and_b32_e32 v166, 0xffff0000, v166
	s_waitcnt lgkmcnt(0)
	v_pk_mul_f32 v[114:115], v[114:115], v[166:167]
	s_nop 0
	v_and_b32_sdwa v52, v115, v227 dst_sel:DWORD dst_unused:UNUSED_PAD src0_sel:WORD_1 src1_sel:DWORD
	v_and_b32_sdwa v166, v114, v227 dst_sel:DWORD dst_unused:UNUSED_PAD src0_sel:WORD_1 src1_sel:DWORD
	v_add3_u32 v52, v115, v52, s97
	v_add3_u32 v114, v114, v166, s97
	v_lshrrev_b32_e32 v52, 16, v52
	v_and_or_b32 v52, v114, s8, v52
	v_lshl_add_u64 v[114:115], v[112:113], 0, v[2:3]
	global_store_dword v[114:115], v52, off

; #define LAS __attribute__((address_space(3)))
; __device__ __forceinline__ int v_st(int k, int c) { const int kk = (k & ~0xC) | ((k & 4) << 1) | ((k & 8) >> 1); return ((kk >> 3) * 4 + (c >> 5)) * 512 + ((kk & 7) * 32 + (c & 31)) * 2; }
; __device__ __forceinline__ int v_rd_base(int lane) { return ((lane & 3) << 3) | (((lane >> 2) & 3) << 6) | (((lane >> 4) & 1) << 5) | (((lane >> 5) & 1) << 8); }
; #define ATT_SLOAD(S, k0) do { S##_v0 = *(const bf16x8*)(Vh + (size_t)(k0) * NC); S##_v1 = *(const bf16x8*)(Vh + (size_t)((k0) + 32) * NC); \
;     S##_k0 = *(const bf16x8*)(Kh + (size_t)(k0) * NC); S##_k1 = *(const bf16x8*)(Kh + (size_t)((k0) + 32) * NC); } while (0)
; #define ATT_SWRITE(b, S) do { *(LAS bf16x8*)(V_lds + (b) * SHM_V + vst0) = S##_v0; *(LAS bf16x8*)(V_lds + (b) * SHM_V + vst1) = S##_v1; \
;     *(LAS bf16x8*)(K_lds + (b) * SHM_K + kst0) = S##_k0; *(LAS bf16x8*)(K_lds + (b) * SHM_K + kst1) = S##_k1; } while (0)
; #define ATT_SWAIT() asm volatile("s_waitcnt vmcnt(4)" ::: "memory")
; #define ATT_PSM(P0, P1, MN, AL, t) partialSM(P0, P1, m_reg, MN, AL, qpos - (t) * KVBLK - 4 * hi, U.slopeL, (t) * KVBLK + KVBLK - 1 > qlo, MOBA && ((t) >> 2) < U.moba_j && !((sel >> ((t) >> 2)) & 1u))
; template <bool MOBA>
; __device__ __forceinline__ void run_unit(const UnitDesc& U, LAS unsigned char* lds, f32x16 (&o)[4], float (&rli)[16]) {
;     ...
;     const int sr = tid >> 4, sc = (tid & 15) * 8, vst0 = v_st(sr, sc), vst1 = v_st(32 + sr, sc), kst0 = ATT_KSWZ(sr, sc * 2), kst1 = ATT_KSWZ(32 + sr, sc * 2);
;     LAS const unsigned char* vb0 = V_lds + v_rd_base(lane);
;     const bf16_t* Kh = U.K + (size_t)(sr + kt0 * KVBLK) * NC + sc; const bf16_t* Vh = U.V + (size_t)(sr + kt0 * KVBLK) * NC + sc;
;     qpos -= kt0 * KVBLK; qlo -= kt0 * KVBLK;
;     bf16x8 sA_v0, sA_v1, sA_k0, sA_k1, sB_v0, sB_v1, sB_k0, sB_k1;
;     ...
;     f32x16 pA0, pA1, pB0, pB1; float mnA, mnB, alA, alB; bf16x8 pa0, pa1, pa2, pa3; const int NT = U.nt - kt0;
;     ATT_SLOAD(sA, 0); ATT_SLOAD(sB, KVBLK); ATT_SWAIT(); ATT_SWRITE(0, sA); __syncthreads();
;     qkt(pA0, pA1, K_lds, qr, r32, hi); ATT_PSM(pA0, pA1, mnA, alA, 0);
.LBB0_814:
	v_ashrrev_i32_e32 v5, 4, v8
	v_and_b32_e32 v7, 0xfffff0, v5
	v_lshlrev_b32_e32 v10, 1, v5
	v_lshlrev_b32_e32 v4, 3, v8
	v_and_or_b32 v7, v10, 8, v7
	v_lshrrev_b32_e32 v7, 1, v7
	v_bfe_u32 v11, v4, 5, 2
	v_and_b32_e32 v6, 0x78, v4
	v_or_b32_e32 v4, v7, v11
	v_lshrrev_b32_e32 v10, 1, v5
	v_lshlrev_b32_e32 v7, 9, v4
	v_and_b32_e32 v4, 3, v5
	v_and_or_b32 v4, v10, 4, v4
	v_lshlrev_b32_e32 v10, 6, v4
	v_lshlrev_b32_e32 v4, 1, v6
	v_and_b32_e32 v6, 48, v4
	v_or3_b32 v22, v7, v10, v6
	v_add_u32_e32 v7, 32, v5
	v_readlane_b32 s0, v254, 59
	v_and_b32_e32 v12, 0xfffff0, v7
	v_lshlrev_b32_e32 v13, 1, v7
	s_add_i32 s8, s66, s0
	s_lshl_b32 s0, s12, 1
	v_readlane_b32 s1, v254, 52
	v_and_or_b32 v12, v13, 8, v12
	s_add_u32 s0, s1, s0
	v_readlane_b32 s1, v254, 53
	v_lshrrev_b32_e32 v12, 1, v12
	s_addc_u32 s1, s1, 0
	s_lshl_b32 s6, s80, 7
	v_or_b32_e32 v11, v12, v11
	s_and_b32 s6, s6, 0x100
	v_readlane_b32 s7, v254, 54
	v_lshlrev_b32_e32 v11, 9, v11
	s_add_u32 s6, s7, s6
	v_readlane_b32 s7, v254, 55
	v_or3_b32 v23, v11, v10, v6
	v_lshlrev_b32_e32 v6, 8, v5
	v_and_b32_e32 v8, 0xf0, v8
	s_addc_u32 s7, s7, 0
	v_bitop3_b32 v24, v4, v6, v8 bitop3:0xde
	v_lshlrev_b32_e32 v6, 8, v7
	s_lshl_b32 s83, s82, 6
	v_bitop3_b32 v25, v4, v6, v8 bitop3:0xde
	v_add_u32_e32 v8, s83, v5
	v_mov_b64_e32 v[6:7], s[0:1]
	s_mov_b32 s9, 0xe800
	v_mad_i64_i32 v[6:7], s[0:1], v8, s9, v[6:7]
	v_mov_b32_e32 v5, v3
	v_lshl_add_u64 v[182:183], v[6:7], 0, v[4:5]
	v_mov_b64_e32 v[6:7], s[6:7]
	v_mad_i64_i32 v[6:7], s[0:1], v8, s9, v[6:7]
	v_lshl_add_u64 v[184:185], v[6:7], 0, v[4:5]
	s_mov_b32 s0, 0x1d0000
	v_add_co_u32_e32 v4, vcc, s0, v184
	v_or_b32_e32 v9, s8, v52
	s_nop 0
	v_addc_co_u32_e32 v5, vcc, 0, v185, vcc
	v_subrev_u32_e32 v190, s83, v9
	global_load_dwordx4 v[8:11], v[184:185], off
	global_load_dwordx4 v[12:15], v[4:5], off
	global_load_dwordx4 v[16:19], v[182:183], off
	v_add_co_u32_e32 v4, vcc, s0, v182
	s_mov_b32 s0, 0x3a0000
	s_nop 0
	v_addc_co_u32_e32 v5, vcc, 0, v183, vcc
	global_load_dwordx4 v[4:7], v[4:5], off
	v_add_co_u32_e32 v20, vcc, s0, v184
	s_mov_b32 s1, 0x570000
	s_nop 0
	v_addc_co_u32_e32 v21, vcc, 0, v185, vcc
	global_load_dwordx4 v[44:47], v[20:21], off
	v_add_co_u32_e32 v20, vcc, s1, v184
	v_add_u32_e32 v214, 0, v22
	s_nop 0
	v_addc_co_u32_e32 v21, vcc, 0, v185, vcc
	global_load_dwordx4 v[48:51], v[20:21], off
	v_add_co_u32_e32 v20, vcc, s0, v182
	v_add_u32_e32 v215, 0, v23
	s_nop 0
	v_addc_co_u32_e32 v21, vcc, 0, v183, vcc
	global_load_dwordx4 v[36:39], v[20:21], off
	v_add_co_u32_e32 v20, vcc, s1, v182
	v_add_u32_e32 v216, 0, v24
	s_nop 0
	v_addc_co_u32_e32 v21, vcc, 0, v183, vcc
	global_load_dwordx4 v[40:43], v[20:21], off
	v_add_u32_e32 v217, 0, v25
	s_waitcnt vmcnt(4)
	s_movk_i32 s0, 0xf0
	v_lshl_add_u32 v62, v52, 8, 0
	v_lshlrev_b32_e32 v202, 2, v1
	v_sub_u32_e32 v1, v190, v202
	v_mov_b32_e32 v197, v196
	s_sub_i32 s81, s8, s83
	s_cmp_gt_i32 s81, 62
	s_waitcnt vmcnt(7)
	ds_write_b128 v214, v[8:11]
	s_waitcnt vmcnt(6)
	ds_write_b128 v215, v[12:15]
	s_waitcnt vmcnt(5)
	ds_write_b128 v216, v[16:19] offset:32768
	s_waitcnt vmcnt(4)
	ds_write_b128 v217, v[4:7] offset:32768
	v_lshlrev_b32_e32 v4, 4, v52
	v_and_b32_e32 v53, 0xf0, v4
	v_bitop3_b32 v4, v2, v4, s0 bitop3:0x78
	v_add_u32_e32 v206, v62, v4
	s_waitcnt lgkmcnt(0)
	s_barrier
	ds_read_b128 v[4:7], v206 offset:32768
	ds_read_b128 v[8:11], v206 offset:40960
	s_waitcnt lgkmcnt(1)
	s_setprio 1
	v_mfma_f32_32x32x16_bf16 v[20:35], v[4:7], v[142:145], 0
	v_bitop3_b32 v54, v2, v53, 32 bitop3:0x36
	v_add_u32_e32 v208, v62, v54
	ds_read_b128 v[54:57], v208 offset:32768
	ds_read_b128 v[58:61], v208 offset:40960
	s_movk_i32 s0, 0x60
	s_waitcnt lgkmcnt(2)
	v_mfma_f32_32x32x16_bf16 v[4:19], v[8:11], v[142:145], 0
	s_waitcnt lgkmcnt(1)
	v_mfma_f32_32x32x16_bf16 v[20:35], v[54:57], v[138:141], v[20:35]
	v_bitop3_b32 v54, v2, v53, 64 bitop3:0x36
	v_add_u32_e32 v204, v62, v54
	s_waitcnt lgkmcnt(0)
	v_mfma_f32_32x32x16_bf16 v[4:19], v[58:61], v[138:141], v[4:19]
	ds_read_b128 v[54:57], v204 offset:32768
	ds_read_b128 v[58:61], v204 offset:40960
	s_waitcnt lgkmcnt(1)
	v_mfma_f32_32x32x16_bf16 v[20:35], v[54:57], v[134:137], v[20:35]
	v_bitop3_b32 v54, v2, v53, s0 bitop3:0x36
	v_add_u32_e32 v209, v62, v54
	s_movk_i32 s0, 0x80
	s_waitcnt lgkmcnt(0)
	v_mfma_f32_32x32x16_bf16 v[4:19], v[58:61], v[134:137], v[4:19]
	ds_read_b128 v[54:57], v209 offset:32768
	ds_read_b128 v[58:61], v209 offset:40960
	s_waitcnt lgkmcnt(1)
	v_mfma_f32_32x32x16_bf16 v[20:35], v[54:57], v[130:133], v[20:35]
	v_bitop3_b32 v54, v2, v53, s0 bitop3:0x36
	v_add_u32_e32 v210, v62, v54
	s_movk_i32 s0, 0xa0
	s_waitcnt lgkmcnt(0)
	v_mfma_f32_32x32x16_bf16 v[4:19], v[58:61], v[130:133], v[4:19]
	ds_read_b128 v[54:57], v210 offset:32768
	ds_read_b128 v[58:61], v210 offset:40960
	s_waitcnt lgkmcnt(1)
	v_mfma_f32_32x32x16_bf16 v[20:35], v[54:57], v[126:129], v[20:35]
	v_bitop3_b32 v54, v2, v53, s0 bitop3:0x36
	v_add_u32_e32 v211, v62, v54
	s_movk_i32 s0, 0xc0
	s_waitcnt lgkmcnt(0)
	v_mfma_f32_32x32x16_bf16 v[4:19], v[58:61], v[126:129], v[4:19]
	ds_read_b128 v[54:57], v211 offset:32768
	ds_read_b128 v[58:61], v211 offset:40960
	s_waitcnt lgkmcnt(1)
	v_mfma_f32_32x32x16_bf16 v[20:35], v[54:57], v[122:125], v[20:35]
	v_bitop3_b32 v54, v2, v53, s0 bitop3:0x36
	v_add_u32_e32 v212, v62, v54
	s_movk_i32 s0, 0xe0
	v_bitop3_b32 v2, v2, v53, s0 bitop3:0x36
	v_add_u32_e32 v213, v62, v2
	v_cvt_f32_i32_e32 v53, v1
	s_mov_b32 s0, 2.0
	s_waitcnt lgkmcnt(0)
	v_mfma_f32_32x32x16_bf16 v[4:19], v[58:61], v[122:125], v[4:19]
	ds_read_b128 v[54:57], v212 offset:32768
	ds_read_b128 v[58:61], v212 offset:40960
	v_mul_f32_e64 v2, -v196, v53
	s_mov_b32 s1, 0x40400000
	v_fma_f32 v66, v198, s86, v2
	v_fma_f32 v67, v199, s87, v2
	v_pk_fma_f32 v[68:69], v[198:199], s[88:89], v[2:3] op_sel_hi:[1,1,0]
	s_waitcnt lgkmcnt(1)
; #define LAS __attribute__((address_space(3)))
; __device__ __forceinline__ void qkt(f32x16& p0, f32x16& p1, LAS const unsigned char* Ks, const bf16x8* qr, int r32, int hi) {
;     p0 = f32x16{}; p1 = f32x16{};
; #pragma unroll
;     for (int d0 = 0; d0 < 8; ++d0) { const int cb = (d0 * 16 + hi * 8) * 2;
;         const bf16x8 b0 = *(LAS const bf16x8*)(Ks + ATT_KSWZ(r32, cb));
;         const bf16x8 b1 = *(LAS const bf16x8*)(Ks + ATT_KSWZ(32 + r32, cb));
;         p0 = __builtin_amdgcn_mfma_f32_32x32x16_bf16(b0, qr[d0], p0, 0, 0, 0);
;         p1 = __builtin_amdgcn_mfma_f32_32x32x16_bf16(b1, qr[d0], p1, 0, 0, 0); }
; }
; __device__ __forceinline__ void partialSM(f32x16& p0, f32x16& p1, float& m_reg, float& mn, float& alpha, int dq, float slopeL, bool diag, bool rowmasked) {
;     const float NEG = -__builtin_inff(); const float a0 = -slopeL * (float)dq;
; #pragma unroll
;     for (int r = 0; r < 16; ++r) { const int c = (r & 3) + 8 * (r >> 2);
;         p0[r] = fmaf(p0[r], CS, fmaf(slopeL, (float)c, a0)); p1[r] = fmaf(p1[r], CS, fmaf(slopeL, (float)(c + 32), a0)); }
;     if (diag) { asm volatile("" ::: "memory");
; #pragma unroll
;         for (int r = 0; r < 16; ++r) { const int c = (r & 3) + 8 * (r >> 2); if (c > dq) p0[r] = NEG; if (c + 32 > dq) p1[r] = NEG; } }
	v_mfma_f32_32x32x16_bf16 v[20:35], v[54:57], v[118:121], v[20:35]
	s_waitcnt lgkmcnt(0)
	v_mfma_f32_32x32x16_bf16 v[4:19], v[58:61], v[118:121], v[4:19]
	ds_read_b128 v[54:57], v213 offset:32768
	ds_read_b128 v[58:61], v213 offset:40960
	s_waitcnt lgkmcnt(1)
	v_mfma_f32_32x32x16_bf16 v[20:35], v[54:57], v[114:117], v[20:35]
	v_fma_f32 v56, v198, s0, v2
	v_fma_f32 v57, v199, s1, v2
	s_mov_b32 s0, 0x41000000
	s_mov_b32 s1, 0x41100000
	v_mov_b32_e32 v54, v2
	v_fma_f32 v55, -v196, v53, v196
	v_fmac_f32_e32 v54, 0, v196
	s_nop 4
	v_pk_fma_f32 v[34:35], v[34:35], s[96:97], v[68:69] op_sel_hi:[1,0,1]
	s_waitcnt lgkmcnt(0)
	v_mfma_f32_32x32x16_bf16 v[4:19], v[58:61], v[114:117], v[4:19]
	s_setprio 0
	v_fma_f32 v58, v198, s0, v2
	v_fma_f32 v59, v199, s1, v2
	s_mov_b32 s0, 0x41200000
	s_mov_b32 s1, 0x41300000
	v_fma_f32 v60, v198, s0, v2
	v_fma_f32 v61, v199, s1, v2
	s_mov_b32 s0, 0x41800000
	s_mov_b32 s1, 0x41880000
	v_pk_fma_f32 v[62:63], v[198:199], s[0:1], v[2:3] op_sel_hi:[1,1,0]
	s_mov_b32 s0, 0x41900000
	s_mov_b32 s1, 0x41980000
	v_pk_fma_f32 v[64:65], v[198:199], s[0:1], v[2:3] op_sel_hi:[1,1,0]
	v_pk_fma_f32 v[32:33], v[32:33], s[96:97], v[66:67] op_sel_hi:[1,0,1]
	v_pk_fma_f32 v[30:31], v[30:31], s[96:97], v[64:65] op_sel_hi:[1,0,1]
	v_pk_fma_f32 v[28:29], v[28:29], s[96:97], v[62:63] op_sel_hi:[1,0,1]
	v_pk_fma_f32 v[26:27], v[26:27], s[96:97], v[60:61] op_sel_hi:[1,0,1]
	v_pk_fma_f32 v[24:25], v[24:25], s[96:97], v[58:59] op_sel_hi:[1,0,1]
	v_pk_fma_f32 v[22:23], v[22:23], s[96:97], v[56:57] op_sel_hi:[1,0,1]
	v_pk_fma_f32 v[20:21], v[20:21], s[96:97], v[54:55] op_sel_hi:[1,0,1]
	v_pk_fma_f32 v[54:55], v[200:201], s[76:77], v[2:3] op_sel_hi:[1,1,0]
	v_pk_fma_f32 v[56:57], v[196:197], s[90:91], v[2:3] op_sel_hi:[1,1,0]
	v_pk_fma_f32 v[58:59], v[196:197], s[92:93], v[2:3] op_sel_hi:[1,1,0]
	v_pk_fma_f32 v[60:61], v[196:197], s[94:95], v[2:3] op_sel_hi:[1,1,0]
	v_pk_fma_f32 v[62:63], v[196:197], s[68:69], v[2:3] op_sel_hi:[1,1,0]
	v_pk_fma_f32 v[64:65], v[196:197], s[70:71], v[2:3] op_sel_hi:[1,1,0]
	v_pk_fma_f32 v[66:67], v[196:197], s[72:73], v[2:3] op_sel_hi:[1,1,0]
	v_pk_fma_f32 v[68:69], v[196:197], s[74:75], v[2:3] op_sel_hi:[1,1,0]
	v_pk_fma_f32 v[16:17], v[16:17], s[96:97], v[66:67] op_sel_hi:[1,0,1]
	v_pk_fma_f32 v[18:19], v[18:19], s[96:97], v[68:69] op_sel_hi:[1,0,1]
	v_pk_fma_f32 v[14:15], v[14:15], s[96:97], v[64:65] op_sel_hi:[1,0,1]
	v_pk_fma_f32 v[12:13], v[12:13], s[96:97], v[62:63] op_sel_hi:[1,0,1]
	v_pk_fma_f32 v[10:11], v[10:11], s[96:97], v[60:61] op_sel_hi:[1,0,1]
	v_pk_fma_f32 v[8:9], v[8:9], s[96:97], v[58:59] op_sel_hi:[1,0,1]
	v_pk_fma_f32 v[6:7], v[6:7], s[96:97], v[56:57] op_sel_hi:[1,0,1]
	v_pk_fma_f32 v[4:5], v[4:5], s[96:97], v[54:55] op_sel_hi:[1,0,1]
	s_cbranch_scc1 .LBB0_818
	v_cmp_gt_i32_e64 s[62:63], 57, v1
	v_cmp_gt_i32_e64 s[64:65], 58, v1
	v_cmp_gt_i32_e64 s[60:61], 56, v1
	s_and_b64 s[62:63], s[64:65], s[62:63]
	v_cmp_gt_i32_e64 s[58:59], 51, v1
	s_and_b64 s[60:61], s[62:63], s[60:61]
	v_cmp_gt_i32_e64 s[56:57], 50, v1
	s_and_b64 s[58:59], s[60:61], s[58:59]
	v_cmp_gt_i32_e64 s[54:55], 49, v1
	s_and_b64 s[56:57], s[58:59], s[56:57]
	v_cmp_gt_i32_e64 s[52:53], 48, v1
	s_and_b64 s[54:55], s[56:57], s[54:55]
	v_cmp_gt_i32_e64 s[50:51], 43, v1
	s_and_b64 s[52:53], s[54:55], s[52:53]
	v_cmp_gt_i32_e64 s[48:49], 42, v1
	s_and_b64 s[50:51], s[52:53], s[50:51]
	v_cmp_gt_i32_e64 s[46:47], 41, v1
	s_and_b64 s[48:49], s[50:51], s[48:49]
	v_cmp_gt_i32_e64 s[44:45], 40, v1
	s_and_b64 s[46:47], s[48:49], s[46:47]
	v_cmp_gt_i32_e64 s[42:43], 35, v1
	s_and_b64 s[44:45], s[46:47], s[44:45]
	v_cmp_gt_i32_e64 s[40:41], 34, v1
	s_and_b64 s[42:43], s[44:45], s[42:43]
	v_cmp_gt_i32_e64 s[38:39], 33, v1
	s_and_b64 s[40:41], s[42:43], s[40:41]
	v_cmp_gt_i32_e64 s[36:37], 32, v1
	s_and_b64 s[38:39], s[40:41], s[38:39]
	s_and_b64 s[36:37], s[38:39], s[36:37]
	v_cmp_gt_i32_e32 vcc, 0, v1
	v_cmp_gt_i32_e64 s[0:1], 1, v1
	v_cmp_gt_i32_e64 s[6:7], 2, v1
	v_cmp_gt_i32_e64 s[8:9], 3, v1
	v_cmp_gt_i32_e64 s[10:11], 8, v1
	v_cmp_gt_i32_e64 s[14:15], 9, v1
	v_cmp_gt_i32_e64 s[16:17], 10, v1
	v_cmp_gt_i32_e64 s[18:19], 11, v1
	v_cmp_gt_i32_e64 s[20:21], 16, v1
	v_cmp_gt_i32_e64 s[22:23], 17, v1
	v_cmp_gt_i32_e64 s[24:25], 18, v1
	v_cmp_gt_i32_e64 s[26:27], 19, v1
	v_cmp_gt_i32_e64 s[28:29], 24, v1
	v_cmp_gt_i32_e64 s[30:31], 25, v1
	v_cmp_gt_i32_e64 s[34:35], 26, v1
	v_cndmask_b32_e64 v18, v18, v241, s[64:65]
	v_cndmask_b32_e64 v17, v17, v241, s[62:63]
	v_cndmask_b32_e64 v16, v16, v241, s[60:61]
	v_cndmask_b32_e64 v15, v15, v241, s[58:59]
	v_cndmask_b32_e64 v14, v14, v241, s[56:57]
	v_cndmask_b32_e64 v13, v13, v241, s[54:55]
	v_cndmask_b32_e64 v12, v12, v241, s[52:53]
	v_cndmask_b32_e64 v11, v11, v241, s[50:51]
	v_cndmask_b32_e64 v10, v10, v241, s[48:49]
	v_cndmask_b32_e64 v9, v9, v241, s[46:47]
	v_cndmask_b32_e64 v8, v8, v241, s[44:45]
	v_cndmask_b32_e64 v7, v7, v241, s[42:43]
	v_cndmask_b32_e64 v6, v6, v241, s[40:41]
	v_cndmask_b32_e64 v5, v5, v241, s[38:39]
	v_cndmask_b32_e64 v4, v4, v241, s[36:37]
	v_cmp_gt_i32_e64 s[36:37], 27, v1
	v_cmp_gt_i32_e64 s[38:39], 59, v1
	s_and_saveexec_b64 s[12:13], s[38:39]
	v_mov_b32_e32 v19, s85
	s_or_b64 exec, exec, s[12:13]
	s_and_b64 s[34:35], s[36:37], s[34:35]
	s_and_b64 s[30:31], s[34:35], s[30:31]
	s_and_b64 s[28:29], s[30:31], s[28:29]
	s_and_b64 s[26:27], s[28:29], s[26:27]
	s_and_b64 s[24:25], s[26:27], s[24:25]
	s_and_b64 s[22:23], s[24:25], s[22:23]
	s_and_b64 s[20:21], s[22:23], s[20:21]
	s_and_b64 s[18:19], s[20:21], s[18:19]
	s_and_b64 s[16:17], s[18:19], s[16:17]
	s_and_b64 s[14:15], s[16:17], s[14:15]
	s_and_b64 s[10:11], s[14:15], s[10:11]
	s_and_b64 s[8:9], s[10:11], s[8:9]
	s_and_b64 s[6:7], s[8:9], s[6:7]
	s_and_b64 s[0:1], s[6:7], s[0:1]
	s_and_b64 vcc, s[0:1], vcc
	v_cndmask_b32_e64 v34, v34, v241, s[34:35]
	v_cndmask_b32_e64 v33, v33, v241, s[30:31]
	v_cndmask_b32_e64 v32, v32, v241, s[28:29]
	v_cndmask_b32_e64 v31, v31, v241, s[26:27]
	v_cndmask_b32_e64 v30, v30, v241, s[24:25]
	v_cndmask_b32_e64 v29, v29, v241, s[22:23]
	v_cndmask_b32_e64 v28, v28, v241, s[20:21]
	v_cndmask_b32_e64 v27, v27, v241, s[18:19]
	v_cndmask_b32_e64 v26, v26, v241, s[16:17]
	v_cndmask_b32_e64 v25, v25, v241, s[14:15]
	v_cndmask_b32_e64 v24, v24, v241, s[10:11]
	v_cndmask_b32_e64 v23, v23, v241, s[8:9]
	v_cndmask_b32_e64 v22, v22, v241, s[6:7]
	v_cndmask_b32_e64 v21, v21, v241, s[0:1]
	v_cndmask_b32_e32 v20, v20, v241, vcc
	v_cndmask_b32_e64 v35, v35, v241, s[36:37]

; __device__ __forceinline__ void qkt(f32x16& p0, f32x16& p1, LAS const unsigned char* Ks, const bf16x8* qr, int r32, int hi) {
;     p0 = f32x16{}; p1 = f32x16{};
; #pragma unroll
;     for (int d0 = 0; d0 < 8; ++d0) { const int cb = (d0 * 16 + hi * 8) * 2;
;         const bf16x8 b0 = *(LAS const bf16x8*)(Ks + ATT_KSWZ(r32, cb));
;         const bf16x8 b1 = *(LAS const bf16x8*)(Ks + ATT_KSWZ(32 + r32, cb));
;         p0 = __builtin_amdgcn_mfma_f32_32x32x16_bf16(b0, qr[d0], p0, 0, 0, 0);
;         p1 = __builtin_amdgcn_mfma_f32_32x32x16_bf16(b1, qr[d0], p1, 0, 0, 0); }
; }
; __device__ __forceinline__ void partialSM(f32x16& p0, f32x16& p1, float& m_reg, float& mn, float& alpha, int dq, float slopeL, bool diag, bool rowmasked) {
;     const float NEG = -__builtin_inff(); const float a0 = -slopeL * (float)dq;
; #pragma unroll
;     for (int r = 0; r < 16; ++r) { const int c = (r & 3) + 8 * (r >> 2);
;         p0[r] = fmaf(p0[r], CS, fmaf(slopeL, (float)c, a0)); p1[r] = fmaf(p1[r], CS, fmaf(slopeL, (float)(c + 32), a0)); }
;     if (diag) { asm volatile("" ::: "memory");
; #pragma unroll
;         for (int r = 0; r < 16; ++r) { const int c = (r & 3) + 8 * (r >> 2); if (c > dq) p0[r] = NEG; if (c + 32 > dq) p1[r] = NEG; } }
;     if (rowmasked) {
; #pragma unroll
;         for (int r = 0; r < 16; ++r) { p0[r] = NEG; p1[r] = NEG; } }
;     float pmax = p0[0];
; #pragma unroll
;     for (int r = 1; r < 16; ++r) pmax = fmaxf(pmax, p0[r]);
; #pragma unroll
;     for (int r = 0; r < 16; ++r) pmax = fmaxf(pmax, p1[r]);
;     { auto rr = __builtin_amdgcn_permlane32_swap(__float_as_uint(pmax), __float_as_uint(pmax), false, false);
;       pmax = fmaxf(__uint_as_float(rr[0]), __uint_as_float(rr[1])); }
;     if (__builtin_expect(__all(pmax - m_reg <= THRL), 1)) { mn = m_reg; alpha = 1.f; }
;     else { mn = fmaxf(m_reg, pmax); alpha = __builtin_amdgcn_exp2f(m_reg - mn); m_reg = mn; }
; #pragma unroll
;     for (int r = 0; r < 16; ++r) { p0[r] = p0[r] - mn; p1[r] = p1[r] - mn; }
; #pragma unroll
;     for (int r = 0; r < 16; ++r) p0[r] = __builtin_amdgcn_exp2f(p0[r]);
; }
; __device__ __forceinline__ void finishSM(f32x16& p0, f32x16& p1, float alpha, float& l_reg, bf16x8& pa0, bf16x8& pa1, bf16x8& pa2, bf16x8& pa3) {
; #pragma unroll
;     for (int r = 0; r < 16; ++r) p1[r] = __builtin_amdgcn_exp2f(p1[r]);
;     float ps = 0;
; #pragma unroll
.LBB0_842:
	v_exp_f32_e32 v179, v80
	v_exp_f32_e32 v197, v81
	ds_read_b128 v[80:83], v206 offset:49152
	v_exp_f32_e32 v216, v78
	v_exp_f32_e32 v217, v79
	v_exp_f32_e32 v184, v1
	v_add_f32_e32 v1, 0, v170
	v_add_f32_e32 v1, v172, v1
	v_add_f32_e32 v1, v173, v1
	s_waitcnt lgkmcnt(0)
	s_setprio 1
	v_mfma_f32_32x32x16_bf16 v[94:109], v[80:83], v[142:145], 0
	ds_read_b128 v[78:81], v208 offset:49152
	v_add_f32_e32 v1, v175, v1
	v_add_f32_e32 v1, v176, v1
	v_add_f32_e32 v1, v177, v1
	v_add_f32_e32 v1, v171, v1
	v_add_f32_e32 v1, v174, v1
	v_add_f32_e32 v1, v163, v1
	s_waitcnt lgkmcnt(0)
	v_mfma_f32_32x32x16_bf16 v[94:109], v[78:81], v[138:141], v[94:109]
	ds_read_b128 v[78:81], v206 offset:57344
	v_add_f32_e32 v1, v166, v1
	v_add_f32_e32 v1, v167, v1
	v_add_f32_e32 v1, v169, v1
	v_add_f32_e32 v1, v162, v1
	v_add_f32_e32 v1, v164, v1
	v_exp_f32_e32 v185, v2
	s_waitcnt lgkmcnt(0)
	v_mfma_f32_32x32x16_bf16 v[78:93], v[78:81], v[142:145], 0
	ds_read_b128 v[110:113], v208 offset:57344
	ds_read_b128 v[142:145], v204 offset:49152
	s_waitcnt vmcnt(3)
	ds_read_b128 v[146:149], v204 offset:57344
	v_add_f32_e32 v1, v165, v1
	v_add_f32_e32 v1, v168, v1
	v_add_f32_e32 v1, v179, v1
	v_add_f32_e32 v1, v184, v1
	v_exp_f32_e32 v76, v76
	v_add_f32_e32 v1, v185, v1
	s_waitcnt lgkmcnt(2)
	v_mfma_f32_32x32x16_bf16 v[78:93], v[110:113], v[138:141], v[78:93]
	s_setprio 0
	ds_read_b128 v[110:113], v209 offset:49152
	ds_read_b128 v[138:141], v209 offset:57344
	s_waitcnt vmcnt(2)
	ds_read_b128 v[150:153], v210 offset:49152
	s_waitcnt vmcnt(1)
	ds_read_b128 v[154:157], v210 offset:57344
	s_waitcnt vmcnt(0)
	ds_read_b128 v[158:161], v211 offset:49152
	ds_read_b128 v[180:183], v211 offset:57344
	v_exp_f32_e32 v77, v77
	v_add_f32_e32 v1, v197, v1
	v_exp_f32_e32 v204, v74
	v_add_f32_e32 v1, v216, v1
	v_exp_f32_e32 v206, v75
	s_waitcnt lgkmcnt(7)
	s_setprio 1
	v_mfma_f32_32x32x16_bf16 v[94:109], v[142:145], v[134:137], v[94:109]
	ds_read_b128 v[142:145], v212 offset:49152
	ds_read_b128 v[192:195], v212 offset:57344
	ds_read_b128 v[208:211], v213 offset:49152
	ds_read_b128 v[212:215], v213 offset:57344
	v_add_f32_e32 v1, v217, v1
	v_exp_f32_e32 v218, v72
	v_add_f32_e32 v1, v76, v1
	v_exp_f32_e32 v222, v73
	v_add_f32_e32 v1, v77, v1
	s_waitcnt lgkmcnt(10)
	v_mfma_f32_32x32x16_bf16 v[78:93], v[146:149], v[134:137], v[78:93]
	v_exp_f32_e32 v134, v70
	v_add_f32_e32 v1, v204, v1
	v_exp_f32_e32 v135, v71
	v_add_f32_e32 v1, v206, v1
	v_exp_f32_e32 v136, v68
	v_add_f32_e32 v1, v218, v1
	v_exp_f32_e32 v137, v69
	s_waitcnt lgkmcnt(9)
	v_mfma_f32_32x32x16_bf16 v[94:109], v[110:113], v[130:133], v[94:109]
	v_add_f32_e32 v1, v222, v1
	v_add_f32_e32 v1, v134, v1
	v_add_f32_e32 v1, v135, v1
	v_add_f32_e32 v1, v136, v1
	v_add_f32_e32 v1, v137, v1
	v_mov_b32_e32 v2, v1
	v_cvt_pk_bf16_f32 v68, v170, v172
	s_waitcnt lgkmcnt(8)
	v_mfma_f32_32x32x16_bf16 v[78:93], v[138:141], v[130:133], v[78:93]
	v_cvt_pk_bf16_f32 v69, v173, v175
	v_cvt_pk_bf16_f32 v70, v176, v177
	v_cvt_pk_bf16_f32 v71, v171, v174
	v_cvt_pk_bf16_f32 v72, v163, v166
	v_cvt_pk_bf16_f32 v73, v167, v169
	v_cvt_pk_bf16_f32 v74, v162, v164
	v_cvt_pk_bf16_f32 v75, v165, v168
	s_waitcnt lgkmcnt(7)
	v_mfma_f32_32x32x16_bf16 v[94:109], v[150:153], v[126:129], v[94:109]
	v_cvt_pk_bf16_f32 v110, v179, v184
	v_cvt_pk_bf16_f32 v112, v216, v217
	v_permlane32_swap_b32_e32 v1, v2
	v_permlane32_swap_b32_e32 v68, v70
	v_permlane32_swap_b32_e32 v69, v71
	s_waitcnt lgkmcnt(6)
	v_mfma_f32_32x32x16_bf16 v[78:93], v[154:157], v[126:129], v[78:93]
	v_permlane32_swap_b32_e32 v72, v74
	v_permlane32_swap_b32_e32 v73, v75
	v_cvt_pk_bf16_f32 v111, v185, v197
	v_cvt_pk_bf16_f32 v113, v76, v77
	v_permlane32_swap_b32_e32 v110, v112
	s_waitcnt lgkmcnt(5)
	v_mfma_f32_32x32x16_bf16 v[94:109], v[158:161], v[122:125], v[94:109]
	v_permlane32_swap_b32_e32 v111, v113
	s_waitcnt lgkmcnt(4)
	v_mfma_f32_32x32x16_bf16 v[78:93], v[180:183], v[122:125], v[78:93]
	s_waitcnt lgkmcnt(3)
	v_mfma_f32_32x32x16_bf16 v[94:109], v[142:145], v[118:121], v[94:109]
	s_waitcnt lgkmcnt(2)
	v_mfma_f32_32x32x16_bf16 v[78:93], v[192:195], v[118:121], v[78:93]
	v_cvt_pk_bf16_f32 v118, v204, v206
	v_cvt_pk_bf16_f32 v119, v218, v222
	v_cvt_pk_bf16_f32 v120, v134, v135
	v_cvt_pk_bf16_f32 v121, v136, v137
	s_nop 0
	v_permlane32_swap_b32_e32 v118, v120
	v_permlane32_swap_b32_e32 v119, v121
	s_waitcnt lgkmcnt(1)
	v_mfma_f32_32x32x16_bf16 v[94:109], v[208:211], v[114:117], v[94:109]
	s_waitcnt lgkmcnt(0)
	v_mfma_f32_32x32x16_bf16 v[78:93], v[212:215], v[114:117], v[78:93]
	ds_read_b64_tr_b16 v[114:115], v188
	ds_read_b64_tr_b16 v[116:117], v188 offset:2048
	ds_read_b64_tr_b16 v[122:123], v188 offset:4096
	ds_read_b64_tr_b16 v[124:125], v188 offset:6144
	ds_read_b64_tr_b16 v[126:127], v188 offset:8192
	ds_read_b64_tr_b16 v[128:129], v188 offset:10240
	ds_read_b64_tr_b16 v[130:131], v188 offset:12288
	ds_read_b64_tr_b16 v[132:133], v188 offset:14336
	s_waitcnt lgkmcnt(6)
	v_mfma_f32_32x32x16_bf16 v[36:51], v[68:71], v[114:117], v[36:51]
	s_lshl_b32 s0, s82, 6
	v_mov_b32_e32 v197, v196
	s_mov_b32 s66, 0xffff0000
	s_waitcnt lgkmcnt(4)
	v_mfma_f32_32x32x16_bf16 v[36:51], v[72:75], v[122:125], v[36:51]
	s_waitcnt lgkmcnt(2)
	v_mfma_f32_32x32x16_bf16 v[36:51], v[110:113], v[126:129], v[36:51]
	s_waitcnt lgkmcnt(0)
	v_mfma_f32_32x32x16_bf16 v[36:51], v[118:121], v[130:133], v[36:51]
	ds_read_b64_tr_b16 v[114:115], v188 offset:512
	ds_read_b64_tr_b16 v[116:117], v188 offset:2560
	ds_read_b64_tr_b16 v[122:123], v188 offset:4608
	ds_read_b64_tr_b16 v[124:125], v188 offset:6656
	ds_read_b64_tr_b16 v[126:127], v188 offset:8704
	ds_read_b64_tr_b16 v[128:129], v188 offset:10752
	ds_read_b64_tr_b16 v[130:131], v188 offset:12800
	ds_read_b64_tr_b16 v[132:133], v188 offset:14848
	s_waitcnt lgkmcnt(6)
; #define LAS __attribute__((address_space(3)))
; __device__ __forceinline__ s16x4 tr_read(LAS const unsigned char* p) { return __builtin_bit_cast(s16x4, __builtin_amdgcn_ds_read_tr16_b64_v4i16((LAS v4i16_t*)p)); }
; __device__ __forceinline__ void partialSM(f32x16& p0, f32x16& p1, float& m_reg, float& mn, float& alpha, int dq, float slopeL, bool diag, bool rowmasked) {
;     const float NEG = -__builtin_inff(); const float a0 = -slopeL * (float)dq;
; #pragma unroll
;     for (int r = 0; r < 16; ++r) { const int c = (r & 3) + 8 * (r >> 2);
;         p0[r] = fmaf(p0[r], CS, fmaf(slopeL, (float)c, a0)); p1[r] = fmaf(p1[r], CS, fmaf(slopeL, (float)(c + 32), a0)); }
; template <int D0> __device__ __forceinline__ void pv_one(f32x16& od, LAS const unsigned char* vb, bf16x8 pa0, bf16x8 pa1, bf16x8 pa2, bf16x8 pa3) {
;     const s16x4 l0 = tr_read(vb + v_rd_off(D0, 0, 0)), h0 = tr_read(vb + v_rd_off(D0, 0, 1)), l1 = tr_read(vb + v_rd_off(D0, 1, 0)), h1 = tr_read(vb + v_rd_off(D0, 1, 1));
;     const s16x4 l2 = tr_read(vb + v_rd_off(D0, 2, 0)), h2 = tr_read(vb + v_rd_off(D0, 2, 1)), l3 = tr_read(vb + v_rd_off(D0, 3, 0)), h3 = tr_read(vb + v_rd_off(D0, 3, 1));
;     ...
;     od = __builtin_amdgcn_mfma_f32_32x32x16_bf16(pa0, ATT_PK(l0, h0), od, 0, 0, 0);
;     od = __builtin_amdgcn_mfma_f32_32x32x16_bf16(pa1, ATT_PK(l1, h1), od, 0, 0, 0);
;     od = __builtin_amdgcn_mfma_f32_32x32x16_bf16(pa2, ATT_PK(l2, h2), od, 0, 0, 0);
;     od = __builtin_amdgcn_mfma_f32_32x32x16_bf16(pa3, ATT_PK(l3, h3), od, 0, 0, 0);
;     ...
; }
; __device__ __forceinline__ void pv_d0(f32x16* o, LAS const unsigned char* vb, bf16x8 pa0, bf16x8 pa1, bf16x8 pa2, bf16x8 pa3) {
;     pv_one<0>(o[0], vb, pa0, pa1, pa2, pa3); pv_one<1>(o[1], vb, pa0, pa1, pa2, pa3); pv_one<2>(o[2], vb, pa0, pa1, pa2, pa3); pv_one<3>(o[3], vb, pa0, pa1, pa2, pa3);
; }
	v_mfma_f32_32x32x16_bf16 v[20:35], v[68:71], v[114:117], v[20:35]
	s_waitcnt lgkmcnt(4)
	v_mfma_f32_32x32x16_bf16 v[20:35], v[72:75], v[122:125], v[20:35]
	s_waitcnt lgkmcnt(2)
	v_mfma_f32_32x32x16_bf16 v[20:35], v[110:113], v[126:129], v[20:35]
	s_waitcnt lgkmcnt(0)
	v_mfma_f32_32x32x16_bf16 v[20:35], v[118:121], v[130:133], v[20:35]
	ds_read_b64_tr_b16 v[114:115], v188 offset:1024
	ds_read_b64_tr_b16 v[116:117], v188 offset:3072
	ds_read_b64_tr_b16 v[122:123], v188 offset:5120
	ds_read_b64_tr_b16 v[124:125], v188 offset:7168
	ds_read_b64_tr_b16 v[126:127], v188 offset:9216
	ds_read_b64_tr_b16 v[128:129], v188 offset:11264
	ds_read_b64_tr_b16 v[130:131], v188 offset:13312
	ds_read_b64_tr_b16 v[132:133], v188 offset:15360
	s_waitcnt lgkmcnt(6)
	v_mfma_f32_32x32x16_bf16 v[52:67], v[68:71], v[114:117], v[52:67]
	s_waitcnt lgkmcnt(4)
	v_mfma_f32_32x32x16_bf16 v[52:67], v[72:75], v[122:125], v[52:67]
	s_waitcnt lgkmcnt(2)
	v_mfma_f32_32x32x16_bf16 v[52:67], v[110:113], v[126:129], v[52:67]
	s_waitcnt lgkmcnt(0)
	v_mfma_f32_32x32x16_bf16 v[52:67], v[118:121], v[130:133], v[52:67]
	ds_read_b64_tr_b16 v[114:115], v188 offset:1536
	ds_read_b64_tr_b16 v[116:117], v188 offset:3584
	ds_read_b64_tr_b16 v[122:123], v188 offset:5632
	ds_read_b64_tr_b16 v[124:125], v188 offset:7680
	ds_read_b64_tr_b16 v[126:127], v188 offset:9728
	ds_read_b64_tr_b16 v[128:129], v188 offset:11776
	ds_read_b64_tr_b16 v[130:131], v188 offset:13824
	ds_read_b64_tr_b16 v[132:133], v188 offset:15872
	s_waitcnt lgkmcnt(6)
	v_mfma_f32_32x32x16_bf16 v[4:19], v[68:71], v[114:117], v[4:19]
	v_or_b32_e32 v68, s0, v202
	v_sub_u32_e32 v68, v190, v68
	s_add_i32 s0, s0, -1
	s_cmp_le_i32 s0, s81
	s_mov_b32 s0, 2.0
	s_mov_b32 s1, 0x40400000
	s_waitcnt lgkmcnt(4)
	v_mfma_f32_32x32x16_bf16 v[4:19], v[72:75], v[122:125], v[4:19]
	s_waitcnt lgkmcnt(2)
	v_mfma_f32_32x32x16_bf16 v[4:19], v[110:113], v[126:129], v[4:19]
	v_add_u32_e32 v110, 64, v68
	v_cvt_f32_i32_e32 v68, v110
	v_mul_f32_e64 v112, -v196, v68
	v_fma_f32 v114, v198, s0, v112
	v_fma_f32 v115, v199, s1, v112
	s_mov_b32 s0, 0x41000000
	s_mov_b32 s1, 0x41100000
	v_pk_fma_f32 v[116:117], v[198:199], s[0:1], v[112:113] op_sel_hi:[1,1,0]
	s_mov_b32 s0, 0x41200000
	s_waitcnt lgkmcnt(0)
	v_mfma_f32_32x32x16_bf16 v[4:19], v[118:121], v[130:133], v[4:19]
	s_setprio 0
	s_mov_b32 s1, 0x41300000
	v_fma_f32 v118, v198, s0, v112
	v_fma_f32 v119, v199, s1, v112
	s_mov_b32 s0, 0x41800000
	s_mov_b32 s1, 0x41880000
	v_pk_fma_f32 v[76:77], v[198:199], s[0:1], v[112:113] op_sel_hi:[1,1,0]
	s_mov_b32 s0, 0x41900000
	v_fma_f32 v69, -v196, v68, v196
	v_mov_b32_e32 v68, v112
	s_mov_b32 s1, 0x41980000
	v_fmac_f32_e32 v68, 0, v196
	v_pk_fma_f32 v[74:75], v[198:199], s[0:1], v[112:113] op_sel_hi:[1,1,0]
	v_pk_fma_f32 v[70:71], v[198:199], s[86:87], v[112:113] op_sel_hi:[1,1,0]
	v_pk_fma_f32 v[120:121], v[198:199], s[88:89], v[112:113] op_sel_hi:[1,1,0]
	v_pk_fma_f32 v[72:73], v[94:95], s[96:97], v[68:69] op_sel_hi:[1,0,1]
	v_pk_fma_f32 v[68:69], v[108:109], s[96:97], v[120:121] op_sel_hi:[1,0,1]
	v_pk_fma_f32 v[70:71], v[106:107], s[96:97], v[70:71] op_sel_hi:[1,0,1]
	v_pk_fma_f32 v[74:75], v[104:105], s[96:97], v[74:75] op_sel_hi:[1,0,1]
	v_pk_fma_f32 v[76:77], v[102:103], s[96:97], v[76:77] op_sel_hi:[1,0,1]
	v_pk_fma_f32 v[94:95], v[100:101], s[96:97], v[118:119] op_sel_hi:[1,0,1]
	v_pk_fma_f32 v[98:99], v[98:99], s[96:97], v[116:117] op_sel_hi:[1,0,1]
	v_pk_fma_f32 v[96:97], v[96:97], s[96:97], v[114:115] op_sel_hi:[1,0,1]
	v_pk_fma_f32 v[100:101], v[196:197], s[90:91], v[112:113] op_sel_hi:[1,1,0]
	v_pk_fma_f32 v[102:103], v[196:197], s[92:93], v[112:113] op_sel_hi:[1,1,0]
	v_pk_fma_f32 v[104:105], v[196:197], s[94:95], v[112:113] op_sel_hi:[1,1,0]
	v_pk_fma_f32 v[106:107], v[196:197], s[68:69], v[112:113] op_sel_hi:[1,1,0]
	v_pk_fma_f32 v[108:109], v[196:197], s[70:71], v[112:113] op_sel_hi:[1,1,0]
	v_pk_fma_f32 v[114:115], v[196:197], s[72:73], v[112:113] op_sel_hi:[1,1,0]
	v_pk_fma_f32 v[116:117], v[196:197], s[74:75], v[112:113] op_sel_hi:[1,1,0]
	v_pk_fma_f32 v[112:113], v[200:201], s[76:77], v[112:113] op_sel_hi:[1,1,0]
	v_pk_fma_f32 v[92:93], v[92:93], s[96:97], v[116:117] op_sel_hi:[1,0,1]
	v_pk_fma_f32 v[90:91], v[90:91], s[96:97], v[114:115] op_sel_hi:[1,0,1]
	v_pk_fma_f32 v[88:89], v[88:89], s[96:97], v[108:109] op_sel_hi:[1,0,1]
	v_pk_fma_f32 v[86:87], v[86:87], s[96:97], v[106:107] op_sel_hi:[1,0,1]
	v_pk_fma_f32 v[84:85], v[84:85], s[96:97], v[104:105] op_sel_hi:[1,0,1]
	v_pk_fma_f32 v[82:83], v[82:83], s[96:97], v[102:103] op_sel_hi:[1,0,1]
	v_pk_fma_f32 v[80:81], v[80:81], s[96:97], v[100:101] op_sel_hi:[1,0,1]
	v_pk_fma_f32 v[78:79], v[78:79], s[96:97], v[112:113] op_sel_hi:[1,0,1]
	s_cbranch_scc1 .LBB0_846
; __device__ __forceinline__ void partialSM(f32x16& p0, f32x16& p1, float& m_reg, float& mn, float& alpha, int dq, float slopeL, bool diag, bool rowmasked) {
;     ...
;     for (int r = 0; r < 16; ++r) { const int c = (r & 3) + 8 * (r >> 2);
;         p0[r] = fmaf(p0[r], CS, fmaf(slopeL, (float)c, a0)); p1[r] = fmaf(p1[r], CS, fmaf(slopeL, (float)(c + 32), a0)); }
;     if (diag) { asm volatile("" ::: "memory");
; #pragma unroll
;         for (int r = 0; r < 16; ++r) { const int c = (r & 3) + 8 * (r >> 2); if (c > dq) p0[r] = NEG; if (c + 32 > dq) p1[r] = NEG; } }
	v_cmp_gt_i32_e64 s[62:63], 57, v110
	v_cmp_gt_i32_e64 s[64:65], 58, v110
	v_cmp_gt_i32_e64 s[60:61], 56, v110
	s_and_b64 s[62:63], s[64:65], s[62:63]
	v_cmp_gt_i32_e64 s[58:59], 51, v110
	s_and_b64 s[60:61], s[62:63], s[60:61]
	v_cmp_gt_i32_e64 s[56:57], 50, v110
	s_and_b64 s[58:59], s[60:61], s[58:59]
	v_cmp_gt_i32_e64 s[54:55], 49, v110
	s_and_b64 s[56:57], s[58:59], s[56:57]
	v_cmp_gt_i32_e64 s[52:53], 48, v110
	s_and_b64 s[54:55], s[56:57], s[54:55]
	v_cmp_gt_i32_e64 s[50:51], 43, v110
	s_and_b64 s[52:53], s[54:55], s[52:53]
	v_cmp_gt_i32_e64 s[48:49], 42, v110
	s_and_b64 s[50:51], s[52:53], s[50:51]
	v_cmp_gt_i32_e64 s[46:47], 41, v110
	s_and_b64 s[48:49], s[50:51], s[48:49]
	v_cmp_gt_i32_e64 s[44:45], 40, v110
	s_and_b64 s[46:47], s[48:49], s[46:47]
	v_cmp_gt_i32_e64 s[42:43], 35, v110
	s_and_b64 s[44:45], s[46:47], s[44:45]
	v_cmp_gt_i32_e64 s[40:41], 34, v110
	s_and_b64 s[42:43], s[44:45], s[42:43]
	v_cmp_gt_i32_e64 s[38:39], 33, v110
	s_and_b64 s[40:41], s[42:43], s[40:41]
	v_cmp_gt_i32_e64 s[36:37], 32, v110
	s_and_b64 s[38:39], s[40:41], s[38:39]
	s_and_b64 s[36:37], s[38:39], s[36:37]
	v_cmp_gt_i32_e32 vcc, 0, v110
	v_cmp_gt_i32_e64 s[0:1], 1, v110
	v_cmp_gt_i32_e64 s[6:7], 2, v110
	v_cmp_gt_i32_e64 s[8:9], 3, v110
	v_cmp_gt_i32_e64 s[10:11], 8, v110
	v_cmp_gt_i32_e64 s[14:15], 9, v110
	v_cmp_gt_i32_e64 s[16:17], 10, v110
	v_cmp_gt_i32_e64 s[18:19], 11, v110
	v_cmp_gt_i32_e64 s[20:21], 16, v110
	v_cmp_gt_i32_e64 s[22:23], 17, v110
	v_cmp_gt_i32_e64 s[24:25], 18, v110
	v_cmp_gt_i32_e64 s[26:27], 19, v110
	v_cmp_gt_i32_e64 s[28:29], 24, v110
	v_cmp_gt_i32_e64 s[30:31], 25, v110
	v_cmp_gt_i32_e64 s[34:35], 26, v110
	v_cndmask_b32_e64 v92, v92, v241, s[64:65]
	v_cndmask_b32_e64 v91, v91, v241, s[62:63]
	v_cndmask_b32_e64 v90, v90, v241, s[60:61]
	v_cndmask_b32_e64 v89, v89, v241, s[58:59]
	v_cndmask_b32_e64 v88, v88, v241, s[56:57]
	v_cndmask_b32_e64 v87, v87, v241, s[54:55]
	v_cndmask_b32_e64 v86, v86, v241, s[52:53]
	v_cndmask_b32_e64 v85, v85, v241, s[50:51]
	v_cndmask_b32_e64 v84, v84, v241, s[48:49]
	v_cndmask_b32_e64 v83, v83, v241, s[46:47]
	v_cndmask_b32_e64 v82, v82, v241, s[44:45]
	v_cndmask_b32_e64 v81, v81, v241, s[42:43]
	v_cndmask_b32_e64 v80, v80, v241, s[40:41]
	v_cndmask_b32_e64 v79, v79, v241, s[38:39]
	v_cndmask_b32_e64 v78, v78, v241, s[36:37]
	v_cmp_gt_i32_e64 s[36:37], 27, v110
	v_cmp_gt_i32_e64 s[38:39], 59, v110
	s_and_saveexec_b64 s[12:13], s[38:39]
	v_mov_b32_e32 v93, s85
	s_or_b64 exec, exec, s[12:13]
	s_and_b64 s[34:35], s[36:37], s[34:35]
	s_and_b64 s[30:31], s[34:35], s[30:31]
	s_and_b64 s[28:29], s[30:31], s[28:29]
	s_and_b64 s[26:27], s[28:29], s[26:27]
	s_and_b64 s[24:25], s[26:27], s[24:25]
	s_and_b64 s[22:23], s[24:25], s[22:23]
	s_and_b64 s[20:21], s[22:23], s[20:21]
	s_and_b64 s[18:19], s[20:21], s[18:19]
	s_and_b64 s[16:17], s[18:19], s[16:17]
	s_and_b64 s[14:15], s[16:17], s[14:15]
	s_and_b64 s[10:11], s[14:15], s[10:11]
	s_and_b64 s[8:9], s[10:11], s[8:9]
	s_and_b64 s[6:7], s[8:9], s[6:7]
	s_and_b64 s[0:1], s[6:7], s[0:1]
	s_and_b64 vcc, s[0:1], vcc
	v_cndmask_b32_e64 v68, v68, v241, s[34:35]
	v_cndmask_b32_e64 v71, v71, v241, s[30:31]
	v_cndmask_b32_e64 v70, v70, v241, s[28:29]
	v_cndmask_b32_e64 v75, v75, v241, s[26:27]
	v_cndmask_b32_e64 v74, v74, v241, s[24:25]
	v_cndmask_b32_e64 v77, v77, v241, s[22:23]
	v_cndmask_b32_e64 v76, v76, v241, s[20:21]
	v_cndmask_b32_e64 v95, v95, v241, s[18:19]
	v_cndmask_b32_e64 v94, v94, v241, s[16:17]
	v_cndmask_b32_e64 v99, v99, v241, s[14:15]
	v_cndmask_b32_e64 v98, v98, v241, s[10:11]
	v_cndmask_b32_e64 v97, v97, v241, s[8:9]
	v_cndmask_b32_e64 v96, v96, v241, s[6:7]
	v_cndmask_b32_e64 v73, v73, v241, s[0:1]
	v_cndmask_b32_e32 v72, v72, v241, vcc
	v_cndmask_b32_e64 v69, v69, v241, s[36:37]

; #define LAS __attribute__((address_space(3)))
; __device__ __forceinline__ s16x4 tr_read(LAS const unsigned char* p) { return __builtin_bit_cast(s16x4, __builtin_amdgcn_ds_read_tr16_b64_v4i16((LAS v4i16_t*)p)); }
; __device__ __forceinline__ void partialSM(f32x16& p0, f32x16& p1, float& m_reg, float& mn, float& alpha, int dq, float slopeL, bool diag, bool rowmasked) {
;     ...
;     else { mn = fmaxf(m_reg, pmax); alpha = __builtin_amdgcn_exp2f(m_reg - mn); m_reg = mn; }
; #pragma unroll
;     for (int r = 0; r < 16; ++r) { p0[r] = p0[r] - mn; p1[r] = p1[r] - mn; }
; #pragma unroll
;     for (int r = 0; r < 16; ++r) p0[r] = __builtin_amdgcn_exp2f(p0[r]);
; }
; __device__ __forceinline__ void finishSM(f32x16& p0, f32x16& p1, float alpha, float& l_reg, bf16x8& pa0, bf16x8& pa1, bf16x8& pa2, bf16x8& pa3) {
; #pragma unroll
;     for (int r = 0; r < 16; ++r) p1[r] = __builtin_amdgcn_exp2f(p1[r]);
;     float ps = 0;
; #pragma unroll
;     for (int r = 0; r < 16; ++r) ps += p0[r];
; #pragma unroll
;     for (int r = 0; r < 16; ++r) ps += p1[r];
;     { auto rr = __builtin_amdgcn_permlane32_swap(__float_as_uint(ps), __float_as_uint(ps), false, false);
;       ps = __uint_as_float(rr[0]) + __uint_as_float(rr[1]); }
;     l_reg = l_reg * alpha + ps;
;     ...
;     ATT_PK4(p0, 0, pa0); ATT_PK4(p0, 8, pa1); ATT_PK4(p1, 0, pa2); ATT_PK4(p1, 8, pa3);
;     ...
; }
; template <int D0> __device__ __forceinline__ void pv_one(f32x16& od, LAS const unsigned char* vb, bf16x8 pa0, bf16x8 pa1, bf16x8 pa2, bf16x8 pa3) {
;     const s16x4 l0 = tr_read(vb + v_rd_off(D0, 0, 0)), h0 = tr_read(vb + v_rd_off(D0, 0, 1)), l1 = tr_read(vb + v_rd_off(D0, 1, 0)), h1 = tr_read(vb + v_rd_off(D0, 1, 1));
;     const s16x4 l2 = tr_read(vb + v_rd_off(D0, 2, 0)), h2 = tr_read(vb + v_rd_off(D0, 2, 1)), l3 = tr_read(vb + v_rd_off(D0, 3, 0)), h3 = tr_read(vb + v_rd_off(D0, 3, 1));
;     ...
;     od = __builtin_amdgcn_mfma_f32_32x32x16_bf16(pa0, ATT_PK(l0, h0), od, 0, 0, 0);
;     od = __builtin_amdgcn_mfma_f32_32x32x16_bf16(pa1, ATT_PK(l1, h1), od, 0, 0, 0);
;     od = __builtin_amdgcn_mfma_f32_32x32x16_bf16(pa2, ATT_PK(l2, h2), od, 0, 0, 0);
;     od = __builtin_amdgcn_mfma_f32_32x32x16_bf16(pa3, ATT_PK(l3, h3), od, 0, 0, 0);
.LBB0_850:
	v_cndmask_b32_e64 v101, v101, v220, s[0:1]
	v_sub_f32_e32 v72, v72, v101
	v_sub_f32_e32 v73, v73, v101
	v_sub_f32_e32 v104, v76, v101
	v_exp_f32_e32 v76, v72
	v_sub_f32_e32 v96, v96, v101
	v_sub_f32_e32 v105, v77, v101
	v_exp_f32_e32 v77, v73
	v_sub_f32_e32 v97, v97, v101
	v_sub_f32_e32 v102, v94, v101
	v_exp_f32_e32 v94, v96
	v_sub_f32_e32 v98, v98, v101
	v_sub_f32_e32 v103, v95, v101
	v_exp_f32_e32 v95, v97
	v_sub_f32_e32 v78, v78, v101
	v_sub_f32_e32 v99, v99, v101
	v_sub_f32_e32 v74, v74, v101
	v_sub_f32_e32 v75, v75, v101
	v_sub_f32_e32 v106, v70, v101
	v_sub_f32_e32 v107, v71, v101
	v_sub_f32_e32 v108, v68, v101
	v_sub_f32_e32 v109, v69, v101
	v_exp_f32_e32 v96, v98
	v_sub_f32_e32 v79, v79, v101
	v_sub_f32_e32 v80, v80, v101
	v_sub_f32_e32 v81, v81, v101
	v_sub_f32_e32 v82, v82, v101
	v_sub_f32_e32 v83, v83, v101
	v_sub_f32_e32 v84, v84, v101
	v_sub_f32_e32 v85, v85, v101
	v_sub_f32_e32 v86, v86, v101
	v_sub_f32_e32 v87, v87, v101
	v_sub_f32_e32 v88, v88, v101
	v_sub_f32_e32 v89, v89, v101
	v_sub_f32_e32 v90, v90, v101
	v_sub_f32_e32 v91, v91, v101
	v_sub_f32_e32 v92, v92, v101
	v_sub_f32_e32 v93, v93, v101
	v_exp_f32_e32 v101, v78
	v_add_f32_e32 v78, 0, v76
	v_exp_f32_e32 v97, v99
	v_add_f32_e32 v78, v77, v78
	v_exp_f32_e32 v98, v102
	v_add_f32_e32 v78, v94, v78
	v_exp_f32_e32 v99, v103
	v_add_f32_e32 v78, v95, v78
	v_exp_f32_e32 v68, v104
	v_add_f32_e32 v78, v96, v78
	v_exp_f32_e32 v69, v105
	v_add_f32_e32 v78, v97, v78
	v_exp_f32_e32 v70, v74
	v_add_f32_e32 v78, v98, v78
	v_exp_f32_e32 v71, v75
	v_add_f32_e32 v78, v99, v78
	v_exp_f32_e32 v72, v106
	v_add_f32_e32 v78, v68, v78
	v_exp_f32_e32 v73, v107
	v_add_f32_e32 v78, v69, v78
	v_exp_f32_e32 v74, v108
	v_add_f32_e32 v78, v70, v78
	v_exp_f32_e32 v75, v109
	v_add_f32_e32 v78, v71, v78
	v_add_f32_e32 v78, v72, v78
	v_exp_f32_e32 v102, v79
	v_add_f32_e32 v78, v73, v78
	v_exp_f32_e32 v103, v80
	v_add_f32_e32 v78, v74, v78
	v_exp_f32_e32 v104, v81
	v_add_f32_e32 v78, v75, v78
	v_exp_f32_e32 v105, v82
	v_add_f32_e32 v78, v101, v78
	v_exp_f32_e32 v106, v83
	v_add_f32_e32 v78, v102, v78
	v_exp_f32_e32 v107, v84
	v_add_f32_e32 v78, v103, v78
	v_exp_f32_e32 v108, v85
	v_add_f32_e32 v78, v104, v78
	v_exp_f32_e32 v86, v86
	v_add_f32_e32 v78, v105, v78
	v_exp_f32_e32 v87, v87
	v_add_f32_e32 v78, v106, v78
	v_exp_f32_e32 v88, v88
	v_add_f32_e32 v78, v107, v78
	v_exp_f32_e32 v89, v89
	v_add_f32_e32 v78, v108, v78
	v_exp_f32_e32 v90, v90
	v_add_f32_e32 v78, v86, v78
	v_exp_f32_e32 v91, v91
	v_add_f32_e32 v78, v87, v78
	v_exp_f32_e32 v92, v92
	v_add_f32_e32 v78, v88, v78
	v_exp_f32_e32 v93, v93
	v_add_f32_e32 v78, v89, v78
	v_add_f32_e32 v78, v90, v78
	v_add_f32_e32 v78, v91, v78
	v_add_f32_e32 v78, v92, v78
	v_add_f32_e32 v84, v93, v78
	v_mov_b32_e32 v85, v84
	s_nop 1
	v_permlane32_swap_b32_e32 v84, v85
	v_cvt_pk_bf16_f32 v80, v76, v77
	v_cvt_pk_bf16_f32 v81, v94, v95
	v_cvt_pk_bf16_f32 v82, v96, v97
	v_cvt_pk_bf16_f32 v83, v98, v99
	v_cvt_pk_bf16_f32 v76, v68, v69
	v_cvt_pk_bf16_f32 v77, v70, v71
	v_cvt_pk_bf16_f32 v78, v72, v73
	v_cvt_pk_bf16_f32 v79, v74, v75
	v_cvt_pk_bf16_f32 v72, v101, v102
	v_cvt_pk_bf16_f32 v73, v103, v104
	v_cvt_pk_bf16_f32 v74, v105, v106
	v_cvt_pk_bf16_f32 v75, v107, v108
	v_cvt_pk_bf16_f32 v68, v86, v87
	v_cvt_pk_bf16_f32 v69, v88, v89
	v_cvt_pk_bf16_f32 v70, v90, v91
	v_cvt_pk_bf16_f32 v71, v92, v93
	v_permlane32_swap_b32_e32 v80, v82
	v_permlane32_swap_b32_e32 v81, v83
	v_permlane32_swap_b32_e32 v76, v78
	v_permlane32_swap_b32_e32 v77, v79
	v_permlane32_swap_b32_e32 v72, v74
	v_permlane32_swap_b32_e32 v73, v75
	v_permlane32_swap_b32_e32 v68, v70
	v_permlane32_swap_b32_e32 v69, v71
	ds_read_b64_tr_b16 v[86:87], v188 offset:16384
	ds_read_b64_tr_b16 v[88:89], v188 offset:18432
	v_cmp_gt_u32_e32 vcc, 32, v186
	s_waitcnt lgkmcnt(0)
	s_setprio 1
	v_mfma_f32_32x32x16_bf16 v[36:51], v[80:83], v[86:89], v[36:51]
	ds_read_b64_tr_b16 v[86:87], v188 offset:20480
	ds_read_b64_tr_b16 v[88:89], v188 offset:22528
	s_waitcnt lgkmcnt(0)
	v_mfma_f32_32x32x16_bf16 v[36:51], v[76:79], v[86:89], v[36:51]
	ds_read_b64_tr_b16 v[86:87], v188 offset:24576
	ds_read_b64_tr_b16 v[88:89], v188 offset:26624
	s_waitcnt lgkmcnt(0)
	v_mfma_f32_32x32x16_bf16 v[36:51], v[72:75], v[86:89], v[36:51]
	ds_read_b64_tr_b16 v[86:87], v188 offset:28672
	ds_read_b64_tr_b16 v[88:89], v188 offset:30720
	s_waitcnt lgkmcnt(0)
	v_mfma_f32_32x32x16_bf16 v[36:51], v[68:71], v[86:89], v[36:51]
	ds_read_b64_tr_b16 v[86:87], v188 offset:16896
	ds_read_b64_tr_b16 v[88:89], v188 offset:18944
	s_waitcnt lgkmcnt(0)
	v_mfma_f32_32x32x16_bf16 v[20:35], v[80:83], v[86:89], v[20:35]
	ds_read_b64_tr_b16 v[86:87], v188 offset:20992
	ds_read_b64_tr_b16 v[88:89], v188 offset:23040
	s_waitcnt lgkmcnt(0)
	v_mfma_f32_32x32x16_bf16 v[20:35], v[76:79], v[86:89], v[20:35]
	ds_read_b64_tr_b16 v[86:87], v188 offset:25088
	ds_read_b64_tr_b16 v[88:89], v188 offset:27136
	s_waitcnt lgkmcnt(0)
	v_mfma_f32_32x32x16_bf16 v[20:35], v[72:75], v[86:89], v[20:35]
	ds_read_b64_tr_b16 v[86:87], v188 offset:29184
	ds_read_b64_tr_b16 v[88:89], v188 offset:31232
	s_waitcnt lgkmcnt(0)
	v_mfma_f32_32x32x16_bf16 v[20:35], v[68:71], v[86:89], v[20:35]
	ds_read_b64_tr_b16 v[86:87], v188 offset:17408
	ds_read_b64_tr_b16 v[88:89], v188 offset:19456
	s_waitcnt lgkmcnt(0)
	v_mfma_f32_32x32x16_bf16 v[52:67], v[80:83], v[86:89], v[52:67]
	ds_read_b64_tr_b16 v[86:87], v188 offset:21504
	ds_read_b64_tr_b16 v[88:89], v188 offset:23552
	s_waitcnt lgkmcnt(0)
	v_mfma_f32_32x32x16_bf16 v[52:67], v[76:79], v[86:89], v[52:67]
	ds_read_b64_tr_b16 v[86:87], v188 offset:25600
	ds_read_b64_tr_b16 v[88:89], v188 offset:27648
	s_waitcnt lgkmcnt(0)
; #define LAS __attribute__((address_space(3)))
; #define ATT_SBAR() __builtin_amdgcn_sched_barrier(0)
; __device__ __forceinline__ int crow(int r, int hi) { return (r & 3) + 8 * (r >> 2) + 4 * hi; }
; __device__ __forceinline__ s16x4 tr_read(LAS const unsigned char* p) { return __builtin_bit_cast(s16x4, __builtin_amdgcn_ds_read_tr16_b64_v4i16((LAS v4i16_t*)p)); }
; #define ATT_RESC(a) do { if (__any((a) < 1.f)) { if (hi == 0) al_l[r32] = (a); asm volatile("s_waitcnt lgkmcnt(0)" ::: "memory"); \
;     _Pragma("unroll") for (int d_ = 0; d_ < 4; ++d_) _Pragma("unroll") for (int r = 0; r < 16; ++r) o[d_][r] *= al_l[crow(r, hi)]; } } while (0)
; template <int D0> __device__ __forceinline__ void pv_one(f32x16& od, LAS const unsigned char* vb, bf16x8 pa0, bf16x8 pa1, bf16x8 pa2, bf16x8 pa3) {
;     const s16x4 l0 = tr_read(vb + v_rd_off(D0, 0, 0)), h0 = tr_read(vb + v_rd_off(D0, 0, 1)), l1 = tr_read(vb + v_rd_off(D0, 1, 0)), h1 = tr_read(vb + v_rd_off(D0, 1, 1));
;     const s16x4 l2 = tr_read(vb + v_rd_off(D0, 2, 0)), h2 = tr_read(vb + v_rd_off(D0, 2, 1)), l3 = tr_read(vb + v_rd_off(D0, 3, 0)), h3 = tr_read(vb + v_rd_off(D0, 3, 1));
;     ...
;     od = __builtin_amdgcn_mfma_f32_32x32x16_bf16(pa0, ATT_PK(l0, h0), od, 0, 0, 0);
;     od = __builtin_amdgcn_mfma_f32_32x32x16_bf16(pa1, ATT_PK(l1, h1), od, 0, 0, 0);
;     od = __builtin_amdgcn_mfma_f32_32x32x16_bf16(pa2, ATT_PK(l2, h2), od, 0, 0, 0);
;     od = __builtin_amdgcn_mfma_f32_32x32x16_bf16(pa3, ATT_PK(l3, h3), od, 0, 0, 0);
; template <bool MOBA>
; __device__ __forceinline__ void run_unit(const UnitDesc& U, LAS unsigned char* lds, f32x16 (&o)[4], float (&rli)[16]) {
;     ...
;     __syncthreads(); ATT_RESC(alB);
;     finishSM(pB0, pB1, alB, l_reg, pa0, pa1, pa2, pa3); ATT_SBAR();
;     pv_d0(o, vb0 + SHM_V, pa0, pa1, pa2, pa3);
;     if (hi == 0) li_l[r32] = l_reg;
;     asm volatile("s_waitcnt lgkmcnt(0)" ::: "memory");
; #pragma unroll
;     for (int r = 0; r < 16; ++r) rli[r] = 1.0f / li_l[crow(r, hi)];
;     __syncthreads();
	v_mfma_f32_32x32x16_bf16 v[52:67], v[72:75], v[86:89], v[52:67]
	ds_read_b64_tr_b16 v[86:87], v188 offset:29696
	ds_read_b64_tr_b16 v[88:89], v188 offset:31744
	s_waitcnt lgkmcnt(0)
	v_mfma_f32_32x32x16_bf16 v[52:67], v[68:71], v[86:89], v[52:67]
	ds_read_b64_tr_b16 v[86:87], v188 offset:17920
	ds_read_b64_tr_b16 v[88:89], v188 offset:19968
	s_waitcnt lgkmcnt(0)
	v_mfma_f32_32x32x16_bf16 v[4:19], v[80:83], v[86:89], v[4:19]
	ds_read_b64_tr_b16 v[80:81], v188 offset:22016
	ds_read_b64_tr_b16 v[82:83], v188 offset:24064
	s_waitcnt lgkmcnt(0)
	v_mfma_f32_32x32x16_bf16 v[4:19], v[76:79], v[80:83], v[4:19]
	ds_read_b64_tr_b16 v[76:77], v188 offset:26112
	ds_read_b64_tr_b16 v[78:79], v188 offset:28160
	s_waitcnt lgkmcnt(0)
	v_mfma_f32_32x32x16_bf16 v[4:19], v[72:75], v[76:79], v[4:19]
	ds_read_b64_tr_b16 v[72:73], v188 offset:30208
	ds_read_b64_tr_b16 v[74:75], v188 offset:32256
	s_waitcnt lgkmcnt(0)
	v_mfma_f32_32x32x16_bf16 v[4:19], v[68:71], v[72:75], v[4:19]
	s_setprio 0
	s_and_saveexec_b64 s[0:1], vcc
	v_add_f32_e32 v1, v1, v2
	v_fmac_f32_e32 v1, v191, v178
	v_add_f32_e32 v2, v84, v85
	v_fmac_f32_e32 v2, v1, v100
	ds_write_b32 v189, v2
	s_or_b64 exec, exec, s[0:1]
	s_waitcnt lgkmcnt(0)
	ds_read_b128 v[72:75], v187
	ds_read_b128 v[68:71], v187 offset:32
	v_mov_b32_e32 v238, v219
	s_cmp_lg_u32 s2, 0
	s_waitcnt lgkmcnt(1)
	v_div_scale_f32 v1, s[0:1], v72, v72, 1.0
	v_rcp_f32_e32 v2, v1
	s_nop 0
	v_fma_f32 v76, -v1, v2, 1.0
	v_fmac_f32_e32 v2, v76, v2
	v_div_scale_f32 v76, vcc, 1.0, v72, 1.0
	v_mul_f32_e32 v77, v76, v2
	v_fma_f32 v78, -v1, v77, v76
	v_fmac_f32_e32 v77, v78, v2
	v_fma_f32 v1, -v1, v77, v76
	v_div_fmas_f32 v1, v1, v2, v77
	v_div_fixup_f32 v202, v1, v72, 1.0
	v_div_scale_f32 v1, s[0:1], v73, v73, 1.0
	v_rcp_f32_e32 v2, v1
	s_nop 0
	v_fma_f32 v72, -v1, v2, 1.0
	v_fmac_f32_e32 v2, v72, v2
	v_div_scale_f32 v72, vcc, 1.0, v73, 1.0
	v_mul_f32_e32 v76, v72, v2
	v_fma_f32 v77, -v1, v76, v72
	v_fmac_f32_e32 v76, v77, v2
	v_fma_f32 v1, -v1, v76, v72
	v_div_fmas_f32 v1, v1, v2, v76
	v_div_fixup_f32 v204, v1, v73, 1.0
	v_div_scale_f32 v1, s[0:1], v74, v74, 1.0
	v_rcp_f32_e32 v2, v1
	s_nop 0
	v_fma_f32 v72, -v1, v2, 1.0
	v_fmac_f32_e32 v2, v72, v2
	v_div_scale_f32 v72, vcc, 1.0, v74, 1.0
	v_mul_f32_e32 v73, v72, v2
	v_fma_f32 v76, -v1, v73, v72
	v_fmac_f32_e32 v73, v76, v2
	v_fma_f32 v1, -v1, v73, v72
	v_div_fmas_f32 v1, v1, v2, v73
	v_div_fixup_f32 v206, v1, v74, 1.0
	v_div_scale_f32 v1, s[0:1], v75, v75, 1.0
	v_rcp_f32_e32 v2, v1
	s_nop 0
	v_fma_f32 v72, -v1, v2, 1.0
	v_fmac_f32_e32 v2, v72, v2
	v_div_scale_f32 v72, vcc, 1.0, v75, 1.0
	v_mul_f32_e32 v73, v72, v2
	v_fma_f32 v74, -v1, v73, v72
	v_fmac_f32_e32 v73, v74, v2
	v_fma_f32 v1, -v1, v73, v72
	v_div_fmas_f32 v1, v1, v2, v73
	v_div_fixup_f32 v208, v1, v75, 1.0
	s_waitcnt lgkmcnt(0)
	v_div_scale_f32 v1, s[0:1], v68, v68, 1.0
	v_rcp_f32_e32 v2, v1
	s_nop 0
	v_fma_f32 v72, -v1, v2, 1.0
	v_fmac_f32_e32 v2, v72, v2
	v_div_scale_f32 v72, vcc, 1.0, v68, 1.0
	v_mul_f32_e32 v73, v72, v2
	v_fma_f32 v74, -v1, v73, v72
	v_fmac_f32_e32 v73, v74, v2
	v_fma_f32 v1, -v1, v73, v72
	v_div_fmas_f32 v1, v1, v2, v73
	v_div_fixup_f32 v210, v1, v68, 1.0
	v_div_scale_f32 v1, s[0:1], v69, v69, 1.0
	v_rcp_f32_e32 v2, v1
	s_nop 0
	v_fma_f32 v68, -v1, v2, 1.0
	v_fmac_f32_e32 v2, v68, v2
	v_div_scale_f32 v68, vcc, 1.0, v69, 1.0
	v_mul_f32_e32 v72, v68, v2
	v_fma_f32 v73, -v1, v72, v68
	v_fmac_f32_e32 v72, v73, v2
	v_fma_f32 v1, -v1, v72, v68
	v_div_fmas_f32 v1, v1, v2, v72
	v_div_fixup_f32 v212, v1, v69, 1.0
	v_div_scale_f32 v1, s[0:1], v70, v70, 1.0
	v_rcp_f32_e32 v2, v1
	s_nop 0
	v_fma_f32 v68, -v1, v2, 1.0
	v_fmac_f32_e32 v2, v68, v2
	v_div_scale_f32 v68, vcc, 1.0, v70, 1.0
	v_mul_f32_e32 v69, v68, v2
	v_fma_f32 v72, -v1, v69, v68
	v_fmac_f32_e32 v69, v72, v2
	v_fma_f32 v1, -v1, v69, v68
	v_div_fmas_f32 v1, v1, v2, v69
	v_div_fixup_f32 v214, v1, v70, 1.0
	v_div_scale_f32 v1, s[0:1], v71, v71, 1.0
	v_rcp_f32_e32 v2, v1
	s_nop 0
	v_fma_f32 v68, -v1, v2, 1.0
	v_fmac_f32_e32 v2, v68, v2
	v_div_scale_f32 v68, vcc, 1.0, v71, 1.0
	v_mul_f32_e32 v69, v68, v2
	v_fma_f32 v70, -v1, v69, v68
	v_fmac_f32_e32 v69, v70, v2
	v_fma_f32 v1, -v1, v69, v68
	v_div_fmas_f32 v1, v1, v2, v69
	v_div_fixup_f32 v216, v1, v71, 1.0
	ds_read_b128 v[68:71], v187 offset:64
	s_waitcnt lgkmcnt(0)
	v_div_scale_f32 v1, s[0:1], v68, v68, 1.0
	v_rcp_f32_e32 v2, v1
	s_nop 0
	v_fma_f32 v72, -v1, v2, 1.0
	v_fmac_f32_e32 v2, v72, v2
	v_div_scale_f32 v72, vcc, 1.0, v68, 1.0
	v_mul_f32_e32 v73, v72, v2
	v_fma_f32 v74, -v1, v73, v72
	v_fmac_f32_e32 v73, v74, v2
	v_fma_f32 v1, -v1, v73, v72
	v_div_fmas_f32 v1, v1, v2, v73
	v_div_fixup_f32 v218, v1, v68, 1.0
	v_div_scale_f32 v1, s[0:1], v69, v69, 1.0
	v_rcp_f32_e32 v2, v1
	s_nop 0
	v_fma_f32 v68, -v1, v2, 1.0
	v_fmac_f32_e32 v2, v68, v2
	v_div_scale_f32 v68, vcc, 1.0, v69, 1.0
	v_mul_f32_e32 v72, v68, v2
	v_fma_f32 v73, -v1, v72, v68
	v_fmac_f32_e32 v72, v73, v2
	v_fma_f32 v1, -v1, v72, v68
	v_div_fmas_f32 v1, v1, v2, v72
	v_div_fixup_f32 v220, v1, v69, 1.0
	v_div_scale_f32 v1, s[0:1], v70, v70, 1.0
	v_rcp_f32_e32 v2, v1
	s_nop 0
	v_fma_f32 v68, -v1, v2, 1.0
	v_fmac_f32_e32 v2, v68, v2
	v_div_scale_f32 v68, vcc, 1.0, v70, 1.0
	v_mul_f32_e32 v69, v68, v2
	v_fma_f32 v72, -v1, v69, v68
	v_fmac_f32_e32 v69, v72, v2
	v_fma_f32 v1, -v1, v69, v68
	v_div_fmas_f32 v1, v1, v2, v69
	v_div_fixup_f32 v222, v1, v70, 1.0
	v_div_scale_f32 v1, s[0:1], v71, v71, 1.0
	v_rcp_f32_e32 v2, v1
	s_nop 0
	v_fma_f32 v68, -v1, v2, 1.0
	v_fmac_f32_e32 v2, v68, v2
	v_div_scale_f32 v68, vcc, 1.0, v71, 1.0
	v_mul_f32_e32 v69, v68, v2
	v_fma_f32 v70, -v1, v69, v68
	v_fmac_f32_e32 v69, v70, v2
	v_fma_f32 v1, -v1, v69, v68
	v_div_fmas_f32 v1, v1, v2, v69
	v_div_fixup_f32 v224, v1, v71, 1.0
	ds_read_b128 v[68:71], v187 offset:96
	s_waitcnt lgkmcnt(0)
	s_barrier
; __device__ __forceinline__ int crow(int r, int hi) { return (r & 3) + 8 * (r >> 2) + 4 * hi; }
; template <bool MOBA>
; __device__ __forceinline__ void run_unit(const UnitDesc& U, LAS unsigned char* lds, f32x16 (&o)[4], float (&rli)[16]) {
;     ...
;     for (int r = 0; r < 16; ++r) rli[r] = 1.0f / li_l[crow(r, hi)];
;     __syncthreads();
; __global__ void __launch_bounds__(NWAVES * 64, 2) mega_fwd(Args args) {
;     ...
;                         int lane_p = threadIdx.x & 63; asm volatile("" : "+v"(lane_p)); const int r32 = lane_p & 31, hi = lane_p >> 5;
;                         float* sp = S1 + (size_t)(wave * 64 + lane_p) * 64;
	v_div_scale_f32 v1, s[0:1], v68, v68, 1.0
	v_rcp_f32_e32 v2, v1
	s_nop 0
	v_fma_f32 v72, -v1, v2, 1.0
	v_fmac_f32_e32 v2, v72, v2
	v_div_scale_f32 v72, vcc, 1.0, v68, 1.0
	v_mul_f32_e32 v73, v72, v2
	v_fma_f32 v74, -v1, v73, v72
	v_fmac_f32_e32 v73, v74, v2
	v_fma_f32 v1, -v1, v73, v72
	v_div_fmas_f32 v1, v1, v2, v73
	v_div_fixup_f32 v226, v1, v68, 1.0
	v_div_scale_f32 v1, s[0:1], v69, v69, 1.0
	v_rcp_f32_e32 v2, v1
	s_nop 0
	v_fma_f32 v68, -v1, v2, 1.0
	v_fmac_f32_e32 v2, v68, v2
	v_div_scale_f32 v68, vcc, 1.0, v69, 1.0
	v_mul_f32_e32 v72, v68, v2
	v_fma_f32 v73, -v1, v72, v68
	v_fmac_f32_e32 v72, v73, v2
	v_fma_f32 v1, -v1, v72, v68
	v_div_fmas_f32 v1, v1, v2, v72
	v_div_fixup_f32 v228, v1, v69, 1.0
	v_div_scale_f32 v1, s[0:1], v70, v70, 1.0
	v_rcp_f32_e32 v2, v1
	s_nop 0
	v_fma_f32 v68, -v1, v2, 1.0
	v_fmac_f32_e32 v2, v68, v2
	v_div_scale_f32 v68, vcc, 1.0, v70, 1.0
	v_mul_f32_e32 v69, v68, v2
	v_fma_f32 v72, -v1, v69, v68
	v_fmac_f32_e32 v69, v72, v2
	v_fma_f32 v1, -v1, v69, v68
	v_div_fmas_f32 v1, v1, v2, v69
	v_div_fixup_f32 v230, v1, v70, 1.0
	v_div_scale_f32 v1, s[0:1], v71, v71, 1.0
	v_rcp_f32_e32 v2, v1
	v_readlane_b32 s0, v254, 32
	v_fma_f32 v68, -v1, v2, 1.0
	v_fmac_f32_e32 v2, v68, v2
	v_div_scale_f32 v68, vcc, 1.0, v71, 1.0
	v_mul_f32_e32 v69, v68, v2
	v_fma_f32 v70, -v1, v69, v68
	v_fmac_f32_e32 v69, v70, v2
	v_fma_f32 v1, -v1, v69, v68
	v_mov_b32_e32 v68, s0
	v_lshlrev_b32_e32 v68, 8, v68
	v_lshl_add_u32 v68, v238, 4, v68
	v_add_u32_e32 v68, 0x1000, v68
	v_div_fmas_f32 v1, v1, v2, v69
	v_ashrrev_i32_e32 v69, 31, v68
	v_readlane_b32 s0, v254, 26
	v_div_fixup_f32 v232, v1, v71, 1.0
	v_lshlrev_b64 v[70:71], 0, v[68:69]
	v_readlane_b32 s1, v254, 27
	s_nop 1
	v_lshl_add_u64 v[234:235], s[0:1], 0, v[70:71]
	s_mov_b64 s[0:1], -1
	s_cbranch_scc1 .LBB0_854
	s_mov_b32 s85, 0xffff0000
	s_andn2_b64 vcc, exec, s[0:1]
	s_cbranch_vccnz .LBB0_799
	s_branch .LBB0_1115

; #define LAS __attribute__((address_space(3)))
; __device__ __forceinline__ void stage_load(u32x4 (&v)[16], const bf16_t* src, int row_stride, int wave, int lane) {
;     const bf16_t* p = src + (size_t)(wave * 2 + (lane >> 5)) * row_stride + (lane & 31) * 8;
; #pragma unroll
;     for (int i = 0; i < 16; ++i) v[i] = *(const u32x4*)(p + (size_t)(16 * i) * row_stride);
; }
; __device__ __forceinline__ void stage_store(const u32x4 (&v)[16], LAS unsigned char* lds, int wave, int lane) {
;     const int c = lane & 31, r0 = wave * 2 + (lane >> 5);
; #pragma unroll
;     for (int i = 0; i < 16; ++i) { const int r = r0 + 16 * i; *(LAS u32x4*)(lds + r * 512 + ((c ^ (r & 31)) << 4)) = v[i]; }
; }
; __device__ __forceinline__ void unit(const bf16_t* proj, const bf16_t* mk, const bf16_t* mvt, bf16_t* Y3, int un, LAS unsigned char* lds) {
;     int tid_l = threadIdx.x; asm volatile("" : "+v"(tid_l));
;     const int tid = tid_l, wave = __builtin_amdgcn_readfirstlane(tid >> 6), lane = tid & 63, r32 = lane & 31, hi = lane >> 5;
;     const int tk = un * 8 + wave, rb = tk & 63, h = (tk >> 6) & 3, b = tk >> 8, bt0 = b * SEQ + rb * 32;
;     u32x4 st[16]; att::bf16x8 qr[16];
;     stage_load(st, mk + (size_t)(b * MEML) * 2048 + h * 256, 2048, wave, lane);
;     const bf16_t* qp = proj + (size_t)(bt0 + r32) * NC + C_QM + h * 256 + hi * 8;
; #pragma unroll
;     for (int d0 = 0; d0 < 16; ++d0) qr[d0] = *(const att::bf16x8*)(qp + d0 * 16);
.LBB0_1117:
	s_andn2_b64 vcc, exec, s[0:1]
	s_cbranch_vccnz .LBB0_1375
	v_mov_b32_e32 v220, v0
	s_mov_b32 s11, 0xe800
	v_readfirstlane_b32 s0, v220
	s_ashr_i32 s6, s0, 6
	v_readlane_b32 s0, v254, 47
	s_lshl_b32 s0, s0, 3
	s_add_i32 s0, s0, s6
	s_addk_i32 s0, 0xf400
	s_ashr_i32 s8, s0, 8
	s_lshl_b32 s2, s0, 5
	s_and_b32 s4, s0, 0xffffff00
	s_lshl_b32 s1, s8, 11
	s_and_b32 s2, s2, 0x7e0
	s_ashr_i32 s5, s4, 31
	s_or_b32 s1, s1, s2
	s_lshl_b64 s[4:5], s[4:5], 12
	v_readlane_b32 s2, v253, 59
	s_add_u32 s4, s2, s4
	v_readlane_b32 s2, v253, 60
	s_addc_u32 s5, s2, s5
	s_lshl_b32 s0, s0, 2
	s_and_b32 s0, s0, 0x300
	s_lshl_b32 s2, s0, 1
	s_add_u32 s4, s4, s2
	v_bfe_u32 v200, v220, 5, 1
	s_addc_u32 s5, s5, 0
	s_lshl_b32 s6, s6, 1
	v_or_b32_e32 v198, s6, v200
	v_ashrrev_i32_e32 v199, 31, v198
	v_lshlrev_b64 v[4:5], 12, v[198:199]
	v_lshlrev_b32_e32 v2, 4, v220
	v_lshl_add_u64 v[4:5], s[4:5], 0, v[4:5]
	v_and_b32_e32 v2, 0x1f0, v2
	v_lshl_add_u64 v[60:61], v[4:5], 0, v[2:3]
	v_add_co_u32_e32 v8, vcc, s84, v60
	s_mov_b32 s4, 0x20000
	s_nop 0
	v_addc_co_u32_e32 v9, vcc, 0, v61, vcc
	s_waitcnt lgkmcnt(0)
	global_load_dwordx4 v[4:7], v[60:61], off
	s_nop 0
	global_load_dwordx4 v[8:11], v[8:9], off
	v_add_co_u32_e32 v12, vcc, s4, v60
	s_mov_b32 s4, 0x30000
	s_nop 0
	v_addc_co_u32_e32 v13, vcc, 0, v61, vcc
	v_add_co_u32_e32 v16, vcc, s4, v60
	s_mov_b32 s4, 0x40000
	s_nop 0
	v_addc_co_u32_e32 v17, vcc, 0, v61, vcc
	v_add_co_u32_e32 v20, vcc, s4, v60
	s_mov_b32 s4, 0x50000
	s_nop 0
	v_addc_co_u32_e32 v21, vcc, 0, v61, vcc
	v_add_co_u32_e32 v24, vcc, s4, v60
	s_mov_b32 s4, 0x60000
	s_nop 0
	v_addc_co_u32_e32 v25, vcc, 0, v61, vcc
	v_add_co_u32_e32 v28, vcc, s4, v60
	s_mov_b32 s4, 0x70000
	s_nop 0
	v_addc_co_u32_e32 v29, vcc, 0, v61, vcc
	v_add_co_u32_e32 v32, vcc, s4, v60
	s_mov_b32 s4, 0x80000
	s_nop 0
	v_addc_co_u32_e32 v33, vcc, 0, v61, vcc
	v_add_co_u32_e32 v36, vcc, s4, v60
	s_mov_b32 s4, 0x90000
	s_nop 0
	v_addc_co_u32_e32 v37, vcc, 0, v61, vcc
	v_add_co_u32_e32 v40, vcc, s4, v60
	s_mov_b32 s4, 0xa0000
	s_nop 0
	v_addc_co_u32_e32 v41, vcc, 0, v61, vcc
	v_add_co_u32_e32 v44, vcc, s4, v60
	s_mov_b32 s4, 0xb0000
	s_nop 0
	v_addc_co_u32_e32 v45, vcc, 0, v61, vcc
	v_add_co_u32_e32 v48, vcc, s4, v60
	s_mov_b32 s4, 0xc0000
	s_nop 0
	v_addc_co_u32_e32 v49, vcc, 0, v61, vcc
	v_add_co_u32_e32 v52, vcc, s4, v60
	s_mov_b32 s4, 0xd0000
	s_nop 0
	v_addc_co_u32_e32 v53, vcc, 0, v61, vcc
	v_add_co_u32_e32 v56, vcc, s4, v60
	s_mov_b32 s4, 0xe0000
	s_nop 0
	v_addc_co_u32_e32 v57, vcc, 0, v61, vcc
	v_add_co_u32_e32 v62, vcc, s4, v60
	s_mov_b32 s4, 0xf0000
	s_nop 0
	v_addc_co_u32_e32 v63, vcc, 0, v61, vcc
	v_add_co_u32_e32 v64, vcc, s4, v60
	global_load_dwordx4 v[12:15], v[12:13], off
	s_nop 0
	global_load_dwordx4 v[16:19], v[16:17], off
	v_addc_co_u32_e32 v65, vcc, 0, v61, vcc
	global_load_dwordx4 v[20:23], v[20:21], off
	s_nop 0
	global_load_dwordx4 v[24:27], v[24:25], off
	s_nop 0
	global_load_dwordx4 v[28:31], v[28:29], off
	s_nop 0
	global_load_dwordx4 v[32:35], v[32:33], off
	s_nop 0
	global_load_dwordx4 v[36:39], v[36:37], off
	s_nop 0
	global_load_dwordx4 v[40:43], v[40:41], off
	s_nop 0
	global_load_dwordx4 v[44:47], v[44:45], off
	s_nop 0
	global_load_dwordx4 v[48:51], v[48:49], off
	s_nop 0
	global_load_dwordx4 v[52:55], v[52:53], off
	s_nop 0
	global_load_dwordx4 v[56:59], v[56:57], off
	s_nop 0
	global_load_dwordx4 v[60:63], v[62:63], off
	s_nop 0
	global_load_dwordx4 v[64:67], v[64:65], off
	v_readlane_b32 s4, v253, 48
	s_waitcnt vmcnt(16)
	v_and_b32_e32 v1, 31, v220
	v_readlane_b32 s5, v253, 49
	v_or_b32_e32 v68, s1, v1
	v_lshlrev_b32_e32 v70, 4, v200
	v_mov_b64_e32 v[196:197], s[4:5]
	v_mad_i64_i32 v[68:69], s[4:5], v68, s11, v[196:197]
	v_lshl_add_u64 v[68:69], v[68:69], 0, s[2:3]
	v_mov_b32_e32 v71, v3
	v_lshl_add_u64 v[68:69], v[68:69], 0, v[70:71]
	s_mov_b64 s[4:5], 0x5800
	v_lshl_add_u64 v[70:71], v[68:69], 0, s[4:5]
	s_movk_i32 s4, 0x5000
	v_add_co_u32_e32 v68, vcc, s4, v68
	v_or_b32_e32 v209, 2, v200
	s_nop 0
	v_addc_co_u32_e32 v69, vcc, 0, v69, vcc
	global_load_dwordx4 v[188:191], v[70:71], off offset:32
	global_load_dwordx4 v[184:187], v[70:71], off offset:64
	global_load_dwordx4 v[180:183], v[70:71], off offset:96
	global_load_dwordx4 v[176:179], v[70:71], off offset:128
	global_load_dwordx4 v[172:175], v[70:71], off offset:160
	global_load_dwordx4 v[168:171], v[70:71], off offset:192
	global_load_dwordx4 v[164:167], v[70:71], off offset:224
	global_load_dwordx4 v[160:163], v[70:71], off offset:256
	global_load_dwordx4 v[156:159], v[70:71], off offset:288
	global_load_dwordx4 v[152:155], v[70:71], off offset:320
	global_load_dwordx4 v[148:151], v[70:71], off offset:352
	global_load_dwordx4 v[144:147], v[70:71], off offset:384
	global_load_dwordx4 v[140:143], v[70:71], off offset:416
	global_load_dwordx4 v[136:139], v[70:71], off offset:448
	global_load_dwordx4 v[116:119], v[68:69], off offset:2048
	global_load_dwordx4 v[132:135], v[70:71], off offset:480
	v_bitop3_b32 v69, s6, v220, v200 bitop3:0x36
	v_lshlrev_b32_e32 v69, 4, v69
	v_lshlrev_b32_e32 v68, 9, v198
	v_and_b32_e32 v69, 0x1f0, v69
	v_add3_u32 v222, 0, v68, v69
	s_waitcnt vmcnt(31)
; #define LAS __attribute__((address_space(3)))
; __device__ __forceinline__ void stage_store(const u32x4 (&v)[16], LAS unsigned char* lds, int wave, int lane) {
;     const int c = lane & 31, r0 = wave * 2 + (lane >> 5);
; #pragma unroll
;     for (int i = 0; i < 16; ++i) { const int r = r0 + 16 * i; *(LAS u32x4*)(lds + r * 512 + ((c ^ (r & 31)) << 4)) = v[i]; }
; }
; __device__ __forceinline__ void unit(const bf16_t* proj, const bf16_t* mk, const bf16_t* mvt, bf16_t* Y3, int un, LAS unsigned char* lds) {
;     int tid_l = threadIdx.x; asm volatile("" : "+v"(tid_l));
;     const int tid = tid_l, wave = __builtin_amdgcn_readfirstlane(tid >> 6), lane = tid & 63, r32 = lane & 31, hi = lane >> 5;
;     const int tk = un * 8 + wave, rb = tk & 63, h = (tk >> 6) & 3, b = tk >> 8, bt0 = b * SEQ + rb * 32;
;     u32x4 st[16]; att::bf16x8 qr[16];
;     stage_load(st, mk + (size_t)(b * MEML) * 2048 + h * 256, 2048, wave, lane);
;     const bf16_t* qp = proj + (size_t)(bt0 + r32) * NC + C_QM + h * 256 + hi * 8;
; #pragma unroll
;     for (int d0 = 0; d0 < 16; ++d0) qr[d0] = *(const att::bf16x8*)(qp + d0 * 16);
;     asm volatile("" ::: "memory");
;     stage_store(st, lds, wave, lane);
;     __syncthreads();
;     att::f32x16 s[8];
; #pragma unroll
;     for (int kb = 0; kb < 8; ++kb) { s[kb] = att::f32x16{};
; #pragma unroll
;         for (int q2 = 0; q2 < 8; ++q2) { att::bf16x8 kf[2]; int rv = r32; asm volatile("" : "+v"(rv));
; #pragma unroll
;             for (int i = 0; i < 2; ++i) kf[i] = frag(lds, kb * 32 + rv, 2 * (q2 * 2 + i) + hi);
;             asm volatile("" ::: "memory");
; #pragma unroll
;             for (int i = 0; i < 2; ++i) s[kb] = __builtin_amdgcn_mfma_f32_32x32x16_bf16(kf[i], qr[q2 * 2 + i], s[kb], 0, 0, 0); } }
	ds_write_b128 v222, v[4:7]
	v_add_u32_e32 v4, 16, v198
	v_lshlrev_b32_e32 v5, 9, v4
	v_xor_b32_e32 v4, v4, v220
	v_lshlrev_b32_e32 v4, 4, v4
	v_and_b32_e32 v4, 0x1f0, v4
	v_add3_u32 v224, 0, v5, v4
	v_add_u32_e32 v4, 48, v198
	v_lshlrev_b32_e32 v5, 9, v4
	v_xor_b32_e32 v4, v4, v220
	v_lshlrev_b32_e32 v4, 4, v4
	v_and_b32_e32 v4, 0x1f0, v4
	v_add3_u32 v226, 0, v5, v4
	v_add_u32_e32 v4, 0x50, v198
	v_lshlrev_b32_e32 v5, 9, v4
	v_xor_b32_e32 v4, v4, v220
	v_lshlrev_b32_e32 v4, 4, v4
	v_and_b32_e32 v4, 0x1f0, v4
	v_add3_u32 v228, 0, v5, v4
	v_add_u32_e32 v4, 0x70, v198
	v_lshlrev_b32_e32 v5, 9, v4
	v_xor_b32_e32 v4, v4, v220
	v_lshlrev_b32_e32 v4, 4, v4
	v_and_b32_e32 v4, 0x1f0, v4
	v_add3_u32 v230, 0, v5, v4
	v_add_u32_e32 v4, 0x90, v198
	v_lshlrev_b32_e32 v5, 9, v4
	v_xor_b32_e32 v4, v4, v220
	v_lshlrev_b32_e32 v4, 4, v4
	v_and_b32_e32 v4, 0x1f0, v4
	v_add3_u32 v240, 0, v5, v4
	v_add_u32_e32 v4, 0xb0, v198
	v_lshlrev_b32_e32 v5, 9, v4
	v_xor_b32_e32 v4, v4, v220
	v_lshlrev_b32_e32 v4, 4, v4
	v_and_b32_e32 v4, 0x1f0, v4
	v_add3_u32 v250, 0, v5, v4
	v_add_u32_e32 v4, 0xd0, v198
	v_lshlrev_b32_e32 v5, 9, v4
	v_xor_b32_e32 v4, v4, v220
	v_lshlrev_b32_e32 v4, 4, v4
	v_and_b32_e32 v4, 0x1f0, v4
	v_add3_u32 v194, 0, v5, v4
	v_add_u32_e32 v4, 0xf0, v198
	v_lshlrev_b32_e32 v5, 9, v4
	v_xor_b32_e32 v4, v4, v220
	v_lshlrev_b32_e32 v4, 4, v4
	v_and_b32_e32 v4, 0x1f0, v4
	s_waitcnt vmcnt(30)
	ds_write_b128 v224, v[8:11]
	s_waitcnt vmcnt(29)
	ds_write_b128 v222, v[12:15] offset:16384
	v_add_u32_e32 v223, 0x10000, v222
	v_add_u32_e32 v245, 0x14000, v222
	v_add_u32_e32 v251, 0x18000, v222
	v_add_u32_e32 v195, 0x1c000, v222
	v_add3_u32 v244, 0, v5, v4
	v_mov_b32_e32 v8, v1
	s_waitcnt vmcnt(28)
	ds_write_b128 v226, v[16:19]
	s_waitcnt vmcnt(27)
	ds_write_b128 v222, v[20:23] offset:32768
	s_waitcnt vmcnt(26)
	ds_write_b128 v228, v[24:27]
	s_waitcnt vmcnt(25)
	ds_write_b128 v222, v[28:31] offset:49152
	s_waitcnt vmcnt(24)
	ds_write_b128 v230, v[32:35]
	s_waitcnt vmcnt(23)
	ds_write_b128 v223, v[36:39]
	s_waitcnt vmcnt(22)
	ds_write_b128 v240, v[40:43]
	s_waitcnt vmcnt(21)
	ds_write_b128 v245, v[44:47]
	s_waitcnt vmcnt(20)
	ds_write_b128 v250, v[48:51]
	s_waitcnt vmcnt(19)
	ds_write_b128 v251, v[52:55]
	s_waitcnt vmcnt(18)
	ds_write_b128 v194, v[56:59]
	s_waitcnt vmcnt(17)
	ds_write_b128 v195, v[60:63]
	s_waitcnt vmcnt(16)
	ds_write_b128 v244, v[64:67]
	s_waitcnt lgkmcnt(0)
	s_barrier
	v_mov_b32_e32 v24, v1
	v_lshl_add_u32 v9, v8, 9, 0
	v_bitop3_b32 v4, v8, v200, 31 bitop3:0x6c
	v_lshl_add_u32 v4, v4, 4, v9
	ds_read_b128 v[4:7], v4
	v_bitop3_b32 v8, v8, v209, 31 bitop3:0x6c
	v_lshl_add_u32 v20, v8, 4, v9
	ds_read_b128 v[20:23], v20
	s_waitcnt vmcnt(1) lgkmcnt(1)
	s_setprio 1
	v_mfma_f32_32x32x16_bf16 v[4:19], v[4:7], v[116:119], 0
	v_or_b32_e32 v218, 4, v200
	v_or_b32_e32 v214, 6, v200
	v_lshl_add_u32 v25, v24, 9, 0
	v_or_b32_e32 v217, 8, v200
	v_or_b32_e32 v206, 10, v200
	s_waitcnt lgkmcnt(0)
	v_mfma_f32_32x32x16_bf16 v[4:19], v[20:23], v[188:191], v[4:19]
	v_bitop3_b32 v20, v24, v218, 31 bitop3:0x6c
	v_lshl_add_u32 v20, v20, 4, v25
	ds_read_b128 v[20:23], v20
	v_bitop3_b32 v24, v24, v214, 31 bitop3:0x6c
	v_lshl_add_u32 v24, v24, 4, v25
	v_or_b32_e32 v216, 12, v200
	v_or_b32_e32 v211, 14, v200
	s_waitcnt lgkmcnt(0)
	v_mfma_f32_32x32x16_bf16 v[4:19], v[20:23], v[184:187], v[4:19]
	ds_read_b128 v[20:23], v24
	v_mov_b32_e32 v24, v1
	v_or_b32_e32 v215, 16, v200
	v_lshl_add_u32 v25, v24, 9, 0
	v_or_b32_e32 v202, 18, v200
	s_waitcnt lgkmcnt(0)
	v_mfma_f32_32x32x16_bf16 v[4:19], v[20:23], v[180:183], v[4:19]
	v_bitop3_b32 v20, v24, v217, 31 bitop3:0x6c
	v_lshl_add_u32 v20, v20, 4, v25
	ds_read_b128 v[20:23], v20
	v_bitop3_b32 v24, v24, v206, 31 bitop3:0x6c
	v_lshl_add_u32 v24, v24, 4, v25
	v_or_b32_e32 v213, 20, v200
	v_or_b32_e32 v208, 22, v200
	s_waitcnt lgkmcnt(0)
	v_mfma_f32_32x32x16_bf16 v[4:19], v[20:23], v[176:179], v[4:19]
	ds_read_b128 v[20:23], v24
	v_mov_b32_e32 v24, v1
	v_or_b32_e32 v212, 24, v200
	v_lshl_add_u32 v25, v24, 9, 0
	v_or_b32_e32 v201, 26, v200
	s_waitcnt lgkmcnt(0)
	v_mfma_f32_32x32x16_bf16 v[4:19], v[20:23], v[172:175], v[4:19]
	v_bitop3_b32 v20, v24, v216, 31 bitop3:0x6c
	v_lshl_add_u32 v20, v20, 4, v25
	ds_read_b128 v[20:23], v20
	v_bitop3_b32 v24, v24, v211, 31 bitop3:0x6c
	v_lshl_add_u32 v24, v24, 4, v25
	v_or_b32_e32 v210, 28, v200
	v_or_b32_e32 v204, 30, v200
	s_waitcnt lgkmcnt(0)
	v_mfma_f32_32x32x16_bf16 v[4:19], v[20:23], v[168:171], v[4:19]
	ds_read_b128 v[20:23], v24
	v_mov_b32_e32 v24, v1
	v_mov_b32_e32 v40, v1
	v_lshl_add_u32 v25, v24, 9, 0
	v_mov_b32_e32 v56, v1
	s_waitcnt lgkmcnt(0)
	v_mfma_f32_32x32x16_bf16 v[4:19], v[20:23], v[164:167], v[4:19]
	v_bitop3_b32 v20, v24, v215, 31 bitop3:0x6c
	v_lshl_add_u32 v20, v20, 4, v25
	ds_read_b128 v[20:23], v20
	v_bitop3_b32 v24, v24, v202, 31 bitop3:0x6c
	v_lshl_add_u32 v24, v24, 4, v25
	v_mov_b32_e32 v72, v1
	s_add_i32 s7, 0, 0x10000
	s_waitcnt lgkmcnt(0)
	v_mfma_f32_32x32x16_bf16 v[4:19], v[20:23], v[160:163], v[4:19]
	ds_read_b128 v[20:23], v24
	v_mov_b32_e32 v24, v1
	v_mov_b32_e32 v88, v1
	v_lshl_add_u32 v25, v24, 9, 0
	s_add_i32 s6, 0, 0x14000
	s_waitcnt lgkmcnt(0)
	v_mfma_f32_32x32x16_bf16 v[4:19], v[20:23], v[156:159], v[4:19]
	v_bitop3_b32 v20, v24, v213, 31 bitop3:0x6c
	v_lshl_add_u32 v20, v20, 4, v25
	ds_read_b128 v[20:23], v20
	v_bitop3_b32 v24, v24, v208, 31 bitop3:0x6c
	v_lshl_add_u32 v24, v24, 4, v25
	v_mov_b32_e32 v104, v1
	s_add_i32 s5, 0, 0x18000
	s_waitcnt lgkmcnt(0)
	v_mfma_f32_32x32x16_bf16 v[4:19], v[20:23], v[152:155], v[4:19]
	ds_read_b128 v[20:23], v24
	v_mov_b32_e32 v24, v1
	v_mov_b32_e32 v124, v1
	v_lshl_add_u32 v25, v24, 9, 0
	s_add_i32 s4, 0, 0x1c000
	s_waitcnt lgkmcnt(0)
; __device__ __forceinline__ void unit(const bf16_t* proj, const bf16_t* mk, const bf16_t* mvt, bf16_t* Y3, int un, LAS unsigned char* lds) {
;     ...
;     for (int kb = 0; kb < 8; ++kb) { s[kb] = att::f32x16{};
; #pragma unroll
;         for (int q2 = 0; q2 < 8; ++q2) { att::bf16x8 kf[2]; int rv = r32; asm volatile("" : "+v"(rv));
; #pragma unroll
;             for (int i = 0; i < 2; ++i) kf[i] = frag(lds, kb * 32 + rv, 2 * (q2 * 2 + i) + hi);
;             asm volatile("" ::: "memory");
; #pragma unroll
;             for (int i = 0; i < 2; ++i) s[kb] = __builtin_amdgcn_mfma_f32_32x32x16_bf16(kf[i], qr[q2 * 2 + i], s[kb], 0, 0, 0); } }
	v_mfma_f32_32x32x16_bf16 v[4:19], v[20:23], v[148:151], v[4:19]
	v_bitop3_b32 v20, v24, v212, 31 bitop3:0x6c
	v_lshl_add_u32 v20, v20, 4, v25
	ds_read_b128 v[20:23], v20
	v_bitop3_b32 v24, v24, v201, 31 bitop3:0x6c
	v_lshl_add_u32 v24, v24, 4, v25
	s_mov_b32 s9, 0xff800000
	s_lshl_b32 s8, s8, 10
	s_waitcnt lgkmcnt(0)
	v_mfma_f32_32x32x16_bf16 v[4:19], v[20:23], v[144:147], v[4:19]
	ds_read_b128 v[20:23], v24
	v_mov_b32_e32 v24, v1
	s_or_b32 s8, s8, s0
	v_lshl_add_u32 v25, v24, 9, 0
	v_readlane_b32 s10, v254, 33
	s_waitcnt lgkmcnt(0)
	v_mfma_f32_32x32x16_bf16 v[4:19], v[20:23], v[140:143], v[4:19]
	v_bitop3_b32 v20, v24, v210, 31 bitop3:0x6c
	v_lshl_add_u32 v20, v20, 4, v25
	ds_read_b128 v[20:23], v20
	v_bitop3_b32 v24, v24, v204, 31 bitop3:0x6c
	v_lshl_add_u32 v24, v24, 4, v25
	s_mov_b64 s[12:13], 0x6000
	s_waitcnt lgkmcnt(0)
	v_mfma_f32_32x32x16_bf16 v[4:19], v[20:23], v[136:139], v[4:19]
	ds_read_b128 v[20:23], v24
	v_mov_b32_e32 v24, v1
	s_nop 0
	v_lshl_add_u32 v25, v24, 9, 0
	s_waitcnt vmcnt(0) lgkmcnt(0)
	v_mfma_f32_32x32x16_bf16 v[4:19], v[20:23], v[132:135], v[4:19]
	v_bitop3_b32 v20, v24, v200, 31 bitop3:0x6c
	v_lshl_add_u32 v20, v20, 4, v25
	ds_read_b128 v[20:23], v20 offset:16384
	v_bitop3_b32 v24, v24, v209, 31 bitop3:0x6c
	v_lshl_add_u32 v36, v24, 4, v25
	ds_read_b128 v[36:39], v36 offset:16384
	s_waitcnt lgkmcnt(1)
	v_mfma_f32_32x32x16_bf16 v[20:35], v[20:23], v[116:119], 0
	s_nop 0
	v_lshl_add_u32 v41, v40, 9, 0
	s_waitcnt lgkmcnt(0)
	v_mfma_f32_32x32x16_bf16 v[20:35], v[36:39], v[188:191], v[20:35]
	v_bitop3_b32 v36, v40, v218, 31 bitop3:0x6c
	v_lshl_add_u32 v36, v36, 4, v41
	ds_read_b128 v[36:39], v36 offset:16384
	v_bitop3_b32 v40, v40, v214, 31 bitop3:0x6c
	v_lshl_add_u32 v40, v40, 4, v41
	s_waitcnt lgkmcnt(0)
	v_mfma_f32_32x32x16_bf16 v[20:35], v[36:39], v[184:187], v[20:35]
	ds_read_b128 v[36:39], v40 offset:16384
	v_mov_b32_e32 v40, v1
	s_nop 0
	v_lshl_add_u32 v41, v40, 9, 0
	s_waitcnt lgkmcnt(0)
	v_mfma_f32_32x32x16_bf16 v[20:35], v[36:39], v[180:183], v[20:35]
	v_bitop3_b32 v36, v40, v217, 31 bitop3:0x6c
	v_lshl_add_u32 v36, v36, 4, v41
	ds_read_b128 v[36:39], v36 offset:16384
	v_bitop3_b32 v40, v40, v206, 31 bitop3:0x6c
	v_lshl_add_u32 v40, v40, 4, v41
	s_waitcnt lgkmcnt(0)
	v_mfma_f32_32x32x16_bf16 v[20:35], v[36:39], v[176:179], v[20:35]
	ds_read_b128 v[36:39], v40 offset:16384
	v_mov_b32_e32 v40, v1
	s_nop 0
	v_lshl_add_u32 v41, v40, 9, 0
	s_waitcnt lgkmcnt(0)
	v_mfma_f32_32x32x16_bf16 v[20:35], v[36:39], v[172:175], v[20:35]
	v_bitop3_b32 v36, v40, v216, 31 bitop3:0x6c
	v_lshl_add_u32 v36, v36, 4, v41
	ds_read_b128 v[36:39], v36 offset:16384
	v_bitop3_b32 v40, v40, v211, 31 bitop3:0x6c
	v_lshl_add_u32 v40, v40, 4, v41
	s_waitcnt lgkmcnt(0)
	v_mfma_f32_32x32x16_bf16 v[20:35], v[36:39], v[168:171], v[20:35]
	ds_read_b128 v[36:39], v40 offset:16384
	v_mov_b32_e32 v40, v1
	s_nop 0
	v_lshl_add_u32 v41, v40, 9, 0
	s_waitcnt lgkmcnt(0)
	v_mfma_f32_32x32x16_bf16 v[20:35], v[36:39], v[164:167], v[20:35]
	v_bitop3_b32 v36, v40, v215, 31 bitop3:0x6c
	v_lshl_add_u32 v36, v36, 4, v41
	ds_read_b128 v[36:39], v36 offset:16384
	v_bitop3_b32 v40, v40, v202, 31 bitop3:0x6c
	v_lshl_add_u32 v40, v40, 4, v41
	s_waitcnt lgkmcnt(0)
	v_mfma_f32_32x32x16_bf16 v[20:35], v[36:39], v[160:163], v[20:35]
	ds_read_b128 v[36:39], v40 offset:16384
	v_mov_b32_e32 v40, v1
	s_nop 0
	v_lshl_add_u32 v41, v40, 9, 0
	s_waitcnt lgkmcnt(0)
	v_mfma_f32_32x32x16_bf16 v[20:35], v[36:39], v[156:159], v[20:35]
	v_bitop3_b32 v36, v40, v213, 31 bitop3:0x6c
	v_lshl_add_u32 v36, v36, 4, v41
	ds_read_b128 v[36:39], v36 offset:16384
	v_bitop3_b32 v40, v40, v208, 31 bitop3:0x6c
	v_lshl_add_u32 v40, v40, 4, v41
	s_waitcnt lgkmcnt(0)
	v_mfma_f32_32x32x16_bf16 v[20:35], v[36:39], v[152:155], v[20:35]
	ds_read_b128 v[36:39], v40 offset:16384
	v_mov_b32_e32 v40, v1
	s_nop 0
	v_lshl_add_u32 v41, v40, 9, 0
	s_waitcnt lgkmcnt(0)
	v_mfma_f32_32x32x16_bf16 v[20:35], v[36:39], v[148:151], v[20:35]
	v_bitop3_b32 v36, v40, v212, 31 bitop3:0x6c
	v_lshl_add_u32 v36, v36, 4, v41
	ds_read_b128 v[36:39], v36 offset:16384
	v_bitop3_b32 v40, v40, v201, 31 bitop3:0x6c
	v_lshl_add_u32 v40, v40, 4, v41
	s_waitcnt lgkmcnt(0)
	v_mfma_f32_32x32x16_bf16 v[20:35], v[36:39], v[144:147], v[20:35]
	ds_read_b128 v[36:39], v40 offset:16384
	v_mov_b32_e32 v40, v1
	s_nop 0
	v_lshl_add_u32 v41, v40, 9, 0
	s_waitcnt lgkmcnt(0)
	v_mfma_f32_32x32x16_bf16 v[20:35], v[36:39], v[140:143], v[20:35]
	v_bitop3_b32 v36, v40, v210, 31 bitop3:0x6c
	v_lshl_add_u32 v36, v36, 4, v41
	ds_read_b128 v[36:39], v36 offset:16384
	v_bitop3_b32 v40, v40, v204, 31 bitop3:0x6c
	v_lshl_add_u32 v40, v40, 4, v41
	s_waitcnt lgkmcnt(0)
	v_mfma_f32_32x32x16_bf16 v[20:35], v[36:39], v[136:139], v[20:35]
	ds_read_b128 v[36:39], v40 offset:16384
	v_mov_b32_e32 v40, v1
	s_nop 0
	v_lshl_add_u32 v41, v40, 9, 0
	s_waitcnt lgkmcnt(0)
	v_mfma_f32_32x32x16_bf16 v[20:35], v[36:39], v[132:135], v[20:35]
	v_bitop3_b32 v36, v40, v200, 31 bitop3:0x6c
	v_lshl_add_u32 v36, v36, 4, v41
	ds_read_b128 v[36:39], v36 offset:32768
	v_bitop3_b32 v40, v40, v209, 31 bitop3:0x6c
	v_lshl_add_u32 v52, v40, 4, v41
	ds_read_b128 v[52:55], v52 offset:32768
	s_waitcnt lgkmcnt(1)
	v_mfma_f32_32x32x16_bf16 v[36:51], v[36:39], v[116:119], 0
	s_nop 0
	v_lshl_add_u32 v57, v56, 9, 0
	s_waitcnt lgkmcnt(0)
	v_mfma_f32_32x32x16_bf16 v[36:51], v[52:55], v[188:191], v[36:51]
	v_bitop3_b32 v52, v56, v218, 31 bitop3:0x6c
	v_lshl_add_u32 v52, v52, 4, v57
	ds_read_b128 v[52:55], v52 offset:32768
	v_bitop3_b32 v56, v56, v214, 31 bitop3:0x6c
	v_lshl_add_u32 v56, v56, 4, v57
	s_waitcnt lgkmcnt(0)
; __device__ __forceinline__ void unit(const bf16_t* proj, const bf16_t* mk, const bf16_t* mvt, bf16_t* Y3, int un, LAS unsigned char* lds) {
;     ...
;     for (int kb = 0; kb < 8; ++kb) { s[kb] = att::f32x16{};
; #pragma unroll
;         for (int q2 = 0; q2 < 8; ++q2) { att::bf16x8 kf[2]; int rv = r32; asm volatile("" : "+v"(rv));
; #pragma unroll
;             for (int i = 0; i < 2; ++i) kf[i] = frag(lds, kb * 32 + rv, 2 * (q2 * 2 + i) + hi);
;             asm volatile("" ::: "memory");
; #pragma unroll
;             for (int i = 0; i < 2; ++i) s[kb] = __builtin_amdgcn_mfma_f32_32x32x16_bf16(kf[i], qr[q2 * 2 + i], s[kb], 0, 0, 0); } }
	v_mfma_f32_32x32x16_bf16 v[36:51], v[52:55], v[184:187], v[36:51]
	ds_read_b128 v[52:55], v56 offset:32768
	v_mov_b32_e32 v56, v1
	s_nop 0
	v_lshl_add_u32 v57, v56, 9, 0
	s_waitcnt lgkmcnt(0)
	v_mfma_f32_32x32x16_bf16 v[36:51], v[52:55], v[180:183], v[36:51]
	v_bitop3_b32 v52, v56, v217, 31 bitop3:0x6c
	v_lshl_add_u32 v52, v52, 4, v57
	ds_read_b128 v[52:55], v52 offset:32768
	v_bitop3_b32 v56, v56, v206, 31 bitop3:0x6c
	v_lshl_add_u32 v56, v56, 4, v57
	s_waitcnt lgkmcnt(0)
	v_mfma_f32_32x32x16_bf16 v[36:51], v[52:55], v[176:179], v[36:51]
	ds_read_b128 v[52:55], v56 offset:32768
	v_mov_b32_e32 v56, v1
	s_nop 0
	v_lshl_add_u32 v57, v56, 9, 0
	s_waitcnt lgkmcnt(0)
	v_mfma_f32_32x32x16_bf16 v[36:51], v[52:55], v[172:175], v[36:51]
	v_bitop3_b32 v52, v56, v216, 31 bitop3:0x6c
	v_lshl_add_u32 v52, v52, 4, v57
	ds_read_b128 v[52:55], v52 offset:32768
	v_bitop3_b32 v56, v56, v211, 31 bitop3:0x6c
	v_lshl_add_u32 v56, v56, 4, v57
	s_waitcnt lgkmcnt(0)
	v_mfma_f32_32x32x16_bf16 v[36:51], v[52:55], v[168:171], v[36:51]
	ds_read_b128 v[52:55], v56 offset:32768
	v_mov_b32_e32 v56, v1
	s_nop 0
	v_lshl_add_u32 v57, v56, 9, 0
	s_waitcnt lgkmcnt(0)
	v_mfma_f32_32x32x16_bf16 v[36:51], v[52:55], v[164:167], v[36:51]
	v_bitop3_b32 v52, v56, v215, 31 bitop3:0x6c
	v_lshl_add_u32 v52, v52, 4, v57
	ds_read_b128 v[52:55], v52 offset:32768
	v_bitop3_b32 v56, v56, v202, 31 bitop3:0x6c
	v_lshl_add_u32 v56, v56, 4, v57
	s_waitcnt lgkmcnt(0)
	v_mfma_f32_32x32x16_bf16 v[36:51], v[52:55], v[160:163], v[36:51]
	ds_read_b128 v[52:55], v56 offset:32768
	v_mov_b32_e32 v56, v1
	s_nop 0
	v_lshl_add_u32 v57, v56, 9, 0
	s_waitcnt lgkmcnt(0)
	v_mfma_f32_32x32x16_bf16 v[36:51], v[52:55], v[156:159], v[36:51]
	v_bitop3_b32 v52, v56, v213, 31 bitop3:0x6c
	v_lshl_add_u32 v52, v52, 4, v57
	ds_read_b128 v[52:55], v52 offset:32768
	v_bitop3_b32 v56, v56, v208, 31 bitop3:0x6c
	v_lshl_add_u32 v56, v56, 4, v57
	s_waitcnt lgkmcnt(0)
	v_mfma_f32_32x32x16_bf16 v[36:51], v[52:55], v[152:155], v[36:51]
	ds_read_b128 v[52:55], v56 offset:32768
	v_mov_b32_e32 v56, v1
	s_nop 0
	v_lshl_add_u32 v57, v56, 9, 0
	s_waitcnt lgkmcnt(0)
	v_mfma_f32_32x32x16_bf16 v[36:51], v[52:55], v[148:151], v[36:51]
	v_bitop3_b32 v52, v56, v212, 31 bitop3:0x6c
	v_lshl_add_u32 v52, v52, 4, v57
	ds_read_b128 v[52:55], v52 offset:32768
	v_bitop3_b32 v56, v56, v201, 31 bitop3:0x6c
	v_lshl_add_u32 v56, v56, 4, v57
	s_waitcnt lgkmcnt(0)
	v_mfma_f32_32x32x16_bf16 v[36:51], v[52:55], v[144:147], v[36:51]
	ds_read_b128 v[52:55], v56 offset:32768
	v_mov_b32_e32 v56, v1
	s_nop 0
	v_lshl_add_u32 v57, v56, 9, 0
	s_waitcnt lgkmcnt(0)
	v_mfma_f32_32x32x16_bf16 v[36:51], v[52:55], v[140:143], v[36:51]
	v_bitop3_b32 v52, v56, v210, 31 bitop3:0x6c
	v_lshl_add_u32 v52, v52, 4, v57
	ds_read_b128 v[52:55], v52 offset:32768
	v_bitop3_b32 v56, v56, v204, 31 bitop3:0x6c
	v_lshl_add_u32 v56, v56, 4, v57
	s_waitcnt lgkmcnt(0)
	v_mfma_f32_32x32x16_bf16 v[36:51], v[52:55], v[136:139], v[36:51]
	ds_read_b128 v[52:55], v56 offset:32768
	v_mov_b32_e32 v56, v1
	s_nop 0
	v_lshl_add_u32 v57, v56, 9, 0
	s_waitcnt lgkmcnt(0)
	v_mfma_f32_32x32x16_bf16 v[36:51], v[52:55], v[132:135], v[36:51]
	v_bitop3_b32 v52, v56, v200, 31 bitop3:0x6c
	v_lshl_add_u32 v52, v52, 4, v57
	ds_read_b128 v[52:55], v52 offset:49152
	v_bitop3_b32 v56, v56, v209, 31 bitop3:0x6c
	v_lshl_add_u32 v68, v56, 4, v57
	ds_read_b128 v[68:71], v68 offset:49152
	s_waitcnt lgkmcnt(1)
	v_mfma_f32_32x32x16_bf16 v[52:67], v[52:55], v[116:119], 0
	s_nop 0
	v_lshl_add_u32 v73, v72, 9, 0
	s_waitcnt lgkmcnt(0)
	v_mfma_f32_32x32x16_bf16 v[52:67], v[68:71], v[188:191], v[52:67]
	v_bitop3_b32 v68, v72, v218, 31 bitop3:0x6c
	v_lshl_add_u32 v68, v68, 4, v73
	ds_read_b128 v[68:71], v68 offset:49152
	v_bitop3_b32 v72, v72, v214, 31 bitop3:0x6c
	v_lshl_add_u32 v72, v72, 4, v73
	s_waitcnt lgkmcnt(0)
	v_mfma_f32_32x32x16_bf16 v[52:67], v[68:71], v[184:187], v[52:67]
	ds_read_b128 v[68:71], v72 offset:49152
	v_mov_b32_e32 v72, v1
	s_nop 0
	v_lshl_add_u32 v73, v72, 9, 0
	s_waitcnt lgkmcnt(0)
	v_mfma_f32_32x32x16_bf16 v[52:67], v[68:71], v[180:183], v[52:67]
	v_bitop3_b32 v68, v72, v217, 31 bitop3:0x6c
	v_lshl_add_u32 v68, v68, 4, v73
	ds_read_b128 v[68:71], v68 offset:49152
	v_bitop3_b32 v72, v72, v206, 31 bitop3:0x6c
	v_lshl_add_u32 v72, v72, 4, v73
	s_waitcnt lgkmcnt(0)
	v_mfma_f32_32x32x16_bf16 v[52:67], v[68:71], v[176:179], v[52:67]
	ds_read_b128 v[68:71], v72 offset:49152
	v_mov_b32_e32 v72, v1
	s_nop 0
	v_lshl_add_u32 v73, v72, 9, 0
	s_waitcnt lgkmcnt(0)
	v_mfma_f32_32x32x16_bf16 v[52:67], v[68:71], v[172:175], v[52:67]
	v_bitop3_b32 v68, v72, v216, 31 bitop3:0x6c
	v_lshl_add_u32 v68, v68, 4, v73
	ds_read_b128 v[68:71], v68 offset:49152
	v_bitop3_b32 v72, v72, v211, 31 bitop3:0x6c
	v_lshl_add_u32 v72, v72, 4, v73
	s_waitcnt lgkmcnt(0)
	v_mfma_f32_32x32x16_bf16 v[52:67], v[68:71], v[168:171], v[52:67]
	ds_read_b128 v[68:71], v72 offset:49152
	v_mov_b32_e32 v72, v1
	s_nop 0
	v_lshl_add_u32 v73, v72, 9, 0
	s_waitcnt lgkmcnt(0)
	v_mfma_f32_32x32x16_bf16 v[52:67], v[68:71], v[164:167], v[52:67]
	v_bitop3_b32 v68, v72, v215, 31 bitop3:0x6c
	v_lshl_add_u32 v68, v68, 4, v73
	ds_read_b128 v[68:71], v68 offset:49152
	v_bitop3_b32 v72, v72, v202, 31 bitop3:0x6c
	v_lshl_add_u32 v72, v72, 4, v73
	s_waitcnt lgkmcnt(0)
	v_mfma_f32_32x32x16_bf16 v[52:67], v[68:71], v[160:163], v[52:67]
	ds_read_b128 v[68:71], v72 offset:49152
	v_mov_b32_e32 v72, v1
	s_nop 0
	v_lshl_add_u32 v73, v72, 9, 0
	s_waitcnt lgkmcnt(0)
	v_mfma_f32_32x32x16_bf16 v[52:67], v[68:71], v[156:159], v[52:67]
	v_bitop3_b32 v68, v72, v213, 31 bitop3:0x6c
	v_lshl_add_u32 v68, v68, 4, v73
	ds_read_b128 v[68:71], v68 offset:49152
	v_bitop3_b32 v72, v72, v208, 31 bitop3:0x6c
	v_lshl_add_u32 v72, v72, 4, v73
	s_waitcnt lgkmcnt(0)
; __device__ __forceinline__ void unit(const bf16_t* proj, const bf16_t* mk, const bf16_t* mvt, bf16_t* Y3, int un, LAS unsigned char* lds) {
;     ...
;     for (int kb = 0; kb < 8; ++kb) { s[kb] = att::f32x16{};
; #pragma unroll
;         for (int q2 = 0; q2 < 8; ++q2) { att::bf16x8 kf[2]; int rv = r32; asm volatile("" : "+v"(rv));
; #pragma unroll
;             for (int i = 0; i < 2; ++i) kf[i] = frag(lds, kb * 32 + rv, 2 * (q2 * 2 + i) + hi);
;             asm volatile("" ::: "memory");
; #pragma unroll
;             for (int i = 0; i < 2; ++i) s[kb] = __builtin_amdgcn_mfma_f32_32x32x16_bf16(kf[i], qr[q2 * 2 + i], s[kb], 0, 0, 0); } }
	v_mfma_f32_32x32x16_bf16 v[52:67], v[68:71], v[152:155], v[52:67]
	ds_read_b128 v[68:71], v72 offset:49152
	v_mov_b32_e32 v72, v1
	s_nop 0
	v_lshl_add_u32 v73, v72, 9, 0
	s_waitcnt lgkmcnt(0)
	v_mfma_f32_32x32x16_bf16 v[52:67], v[68:71], v[148:151], v[52:67]
	v_bitop3_b32 v68, v72, v212, 31 bitop3:0x6c
	v_lshl_add_u32 v68, v68, 4, v73
	ds_read_b128 v[68:71], v68 offset:49152
	v_bitop3_b32 v72, v72, v201, 31 bitop3:0x6c
	v_lshl_add_u32 v72, v72, 4, v73
	s_waitcnt lgkmcnt(0)
	v_mfma_f32_32x32x16_bf16 v[52:67], v[68:71], v[144:147], v[52:67]
	ds_read_b128 v[68:71], v72 offset:49152
	v_mov_b32_e32 v72, v1
	s_nop 0
	v_lshl_add_u32 v73, v72, 9, 0
	s_waitcnt lgkmcnt(0)
	v_mfma_f32_32x32x16_bf16 v[52:67], v[68:71], v[140:143], v[52:67]
	v_bitop3_b32 v68, v72, v210, 31 bitop3:0x6c
	v_lshl_add_u32 v68, v68, 4, v73
	ds_read_b128 v[68:71], v68 offset:49152
	v_bitop3_b32 v72, v72, v204, 31 bitop3:0x6c
	v_lshl_add_u32 v72, v72, 4, v73
	s_waitcnt lgkmcnt(0)
	v_mfma_f32_32x32x16_bf16 v[52:67], v[68:71], v[136:139], v[52:67]
	ds_read_b128 v[68:71], v72 offset:49152
	v_mov_b32_e32 v72, v1
	s_nop 0
	v_lshl_add_u32 v73, v72, 9, s7
	s_waitcnt lgkmcnt(0)
	v_mfma_f32_32x32x16_bf16 v[52:67], v[68:71], v[132:135], v[52:67]
	v_bitop3_b32 v68, v72, v200, 31 bitop3:0x6c
	v_lshl_add_u32 v68, v68, 4, v73
	ds_read_b128 v[68:71], v68
	v_bitop3_b32 v72, v72, v209, 31 bitop3:0x6c
	v_lshl_add_u32 v84, v72, 4, v73
	ds_read_b128 v[84:87], v84
	s_waitcnt lgkmcnt(1)
	v_mfma_f32_32x32x16_bf16 v[68:83], v[68:71], v[116:119], 0
	s_nop 0
	v_lshl_add_u32 v89, v88, 9, s7
	s_waitcnt lgkmcnt(0)
	v_mfma_f32_32x32x16_bf16 v[68:83], v[84:87], v[188:191], v[68:83]
	v_bitop3_b32 v84, v88, v218, 31 bitop3:0x6c
	v_lshl_add_u32 v84, v84, 4, v89
	ds_read_b128 v[84:87], v84
	v_bitop3_b32 v88, v88, v214, 31 bitop3:0x6c
	v_lshl_add_u32 v88, v88, 4, v89
	s_waitcnt lgkmcnt(0)
	v_mfma_f32_32x32x16_bf16 v[68:83], v[84:87], v[184:187], v[68:83]
	ds_read_b128 v[84:87], v88
	v_mov_b32_e32 v88, v1
	s_nop 0
	v_lshl_add_u32 v89, v88, 9, s7
	s_waitcnt lgkmcnt(0)
	v_mfma_f32_32x32x16_bf16 v[68:83], v[84:87], v[180:183], v[68:83]
	v_bitop3_b32 v84, v88, v217, 31 bitop3:0x6c
	v_lshl_add_u32 v84, v84, 4, v89
	ds_read_b128 v[84:87], v84
	v_bitop3_b32 v88, v88, v206, 31 bitop3:0x6c
	v_lshl_add_u32 v88, v88, 4, v89
	s_waitcnt lgkmcnt(0)
	v_mfma_f32_32x32x16_bf16 v[68:83], v[84:87], v[176:179], v[68:83]
	ds_read_b128 v[84:87], v88
	v_mov_b32_e32 v88, v1
	s_nop 0
	v_lshl_add_u32 v89, v88, 9, s7
	s_waitcnt lgkmcnt(0)
	v_mfma_f32_32x32x16_bf16 v[68:83], v[84:87], v[172:175], v[68:83]
	v_bitop3_b32 v84, v88, v216, 31 bitop3:0x6c
	v_lshl_add_u32 v84, v84, 4, v89
	ds_read_b128 v[84:87], v84
	v_bitop3_b32 v88, v88, v211, 31 bitop3:0x6c
	v_lshl_add_u32 v88, v88, 4, v89
	s_waitcnt lgkmcnt(0)
	v_mfma_f32_32x32x16_bf16 v[68:83], v[84:87], v[168:171], v[68:83]
	ds_read_b128 v[84:87], v88
	v_mov_b32_e32 v88, v1
	s_nop 0
	v_lshl_add_u32 v89, v88, 9, s7
	s_waitcnt lgkmcnt(0)
	v_mfma_f32_32x32x16_bf16 v[68:83], v[84:87], v[164:167], v[68:83]
	v_bitop3_b32 v84, v88, v215, 31 bitop3:0x6c
	v_lshl_add_u32 v84, v84, 4, v89
	ds_read_b128 v[84:87], v84
	v_bitop3_b32 v88, v88, v202, 31 bitop3:0x6c
	v_lshl_add_u32 v88, v88, 4, v89
	s_waitcnt lgkmcnt(0)
	v_mfma_f32_32x32x16_bf16 v[68:83], v[84:87], v[160:163], v[68:83]
	ds_read_b128 v[84:87], v88
	v_mov_b32_e32 v88, v1
	s_nop 0
	v_lshl_add_u32 v89, v88, 9, s7
	s_waitcnt lgkmcnt(0)
	v_mfma_f32_32x32x16_bf16 v[68:83], v[84:87], v[156:159], v[68:83]
	v_bitop3_b32 v84, v88, v213, 31 bitop3:0x6c
	v_lshl_add_u32 v84, v84, 4, v89
	ds_read_b128 v[84:87], v84
	v_bitop3_b32 v88, v88, v208, 31 bitop3:0x6c
	v_lshl_add_u32 v88, v88, 4, v89
	s_waitcnt lgkmcnt(0)
	v_mfma_f32_32x32x16_bf16 v[68:83], v[84:87], v[152:155], v[68:83]
	ds_read_b128 v[84:87], v88
	v_mov_b32_e32 v88, v1
	s_nop 0
	v_lshl_add_u32 v89, v88, 9, s7
	s_waitcnt lgkmcnt(0)
	v_mfma_f32_32x32x16_bf16 v[68:83], v[84:87], v[148:151], v[68:83]
	v_bitop3_b32 v84, v88, v212, 31 bitop3:0x6c
	v_lshl_add_u32 v84, v84, 4, v89
	ds_read_b128 v[84:87], v84
	v_bitop3_b32 v88, v88, v201, 31 bitop3:0x6c
	v_lshl_add_u32 v88, v88, 4, v89
	s_waitcnt lgkmcnt(0)
	v_mfma_f32_32x32x16_bf16 v[68:83], v[84:87], v[144:147], v[68:83]
	ds_read_b128 v[84:87], v88
	v_mov_b32_e32 v88, v1
	s_nop 0
	v_lshl_add_u32 v89, v88, 9, s7
	s_waitcnt lgkmcnt(0)
	v_mfma_f32_32x32x16_bf16 v[68:83], v[84:87], v[140:143], v[68:83]
	v_bitop3_b32 v84, v88, v210, 31 bitop3:0x6c
	v_lshl_add_u32 v84, v84, 4, v89
	ds_read_b128 v[84:87], v84
	v_bitop3_b32 v88, v88, v204, 31 bitop3:0x6c
	v_lshl_add_u32 v88, v88, 4, v89
	s_waitcnt lgkmcnt(0)
	v_mfma_f32_32x32x16_bf16 v[68:83], v[84:87], v[136:139], v[68:83]
	ds_read_b128 v[84:87], v88
	v_mov_b32_e32 v88, v1
	s_nop 0
	v_lshl_add_u32 v89, v88, 9, s6
	s_waitcnt lgkmcnt(0)
	v_mfma_f32_32x32x16_bf16 v[68:83], v[84:87], v[132:135], v[68:83]
	v_bitop3_b32 v84, v88, v200, 31 bitop3:0x6c
	v_lshl_add_u32 v84, v84, 4, v89
	ds_read_b128 v[84:87], v84
	v_bitop3_b32 v88, v88, v209, 31 bitop3:0x6c
	v_lshl_add_u32 v100, v88, 4, v89
	ds_read_b128 v[100:103], v100
	s_waitcnt lgkmcnt(1)
	v_mfma_f32_32x32x16_bf16 v[84:99], v[84:87], v[116:119], 0
	s_nop 0
	v_lshl_add_u32 v105, v104, 9, s6
	s_waitcnt lgkmcnt(0)
	v_mfma_f32_32x32x16_bf16 v[84:99], v[100:103], v[188:191], v[84:99]
	v_bitop3_b32 v100, v104, v218, 31 bitop3:0x6c
	v_lshl_add_u32 v100, v100, 4, v105
	ds_read_b128 v[100:103], v100
	v_bitop3_b32 v104, v104, v214, 31 bitop3:0x6c
	v_lshl_add_u32 v104, v104, 4, v105
	s_waitcnt lgkmcnt(0)
	v_mfma_f32_32x32x16_bf16 v[84:99], v[100:103], v[184:187], v[84:99]
	ds_read_b128 v[100:103], v104
	v_mov_b32_e32 v104, v1
	s_nop 0
	v_lshl_add_u32 v105, v104, 9, s6
	s_waitcnt lgkmcnt(0)
; __device__ __forceinline__ void unit(const bf16_t* proj, const bf16_t* mk, const bf16_t* mvt, bf16_t* Y3, int un, LAS unsigned char* lds) {
;     ...
;     for (int kb = 0; kb < 8; ++kb) { s[kb] = att::f32x16{};
; #pragma unroll
;         for (int q2 = 0; q2 < 8; ++q2) { att::bf16x8 kf[2]; int rv = r32; asm volatile("" : "+v"(rv));
; #pragma unroll
;             for (int i = 0; i < 2; ++i) kf[i] = frag(lds, kb * 32 + rv, 2 * (q2 * 2 + i) + hi);
;             asm volatile("" ::: "memory");
; #pragma unroll
;             for (int i = 0; i < 2; ++i) s[kb] = __builtin_amdgcn_mfma_f32_32x32x16_bf16(kf[i], qr[q2 * 2 + i], s[kb], 0, 0, 0); } }
	v_mfma_f32_32x32x16_bf16 v[84:99], v[100:103], v[180:183], v[84:99]
	v_bitop3_b32 v100, v104, v217, 31 bitop3:0x6c
	v_lshl_add_u32 v100, v100, 4, v105
	ds_read_b128 v[100:103], v100
	v_bitop3_b32 v104, v104, v206, 31 bitop3:0x6c
	v_lshl_add_u32 v104, v104, 4, v105
	s_waitcnt lgkmcnt(0)
	v_mfma_f32_32x32x16_bf16 v[84:99], v[100:103], v[176:179], v[84:99]
	ds_read_b128 v[100:103], v104
	v_mov_b32_e32 v104, v1
	s_nop 0
	v_lshl_add_u32 v105, v104, 9, s6
	s_waitcnt lgkmcnt(0)
	v_mfma_f32_32x32x16_bf16 v[84:99], v[100:103], v[172:175], v[84:99]
	v_bitop3_b32 v100, v104, v216, 31 bitop3:0x6c
	v_lshl_add_u32 v100, v100, 4, v105
	ds_read_b128 v[100:103], v100
	v_bitop3_b32 v104, v104, v211, 31 bitop3:0x6c
	v_lshl_add_u32 v104, v104, 4, v105
	s_waitcnt lgkmcnt(0)
	v_mfma_f32_32x32x16_bf16 v[84:99], v[100:103], v[168:171], v[84:99]
	ds_read_b128 v[100:103], v104
	v_mov_b32_e32 v104, v1
	s_nop 0
	v_lshl_add_u32 v105, v104, 9, s6
	s_waitcnt lgkmcnt(0)
	v_mfma_f32_32x32x16_bf16 v[84:99], v[100:103], v[164:167], v[84:99]
	v_bitop3_b32 v100, v104, v215, 31 bitop3:0x6c
	v_lshl_add_u32 v100, v100, 4, v105
	ds_read_b128 v[100:103], v100
	v_bitop3_b32 v104, v104, v202, 31 bitop3:0x6c
	v_lshl_add_u32 v104, v104, 4, v105
	s_waitcnt lgkmcnt(0)
	v_mfma_f32_32x32x16_bf16 v[84:99], v[100:103], v[160:163], v[84:99]
	ds_read_b128 v[100:103], v104
	v_mov_b32_e32 v104, v1
	s_nop 0
	v_lshl_add_u32 v105, v104, 9, s6
	s_waitcnt lgkmcnt(0)
	v_mfma_f32_32x32x16_bf16 v[84:99], v[100:103], v[156:159], v[84:99]
	v_bitop3_b32 v100, v104, v213, 31 bitop3:0x6c
	v_lshl_add_u32 v100, v100, 4, v105
	ds_read_b128 v[100:103], v100
	v_bitop3_b32 v104, v104, v208, 31 bitop3:0x6c
	v_lshl_add_u32 v104, v104, 4, v105
	s_waitcnt lgkmcnt(0)
	v_mfma_f32_32x32x16_bf16 v[84:99], v[100:103], v[152:155], v[84:99]
	ds_read_b128 v[100:103], v104
	v_mov_b32_e32 v104, v1
	s_nop 0
	v_lshl_add_u32 v105, v104, 9, s6
	s_waitcnt lgkmcnt(0)
	v_mfma_f32_32x32x16_bf16 v[84:99], v[100:103], v[148:151], v[84:99]
	v_bitop3_b32 v100, v104, v212, 31 bitop3:0x6c
	v_lshl_add_u32 v100, v100, 4, v105
	ds_read_b128 v[100:103], v100
	v_bitop3_b32 v104, v104, v201, 31 bitop3:0x6c
	v_lshl_add_u32 v104, v104, 4, v105
	s_waitcnt lgkmcnt(0)
	v_mfma_f32_32x32x16_bf16 v[84:99], v[100:103], v[144:147], v[84:99]
	ds_read_b128 v[100:103], v104
	v_mov_b32_e32 v104, v1
	s_nop 0
	v_lshl_add_u32 v105, v104, 9, s6
	s_waitcnt lgkmcnt(0)
	v_mfma_f32_32x32x16_bf16 v[84:99], v[100:103], v[140:143], v[84:99]
	v_bitop3_b32 v100, v104, v210, 31 bitop3:0x6c
	v_lshl_add_u32 v100, v100, 4, v105
	ds_read_b128 v[100:103], v100
	v_bitop3_b32 v104, v104, v204, 31 bitop3:0x6c
	v_lshl_add_u32 v104, v104, 4, v105
	s_waitcnt lgkmcnt(0)
	v_mfma_f32_32x32x16_bf16 v[84:99], v[100:103], v[136:139], v[84:99]
	ds_read_b128 v[100:103], v104
	v_mov_b32_e32 v104, v1
	s_nop 0
	v_lshl_add_u32 v105, v104, 9, s5
	s_waitcnt lgkmcnt(0)
	v_mfma_f32_32x32x16_bf16 v[84:99], v[100:103], v[132:135], v[84:99]
	v_bitop3_b32 v100, v104, v200, 31 bitop3:0x6c
	v_lshl_add_u32 v100, v100, 4, v105
	ds_read_b128 v[100:103], v100
	v_bitop3_b32 v104, v104, v209, 31 bitop3:0x6c
	v_lshl_add_u32 v120, v104, 4, v105
	ds_read_b128 v[120:123], v120
	s_waitcnt lgkmcnt(1)
	v_mfma_f32_32x32x16_bf16 v[100:115], v[100:103], v[116:119], 0
	s_nop 0
	v_lshl_add_u32 v125, v124, 9, s5
	s_waitcnt lgkmcnt(0)
	v_mfma_f32_32x32x16_bf16 v[100:115], v[120:123], v[188:191], v[100:115]
	v_bitop3_b32 v120, v124, v218, 31 bitop3:0x6c
	v_lshl_add_u32 v120, v120, 4, v125
	ds_read_b128 v[120:123], v120
	v_bitop3_b32 v124, v124, v214, 31 bitop3:0x6c
	v_lshl_add_u32 v124, v124, 4, v125
	s_waitcnt lgkmcnt(0)
	v_mfma_f32_32x32x16_bf16 v[100:115], v[120:123], v[184:187], v[100:115]
	ds_read_b128 v[120:123], v124
	v_mov_b32_e32 v124, v1
	s_nop 0
	v_lshl_add_u32 v125, v124, 9, s5
	s_waitcnt lgkmcnt(0)
	v_mfma_f32_32x32x16_bf16 v[100:115], v[120:123], v[180:183], v[100:115]
	v_bitop3_b32 v120, v124, v217, 31 bitop3:0x6c
	v_lshl_add_u32 v120, v120, 4, v125
	ds_read_b128 v[120:123], v120
	v_bitop3_b32 v124, v124, v206, 31 bitop3:0x6c
	v_lshl_add_u32 v124, v124, 4, v125
	s_waitcnt lgkmcnt(0)
	v_mfma_f32_32x32x16_bf16 v[100:115], v[120:123], v[176:179], v[100:115]
	ds_read_b128 v[120:123], v124
	v_mov_b32_e32 v124, v1
	s_nop 0
	v_lshl_add_u32 v125, v124, 9, s5
	s_waitcnt lgkmcnt(0)
	v_mfma_f32_32x32x16_bf16 v[100:115], v[120:123], v[172:175], v[100:115]
	v_bitop3_b32 v120, v124, v216, 31 bitop3:0x6c
	v_lshl_add_u32 v120, v120, 4, v125
	ds_read_b128 v[120:123], v120
	v_bitop3_b32 v124, v124, v211, 31 bitop3:0x6c
	v_lshl_add_u32 v124, v124, 4, v125
	s_waitcnt lgkmcnt(0)
	v_mfma_f32_32x32x16_bf16 v[100:115], v[120:123], v[168:171], v[100:115]
	ds_read_b128 v[120:123], v124
	v_mov_b32_e32 v124, v1
	s_nop 0
	v_lshl_add_u32 v125, v124, 9, s5
	s_waitcnt lgkmcnt(0)
	v_mfma_f32_32x32x16_bf16 v[100:115], v[120:123], v[164:167], v[100:115]
	v_bitop3_b32 v120, v124, v215, 31 bitop3:0x6c
	v_lshl_add_u32 v120, v120, 4, v125
	ds_read_b128 v[120:123], v120
	v_bitop3_b32 v124, v124, v202, 31 bitop3:0x6c
	v_lshl_add_u32 v124, v124, 4, v125
	s_waitcnt lgkmcnt(0)
	v_mfma_f32_32x32x16_bf16 v[100:115], v[120:123], v[160:163], v[100:115]
	ds_read_b128 v[120:123], v124
	v_mov_b32_e32 v124, v1
	s_nop 0
	v_lshl_add_u32 v125, v124, 9, s5
	s_waitcnt lgkmcnt(0)
	v_mfma_f32_32x32x16_bf16 v[100:115], v[120:123], v[156:159], v[100:115]
	v_bitop3_b32 v120, v124, v213, 31 bitop3:0x6c
	v_lshl_add_u32 v120, v120, 4, v125
	ds_read_b128 v[120:123], v120
	v_bitop3_b32 v124, v124, v208, 31 bitop3:0x6c
	v_lshl_add_u32 v124, v124, 4, v125
	s_waitcnt lgkmcnt(0)
	v_mfma_f32_32x32x16_bf16 v[100:115], v[120:123], v[152:155], v[100:115]
	ds_read_b128 v[120:123], v124
	v_mov_b32_e32 v124, v1
	s_nop 0
	v_lshl_add_u32 v125, v124, 9, s5
	s_waitcnt lgkmcnt(0)
; __device__ __forceinline__ void unit(const bf16_t* proj, const bf16_t* mk, const bf16_t* mvt, bf16_t* Y3, int un, LAS unsigned char* lds) {
;     ...
;     for (int kb = 0; kb < 8; ++kb) { s[kb] = att::f32x16{};
; #pragma unroll
;         for (int q2 = 0; q2 < 8; ++q2) { att::bf16x8 kf[2]; int rv = r32; asm volatile("" : "+v"(rv));
; #pragma unroll
;             for (int i = 0; i < 2; ++i) kf[i] = frag(lds, kb * 32 + rv, 2 * (q2 * 2 + i) + hi);
;             asm volatile("" ::: "memory");
; #pragma unroll
;             for (int i = 0; i < 2; ++i) s[kb] = __builtin_amdgcn_mfma_f32_32x32x16_bf16(kf[i], qr[q2 * 2 + i], s[kb], 0, 0, 0); } }
;     constexpr float C = 0.0625f * att::LOG2E;
;     float mx = -__builtin_inff();
; #pragma unroll
;     for (int kb = 0; kb < 8; ++kb)
; #pragma unroll
;         for (int r = 0; r < 16; ++r) mx = fmaxf(mx, s[kb][r]);
	v_mfma_f32_32x32x16_bf16 v[100:115], v[120:123], v[148:151], v[100:115]
	v_bitop3_b32 v120, v124, v212, 31 bitop3:0x6c
	v_lshl_add_u32 v120, v120, 4, v125
	ds_read_b128 v[120:123], v120
	v_bitop3_b32 v124, v124, v201, 31 bitop3:0x6c
	v_lshl_add_u32 v124, v124, 4, v125
	s_waitcnt lgkmcnt(0)
	v_mfma_f32_32x32x16_bf16 v[100:115], v[120:123], v[144:147], v[100:115]
	ds_read_b128 v[120:123], v124
	v_mov_b32_e32 v124, v1
	s_nop 0
	v_lshl_add_u32 v125, v124, 9, s5
	s_waitcnt lgkmcnt(0)
	v_mfma_f32_32x32x16_bf16 v[100:115], v[120:123], v[140:143], v[100:115]
	v_bitop3_b32 v120, v124, v210, 31 bitop3:0x6c
	v_lshl_add_u32 v120, v120, 4, v125
	ds_read_b128 v[120:123], v120
	v_bitop3_b32 v124, v124, v204, 31 bitop3:0x6c
	v_lshl_add_u32 v124, v124, 4, v125
	s_waitcnt lgkmcnt(0)
	v_mfma_f32_32x32x16_bf16 v[100:115], v[120:123], v[136:139], v[100:115]
	ds_read_b128 v[120:123], v124
	v_mov_b32_e32 v124, v1
	s_nop 0
	v_lshl_add_u32 v125, v124, 9, s4
	s_waitcnt lgkmcnt(0)
	v_mfma_f32_32x32x16_bf16 v[100:115], v[120:123], v[132:135], v[100:115]
	v_bitop3_b32 v120, v124, v200, 31 bitop3:0x6c
	v_lshl_add_u32 v120, v120, 4, v125
	ds_read_b128 v[120:123], v120
	v_bitop3_b32 v124, v124, v209, 31 bitop3:0x6c
	v_lshl_add_u32 v192, v124, 4, v125
	ds_read_b128 v[246:249], v192
	v_mov_b32_e32 v192, v1
	s_waitcnt lgkmcnt(1)
	v_mfma_f32_32x32x16_bf16 v[116:131], v[120:123], v[116:119], 0
	s_nop 0
	v_lshl_add_u32 v193, v192, 9, s4
	s_waitcnt lgkmcnt(0)
	v_mfma_f32_32x32x16_bf16 v[116:131], v[246:249], v[188:191], v[116:131]
	v_bitop3_b32 v188, v192, v218, 31 bitop3:0x6c
	v_lshl_add_u32 v188, v188, 4, v193
	ds_read_b128 v[188:191], v188
	v_bitop3_b32 v192, v192, v214, 31 bitop3:0x6c
	v_lshl_add_u32 v192, v192, 4, v193
	s_waitcnt lgkmcnt(0)
	v_mfma_f32_32x32x16_bf16 v[116:131], v[188:191], v[184:187], v[116:131]
	ds_read_b128 v[184:187], v192
	s_waitcnt lgkmcnt(0)
	v_mfma_f32_32x32x16_bf16 v[116:131], v[184:187], v[180:183], v[116:131]
	v_mov_b32_e32 v184, v1
	s_nop 0
	v_lshl_add_u32 v185, v184, 9, s4
	v_bitop3_b32 v180, v184, v217, 31 bitop3:0x6c
	v_lshl_add_u32 v180, v180, 4, v185
	ds_read_b128 v[180:183], v180
	v_bitop3_b32 v184, v184, v206, 31 bitop3:0x6c
	v_lshl_add_u32 v184, v184, 4, v185
	s_waitcnt lgkmcnt(0)
	v_mfma_f32_32x32x16_bf16 v[116:131], v[180:183], v[176:179], v[116:131]
	ds_read_b128 v[176:179], v184
	v_mov_b32_e32 v180, v1
	s_waitcnt lgkmcnt(0)
	v_mfma_f32_32x32x16_bf16 v[116:131], v[176:179], v[172:175], v[116:131]
	v_lshl_add_u32 v176, v180, 9, s4
	v_bitop3_b32 v172, v180, v216, 31 bitop3:0x6c
	v_lshl_add_u32 v172, v172, 4, v176
	ds_read_b128 v[172:175], v172
	v_bitop3_b32 v177, v180, v211, 31 bitop3:0x6c
	v_lshl_add_u32 v176, v177, 4, v176
	ds_read_b128 v[176:179], v176
	s_waitcnt lgkmcnt(1)
	v_mfma_f32_32x32x16_bf16 v[116:131], v[172:175], v[168:171], v[116:131]
	v_mov_b32_e32 v172, v1
	s_nop 0
	v_lshl_add_u32 v173, v172, 9, s4
	v_bitop3_b32 v168, v172, v215, 31 bitop3:0x6c
	v_lshl_add_u32 v168, v168, 4, v173
	ds_read_b128 v[168:171], v168
	s_waitcnt lgkmcnt(1)
	v_mfma_f32_32x32x16_bf16 v[116:131], v[176:179], v[164:167], v[116:131]
	v_bitop3_b32 v164, v172, v202, 31 bitop3:0x6c
	v_lshl_add_u32 v164, v164, 4, v173
	ds_read_b128 v[164:167], v164
	v_mov_b32_e32 v172, v1
	s_waitcnt lgkmcnt(1)
	v_mfma_f32_32x32x16_bf16 v[116:131], v[168:171], v[160:163], v[116:131]
	v_lshl_add_u32 v173, v172, 9, s4
	v_bitop3_b32 v160, v172, v213, 31 bitop3:0x6c
	v_bitop3_b32 v161, v172, v208, 31 bitop3:0x6c
	v_lshl_add_u32 v160, v160, 4, v173
	v_lshl_add_u32 v168, v161, 4, v173
	ds_read_b128 v[160:163], v160
	ds_read_b128 v[168:171], v168
	s_waitcnt lgkmcnt(2)
	v_mfma_f32_32x32x16_bf16 v[116:131], v[164:167], v[156:159], v[116:131]
	v_mov_b32_e32 v156, v1
	v_max3_f32 v164, v4, s9, v5
	v_lshl_add_u32 v157, v156, 9, s4
	v_bitop3_b32 v158, v156, v212, 31 bitop3:0x6c
	v_bitop3_b32 v156, v156, v201, 31 bitop3:0x6c
	v_lshl_add_u32 v158, v158, 4, v157
	s_waitcnt lgkmcnt(1)
	v_mfma_f32_32x32x16_bf16 v[116:131], v[160:163], v[152:155], v[116:131]
	v_lshl_add_u32 v156, v156, 4, v157
	ds_read_b128 v[152:155], v158
	ds_read_b128 v[156:159], v156
	v_mov_b32_e32 v160, v1
	s_ashr_i32 s9, s8, 31
	v_lshl_add_u32 v161, v160, 9, s4
	s_waitcnt lgkmcnt(2)
	v_mfma_f32_32x32x16_bf16 v[116:131], v[168:171], v[148:151], v[116:131]
	v_bitop3_b32 v162, v160, v210, 31 bitop3:0x6c
	v_bitop3_b32 v149, v160, v204, 31 bitop3:0x6c
	v_lshl_add_u32 v148, v162, 4, v161
	v_lshl_add_u32 v160, v149, 4, v161
	ds_read_b128 v[148:151], v148
	ds_read_b128 v[160:163], v160
	s_lshl_b64 s[8:9], s[8:9], 9
	s_add_u32 s8, s10, s8
	s_waitcnt lgkmcnt(3)
	v_mfma_f32_32x32x16_bf16 v[116:131], v[152:155], v[144:147], v[116:131]
	v_max3_f32 v144, v164, v6, v7
	v_max3_f32 v144, v144, v8, v9
	v_max3_f32 v144, v144, v10, v11
	v_max3_f32 v144, v144, v12, v13
	v_max3_f32 v144, v144, v14, v15
	v_max3_f32 v144, v144, v16, v17
	v_max3_f32 v144, v144, v18, v19
	s_waitcnt lgkmcnt(2)
	v_mfma_f32_32x32x16_bf16 v[116:131], v[156:159], v[140:143], v[116:131]
	v_max3_f32 v140, v144, v20, v21
	v_max3_f32 v140, v140, v22, v23
	v_max3_f32 v140, v140, v24, v25
	v_max3_f32 v140, v140, v26, v27
	v_max3_f32 v140, v140, v28, v29
	v_max3_f32 v140, v140, v30, v31
	v_max3_f32 v140, v140, v32, v33
	s_waitcnt lgkmcnt(1)
	v_mfma_f32_32x32x16_bf16 v[116:131], v[148:151], v[136:139], v[116:131]
	v_max3_f32 v136, v140, v34, v35
	v_max3_f32 v136, v136, v36, v37
	v_max3_f32 v136, v136, v38, v39
	v_max3_f32 v136, v136, v40, v41
	v_max3_f32 v136, v136, v42, v43
	v_max3_f32 v136, v136, v44, v45
	v_max3_f32 v136, v136, v46, v47
	s_waitcnt lgkmcnt(0)
; __device__ __forceinline__ void unit(const bf16_t* proj, const bf16_t* mk, const bf16_t* mvt, bf16_t* Y3, int un, LAS unsigned char* lds) {
;     ...
;             for (int i = 0; i < 2; ++i) s[kb] = __builtin_amdgcn_mfma_f32_32x32x16_bf16(kf[i], qr[q2 * 2 + i], s[kb], 0, 0, 0); } }
;     constexpr float C = 0.0625f * att::LOG2E;
;     float mx = -__builtin_inff();
; #pragma unroll
;     for (int kb = 0; kb < 8; ++kb)
; #pragma unroll
;         for (int r = 0; r < 16; ++r) mx = fmaxf(mx, s[kb][r]);
;     { auto rr = __builtin_amdgcn_permlane32_swap(__float_as_uint(mx), __float_as_uint(mx), false, false); mx = fmaxf(__uint_as_float(rr[0]), __uint_as_float(rr[1])); }
;     float l = 0.f; const float mc = mx * C;
; #pragma unroll
;     for (int kb = 0; kb < 8; ++kb)
; #pragma unroll
;         for (int r = 0; r < 16; ++r) { s[kb][r] = __builtin_amdgcn_exp2f(fmaf(s[kb][r], C, -mc)); l += s[kb][r]; }
	v_mfma_f32_32x32x16_bf16 v[116:131], v[160:163], v[132:135], v[116:131]
	s_setprio 0
	v_max3_f32 v132, v136, v48, v49
	v_max3_f32 v132, v132, v50, v51
	v_max3_f32 v132, v132, v52, v53
	v_max3_f32 v132, v132, v54, v55
	v_max3_f32 v132, v132, v56, v57
	v_max3_f32 v132, v132, v58, v59
	v_max3_f32 v132, v132, v60, v61
	v_max3_f32 v132, v132, v62, v63
	v_max3_f32 v132, v132, v64, v65
	v_max3_f32 v132, v132, v66, v67
	v_max3_f32 v132, v132, v68, v69
	v_max3_f32 v132, v132, v70, v71
	v_max3_f32 v132, v132, v72, v73
	v_max3_f32 v132, v132, v74, v75
	v_max3_f32 v132, v132, v76, v77
	v_max3_f32 v132, v132, v78, v79
	v_max3_f32 v132, v132, v80, v81
	v_max3_f32 v132, v132, v82, v83
	v_max3_f32 v132, v132, v84, v85
	v_max3_f32 v132, v132, v86, v87
	v_max3_f32 v132, v132, v88, v89
	v_max3_f32 v132, v132, v90, v91
	v_max3_f32 v132, v132, v92, v93
	v_max3_f32 v132, v132, v94, v95
	v_max3_f32 v132, v132, v96, v97
	v_max3_f32 v132, v132, v98, v99
	v_max3_f32 v132, v132, v100, v101
	v_max3_f32 v132, v132, v102, v103
	v_max3_f32 v132, v132, v104, v105
	v_max3_f32 v132, v132, v106, v107
	v_max3_f32 v132, v132, v108, v109
	v_max3_f32 v132, v132, v110, v111
	v_max3_f32 v132, v132, v112, v113
	v_max3_f32 v132, v132, v114, v115
	v_max3_f32 v132, v132, v116, v117
	v_max3_f32 v132, v132, v118, v119
	v_max3_f32 v132, v132, v120, v121
	v_max3_f32 v132, v132, v122, v123
	v_max3_f32 v132, v132, v124, v125
	v_max3_f32 v132, v132, v126, v127
	v_max3_f32 v132, v132, v128, v129
	v_max3_f32 v132, v132, v130, v131
	v_mov_b32_e32 v133, v132
	s_nop 1
	v_permlane32_swap_b32_e32 v132, v133
	v_max_f32_e32 v133, v133, v133
	v_max_f32_e32 v132, v132, v132
	v_max_f32_e32 v132, v132, v133
	v_mul_f32_e32 v158, 0xbdb8aa3b, v132
	v_fmamk_f32 v4, v4, 0x3db8aa3b, v158
	v_exp_f32_e32 v159, v4
	v_fmamk_f32 v4, v5, 0x3db8aa3b, v158
	v_exp_f32_e32 v160, v4
	v_fmamk_f32 v4, v6, 0x3db8aa3b, v158
	v_exp_f32_e32 v161, v4
	v_fmamk_f32 v4, v7, 0x3db8aa3b, v158
	v_exp_f32_e32 v162, v4
	v_fmamk_f32 v5, v8, 0x3db8aa3b, v158
	v_add_f32_e32 v4, 0, v159
	v_exp_f32_e32 v163, v5
	v_fmamk_f32 v5, v9, 0x3db8aa3b, v158
	v_add_f32_e32 v4, v160, v4
	v_exp_f32_e32 v164, v5
	v_fmamk_f32 v5, v10, 0x3db8aa3b, v158
	v_add_f32_e32 v4, v161, v4
	v_exp_f32_e32 v165, v5
	v_fmamk_f32 v5, v11, 0x3db8aa3b, v158
	v_add_f32_e32 v4, v162, v4
	v_exp_f32_e32 v166, v5
	v_fmamk_f32 v5, v12, 0x3db8aa3b, v158
	v_add_f32_e32 v4, v163, v4
	v_exp_f32_e32 v167, v5
	v_fmamk_f32 v5, v13, 0x3db8aa3b, v158
	v_add_f32_e32 v4, v164, v4
	v_exp_f32_e32 v168, v5
	v_fmamk_f32 v5, v14, 0x3db8aa3b, v158
	v_add_f32_e32 v4, v165, v4
	v_exp_f32_e32 v169, v5
	v_fmamk_f32 v5, v15, 0x3db8aa3b, v158
	v_add_f32_e32 v4, v166, v4
	v_exp_f32_e32 v170, v5
	v_fmamk_f32 v5, v16, 0x3db8aa3b, v158
	v_add_f32_e32 v4, v167, v4
	v_exp_f32_e32 v171, v5
	v_fmamk_f32 v5, v17, 0x3db8aa3b, v158
	v_add_f32_e32 v4, v168, v4
	v_exp_f32_e32 v172, v5
	v_fmamk_f32 v5, v18, 0x3db8aa3b, v158
	v_add_f32_e32 v4, v169, v4
	v_exp_f32_e32 v173, v5
	v_fmamk_f32 v5, v19, 0x3db8aa3b, v158
	v_add_f32_e32 v4, v170, v4
	v_exp_f32_e32 v174, v5
	v_fmamk_f32 v5, v20, 0x3db8aa3b, v158
	v_add_f32_e32 v4, v171, v4
	v_exp_f32_e32 v175, v5
	v_fmamk_f32 v5, v21, 0x3db8aa3b, v158
	v_add_f32_e32 v4, v172, v4
	v_exp_f32_e32 v176, v5
	v_fmamk_f32 v5, v22, 0x3db8aa3b, v158
	v_add_f32_e32 v4, v173, v4
	v_exp_f32_e32 v177, v5
	v_fmamk_f32 v5, v23, 0x3db8aa3b, v158
	v_add_f32_e32 v4, v174, v4
	v_exp_f32_e32 v178, v5
	v_fmamk_f32 v5, v24, 0x3db8aa3b, v158
	v_add_f32_e32 v4, v175, v4
	v_exp_f32_e32 v24, v5
	v_fmamk_f32 v5, v25, 0x3db8aa3b, v158
	v_add_f32_e32 v4, v176, v4
	v_exp_f32_e32 v25, v5
	v_fmamk_f32 v5, v26, 0x3db8aa3b, v158
	v_add_f32_e32 v4, v177, v4
	v_exp_f32_e32 v26, v5
	v_fmamk_f32 v5, v27, 0x3db8aa3b, v158
	v_add_f32_e32 v4, v178, v4
	v_exp_f32_e32 v27, v5
	v_fmamk_f32 v5, v28, 0x3db8aa3b, v158
	v_add_f32_e32 v4, v24, v4
	v_exp_f32_e32 v179, v5
	v_fmamk_f32 v5, v29, 0x3db8aa3b, v158
	v_add_f32_e32 v4, v25, v4
	v_exp_f32_e32 v180, v5
	v_fmamk_f32 v5, v30, 0x3db8aa3b, v158
	v_add_f32_e32 v4, v26, v4
	v_exp_f32_e32 v181, v5
	v_fmamk_f32 v5, v31, 0x3db8aa3b, v158
	v_add_f32_e32 v4, v27, v4
	v_exp_f32_e32 v182, v5
	v_fmamk_f32 v5, v32, 0x3db8aa3b, v158
	v_add_f32_e32 v4, v179, v4
	v_exp_f32_e32 v32, v5
	v_fmamk_f32 v5, v33, 0x3db8aa3b, v158
	v_add_f32_e32 v4, v180, v4
	v_exp_f32_e32 v33, v5
	v_fmamk_f32 v5, v34, 0x3db8aa3b, v158
	v_add_f32_e32 v4, v181, v4
	v_exp_f32_e32 v34, v5
	v_fmamk_f32 v5, v35, 0x3db8aa3b, v158
	v_add_f32_e32 v4, v182, v4
	v_exp_f32_e32 v35, v5
	v_fmamk_f32 v5, v36, 0x3db8aa3b, v158
	v_add_f32_e32 v4, v32, v4
	v_exp_f32_e32 v183, v5
	v_fmamk_f32 v5, v37, 0x3db8aa3b, v158
	v_add_f32_e32 v4, v33, v4
	v_exp_f32_e32 v184, v5
	v_fmamk_f32 v5, v38, 0x3db8aa3b, v158
	v_add_f32_e32 v4, v34, v4
	v_exp_f32_e32 v185, v5
	v_fmamk_f32 v5, v39, 0x3db8aa3b, v158
	v_add_f32_e32 v4, v35, v4
	v_exp_f32_e32 v186, v5
	v_fmamk_f32 v5, v40, 0x3db8aa3b, v158
	v_add_f32_e32 v4, v183, v4
	v_exp_f32_e32 v40, v5
	v_fmamk_f32 v5, v41, 0x3db8aa3b, v158
	v_add_f32_e32 v4, v184, v4
	v_exp_f32_e32 v41, v5
	v_fmamk_f32 v5, v42, 0x3db8aa3b, v158
	v_add_f32_e32 v4, v185, v4
	v_exp_f32_e32 v42, v5
	v_fmamk_f32 v5, v43, 0x3db8aa3b, v158
	v_add_f32_e32 v4, v186, v4
	v_exp_f32_e32 v43, v5
	v_fmamk_f32 v5, v44, 0x3db8aa3b, v158
	v_add_f32_e32 v4, v40, v4
	v_exp_f32_e32 v187, v5
	v_fmamk_f32 v5, v45, 0x3db8aa3b, v158
	v_add_f32_e32 v4, v41, v4
	v_exp_f32_e32 v188, v5
	v_fmamk_f32 v5, v46, 0x3db8aa3b, v158
	v_add_f32_e32 v4, v42, v4
	v_exp_f32_e32 v189, v5
	v_fmamk_f32 v5, v47, 0x3db8aa3b, v158
	v_add_f32_e32 v4, v43, v4
	v_exp_f32_e32 v190, v5
	v_fmamk_f32 v5, v48, 0x3db8aa3b, v158
	v_add_f32_e32 v4, v187, v4
; __device__ __forceinline__ int crow(int r, int hi) { return (r & 3) + 8 * (r >> 2) + 4 * hi; }
; __device__ __forceinline__ void unit(const bf16_t* proj, const bf16_t* mk, const bf16_t* mvt, bf16_t* Y3, int un, LAS unsigned char* lds) {
;     ...
;     float l = 0.f; const float mc = mx * C;
; #pragma unroll
;     for (int kb = 0; kb < 8; ++kb)
; #pragma unroll
;         for (int r = 0; r < 16; ++r) { s[kb][r] = __builtin_amdgcn_exp2f(fmaf(s[kb][r], C, -mc)); l += s[kb][r]; }
;     { auto rr = __builtin_amdgcn_permlane32_swap(__float_as_uint(l), __float_as_uint(l), false, false); l = __uint_as_float(rr[0]) + __uint_as_float(rr[1]); }
;     const float linv = 1.0f / l;
;     att::bf16x8 pa[16];
;     ...
; #pragma unroll
;     for (int kb = 0; kb < 8; ++kb) { MEM_PK4(s[kb], 0, pa[2 * kb]); MEM_PK4(s[kb], 8, pa[2 * kb + 1]); }
;     ...
; #pragma unroll
;     for (int i = 0; i < 16; ++i) { u32x4 w_ = __builtin_bit_cast(u32x4, pa[i]); asm volatile("" : "+v"(w_)); pa[i] = __builtin_bit_cast(att::bf16x8, w_); }
;     float rli[16];
; #pragma unroll
;     for (int r = 0; r < 16; ++r) rli[r] = __shfl(linv, att::crow(r, hi));
;     stage_load(st, mvt + (size_t)((b * 4 + h) * 256) * 256, 256, wave, lane);
	v_exp_f32_e32 v48, v5
	v_fmamk_f32 v5, v49, 0x3db8aa3b, v158
	v_add_f32_e32 v4, v188, v4
	v_exp_f32_e32 v49, v5
	v_fmamk_f32 v5, v50, 0x3db8aa3b, v158
	v_add_f32_e32 v4, v189, v4
	v_exp_f32_e32 v50, v5
	v_fmamk_f32 v5, v51, 0x3db8aa3b, v158
	v_add_f32_e32 v4, v190, v4
	v_exp_f32_e32 v51, v5
	v_fmamk_f32 v5, v52, 0x3db8aa3b, v158
	v_add_f32_e32 v4, v48, v4
	v_exp_f32_e32 v52, v5
	v_fmamk_f32 v5, v53, 0x3db8aa3b, v158
	v_add_f32_e32 v4, v49, v4
	v_exp_f32_e32 v53, v5
	v_fmamk_f32 v5, v54, 0x3db8aa3b, v158
	v_add_f32_e32 v4, v50, v4
	v_exp_f32_e32 v54, v5
	v_fmamk_f32 v5, v55, 0x3db8aa3b, v158
	v_add_f32_e32 v4, v51, v4
	v_exp_f32_e32 v55, v5
	v_fmamk_f32 v5, v56, 0x3db8aa3b, v158
	v_add_f32_e32 v4, v52, v4
	v_exp_f32_e32 v56, v5
	v_fmamk_f32 v5, v57, 0x3db8aa3b, v158
	v_add_f32_e32 v4, v53, v4
	v_exp_f32_e32 v57, v5
	v_fmamk_f32 v5, v58, 0x3db8aa3b, v158
	v_add_f32_e32 v4, v54, v4
	v_exp_f32_e32 v58, v5
	v_fmamk_f32 v5, v59, 0x3db8aa3b, v158
	v_add_f32_e32 v4, v55, v4
	v_exp_f32_e32 v59, v5
	v_add_f32_e32 v4, v56, v4
	v_add_f32_e32 v4, v57, v4
	v_add_f32_e32 v4, v58, v4
	v_add_f32_e32 v134, v59, v4
	v_fmamk_f32 v4, v60, 0x3db8aa3b, v158
	v_exp_f32_e32 v136, v4
	v_fmamk_f32 v4, v61, 0x3db8aa3b, v158
	v_exp_f32_e32 v17, v4
	v_fmamk_f32 v4, v62, 0x3db8aa3b, v158
	v_exp_f32_e32 v133, v4
	v_fmamk_f32 v4, v63, 0x3db8aa3b, v158
	v_exp_f32_e32 v15, v4
	v_fmamk_f32 v4, v64, 0x3db8aa3b, v158
	v_exp_f32_e32 v19, v4
	v_fmamk_f32 v4, v65, 0x3db8aa3b, v158
	v_exp_f32_e32 v14, v4
	v_fmamk_f32 v4, v66, 0x3db8aa3b, v158
	v_exp_f32_e32 v18, v4
	v_fmamk_f32 v4, v67, 0x3db8aa3b, v158
	v_exp_f32_e32 v6, v4
	v_fmamk_f32 v4, v68, 0x3db8aa3b, v158
	v_exp_f32_e32 v7, v4
	v_fmamk_f32 v4, v69, 0x3db8aa3b, v158
	v_exp_f32_e32 v8, v4
	v_fmamk_f32 v4, v70, 0x3db8aa3b, v158
	v_exp_f32_e32 v9, v4
	v_fmamk_f32 v4, v71, 0x3db8aa3b, v158
	v_exp_f32_e32 v10, v4
	v_fmamk_f32 v4, v72, 0x3db8aa3b, v158
	v_exp_f32_e32 v11, v4
	v_fmamk_f32 v4, v73, 0x3db8aa3b, v158
	v_exp_f32_e32 v12, v4
	v_fmamk_f32 v4, v74, 0x3db8aa3b, v158
	v_exp_f32_e32 v13, v4
	v_fmamk_f32 v4, v75, 0x3db8aa3b, v158
	v_exp_f32_e32 v16, v4
	v_fmamk_f32 v4, v76, 0x3db8aa3b, v158
	v_exp_f32_e32 v132, v4
	v_fmamk_f32 v4, v77, 0x3db8aa3b, v158
	v_exp_f32_e32 v135, v4
	v_fmamk_f32 v4, v78, 0x3db8aa3b, v158
	v_exp_f32_e32 v137, v4
	v_fmamk_f32 v4, v79, 0x3db8aa3b, v158
	v_exp_f32_e32 v138, v4
	v_fmamk_f32 v4, v80, 0x3db8aa3b, v158
	v_exp_f32_e32 v139, v4
	v_fmamk_f32 v4, v81, 0x3db8aa3b, v158
	v_exp_f32_e32 v140, v4
	v_fmamk_f32 v4, v82, 0x3db8aa3b, v158
	v_exp_f32_e32 v141, v4
	v_fmamk_f32 v4, v83, 0x3db8aa3b, v158
	v_exp_f32_e32 v142, v4
	v_fmamk_f32 v4, v84, 0x3db8aa3b, v158
	v_exp_f32_e32 v84, v4
	v_fmamk_f32 v4, v85, 0x3db8aa3b, v158
	v_exp_f32_e32 v143, v4
	v_fmamk_f32 v4, v86, 0x3db8aa3b, v158
	v_exp_f32_e32 v86, v4
	v_fmamk_f32 v4, v87, 0x3db8aa3b, v158
	v_exp_f32_e32 v144, v4
	v_fmamk_f32 v4, v88, 0x3db8aa3b, v158
	v_exp_f32_e32 v88, v4
	v_fmamk_f32 v4, v89, 0x3db8aa3b, v158
	v_exp_f32_e32 v145, v4
	v_fmamk_f32 v4, v90, 0x3db8aa3b, v158
	v_exp_f32_e32 v90, v4
	v_fmamk_f32 v4, v91, 0x3db8aa3b, v158
	v_exp_f32_e32 v146, v4
	v_fmamk_f32 v4, v92, 0x3db8aa3b, v158
	v_exp_f32_e32 v92, v4
	v_fmamk_f32 v4, v93, 0x3db8aa3b, v158
	v_exp_f32_e32 v147, v4
	v_fmamk_f32 v4, v94, 0x3db8aa3b, v158
	v_exp_f32_e32 v94, v4
	v_fmamk_f32 v4, v95, 0x3db8aa3b, v158
	v_exp_f32_e32 v149, v4
	v_fmamk_f32 v4, v96, 0x3db8aa3b, v158
	v_exp_f32_e32 v96, v4
	v_fmamk_f32 v4, v97, 0x3db8aa3b, v158
	v_exp_f32_e32 v150, v4
	v_fmamk_f32 v4, v98, 0x3db8aa3b, v158
	v_exp_f32_e32 v98, v4
	v_fmamk_f32 v4, v99, 0x3db8aa3b, v158
	v_exp_f32_e32 v151, v4
	v_fmamk_f32 v4, v100, 0x3db8aa3b, v158
	v_exp_f32_e32 v100, v4
	v_fmamk_f32 v4, v101, 0x3db8aa3b, v158
	v_exp_f32_e32 v152, v4
	v_fmamk_f32 v4, v102, 0x3db8aa3b, v158
	v_exp_f32_e32 v102, v4
	v_fmamk_f32 v4, v103, 0x3db8aa3b, v158
	v_exp_f32_e32 v153, v4
	v_fmamk_f32 v4, v104, 0x3db8aa3b, v158
	v_exp_f32_e32 v104, v4
	v_fmamk_f32 v4, v105, 0x3db8aa3b, v158
	v_exp_f32_e32 v154, v4
	v_fmamk_f32 v4, v106, 0x3db8aa3b, v158
	v_exp_f32_e32 v106, v4
	v_fmamk_f32 v4, v107, 0x3db8aa3b, v158
	v_exp_f32_e32 v155, v4
	v_fmamk_f32 v4, v108, 0x3db8aa3b, v158
	v_fmamk_f32 v20, v115, 0x3db8aa3b, v158
	v_exp_f32_e32 v108, v4
	v_fmamk_f32 v4, v109, 0x3db8aa3b, v158
	v_exp_f32_e32 v97, v20
	v_fmamk_f32 v20, v116, 0x3db8aa3b, v158
	v_exp_f32_e32 v156, v4
	v_fmamk_f32 v4, v110, 0x3db8aa3b, v158
	v_exp_f32_e32 v101, v20
	v_fmamk_f32 v20, v117, 0x3db8aa3b, v158
	v_exp_f32_e32 v110, v4
	v_fmamk_f32 v4, v111, 0x3db8aa3b, v158
	v_exp_f32_e32 v105, v20
	v_fmamk_f32 v20, v118, 0x3db8aa3b, v158
	v_exp_f32_e32 v157, v4
	v_fmamk_f32 v4, v112, 0x3db8aa3b, v158
	v_exp_f32_e32 v109, v20
	v_fmamk_f32 v20, v119, 0x3db8aa3b, v158
	v_exp_f32_e32 v112, v4
	v_fmamk_f32 v4, v113, 0x3db8aa3b, v158
	v_exp_f32_e32 v113, v20
	v_fmamk_f32 v20, v120, 0x3db8aa3b, v158
	v_exp_f32_e32 v148, v20
	v_fmamk_f32 v20, v121, 0x3db8aa3b, v158
	v_readlane_b32 s10, v254, 34
	v_exp_f32_e32 v111, v20
	v_fmamk_f32 v20, v122, 0x3db8aa3b, v158
	s_addc_u32 s9, s10, s9
	v_lshlrev_b64 v[116:117], 9, v[198:199]
	v_exp_f32_e32 v115, v20
	v_fmamk_f32 v20, v123, 0x3db8aa3b, v158
	v_lshl_add_u64 v[116:117], s[8:9], 0, v[116:117]
	v_exp_f32_e32 v89, v20
	v_fmamk_f32 v20, v124, 0x3db8aa3b, v158
	v_cvt_pk_bf16_f32 v39, v26, v27
	v_cvt_pk_bf16_f32 v26, v32, v33
	v_cvt_pk_bf16_f32 v45, v185, v186
	v_cvt_pk_bf16_f32 v32, v187, v188
	v_lshl_add_u64 v[186:187], v[116:117], 0, v[2:3]
	s_movk_i32 s8, 0x2000
	v_exp_f32_e32 v93, v20
	v_fmamk_f32 v20, v125, 0x3db8aa3b, v158
	v_add_co_u32_e32 v120, vcc, s8, v186
	v_exp_f32_e32 v99, v20
	v_fmamk_f32 v20, v126, 0x3db8aa3b, v158
; __device__ __forceinline__ int crow(int r, int hi) { return (r & 3) + 8 * (r >> 2) + 4 * hi; }
; __device__ __forceinline__ void unit(const bf16_t* proj, const bf16_t* mk, const bf16_t* mvt, bf16_t* Y3, int un, LAS unsigned char* lds) {
;     ...
;         for (int r = 0; r < 16; ++r) { s[kb][r] = __builtin_amdgcn_exp2f(fmaf(s[kb][r], C, -mc)); l += s[kb][r]; }
;     { auto rr = __builtin_amdgcn_permlane32_swap(__float_as_uint(l), __float_as_uint(l), false, false); l = __uint_as_float(rr[0]) + __uint_as_float(rr[1]); }
;     const float linv = 1.0f / l;
;     att::bf16x8 pa[16];
;     ...
; #pragma unroll
;     for (int kb = 0; kb < 8; ++kb) { MEM_PK4(s[kb], 0, pa[2 * kb]); MEM_PK4(s[kb], 8, pa[2 * kb + 1]); }
;     ...
; #pragma unroll
;     for (int i = 0; i < 16; ++i) { u32x4 w_ = __builtin_bit_cast(u32x4, pa[i]); asm volatile("" : "+v"(w_)); pa[i] = __builtin_bit_cast(att::bf16x8, w_); }
;     float rli[16];
; #pragma unroll
;     for (int r = 0; r < 16; ++r) rli[r] = __shfl(linv, att::crow(r, hi));
;     stage_load(st, mvt + (size_t)((b * 4 + h) * 256) * 256, 256, wave, lane);
	v_addc_co_u32_e32 v121, vcc, 0, v187, vcc
	s_movk_i32 s8, 0x4000
	v_exp_f32_e32 v103, v20
	v_fmamk_f32 v20, v127, 0x3db8aa3b, v158
	v_add_co_u32_e32 v124, vcc, s8, v186
	v_exp_f32_e32 v107, v20
	v_fmamk_f32 v20, v128, 0x3db8aa3b, v158
	v_addc_co_u32_e32 v125, vcc, 0, v187, vcc
	s_movk_i32 s10, 0x6000
	v_exp_f32_e32 v91, v20
	v_fmamk_f32 v20, v129, 0x3db8aa3b, v158
	v_add_co_u32_e32 v128, vcc, s10, v186
	v_fmamk_f32 v5, v114, 0x3db8aa3b, v158
	v_exp_f32_e32 v95, v20
	v_fmamk_f32 v20, v130, 0x3db8aa3b, v158
	v_fmac_f32_e32 v158, 0x3db8aa3b, v131
	v_addc_co_u32_e32 v129, vcc, 0, v187, vcc
	s_mov_b32 s8, 0x8000
	v_exp_f32_e32 v87, v158
	v_add_co_u32_e32 v158, vcc, s8, v186
	v_cvt_pk_bf16_f32 v28, v159, v160
	s_nop 0
	v_addc_co_u32_e32 v159, vcc, 0, v187, vcc
	s_mov_b32 s8, 0xa000
	v_cvt_pk_bf16_f32 v29, v161, v162
	v_add_co_u32_e32 v162, vcc, s8, v186
	v_cvt_pk_bf16_f32 v30, v163, v164
	s_nop 0
	v_addc_co_u32_e32 v163, vcc, 0, v187, vcc
	s_mov_b32 s8, 0xc000
	v_cvt_pk_bf16_f32 v31, v165, v166
	v_add_co_u32_e32 v166, vcc, s8, v186
	v_exp_f32_e32 v85, v20
	v_cvt_pk_bf16_f32 v20, v167, v168
	v_addc_co_u32_e32 v167, vcc, 0, v187, vcc
	s_mov_b32 s8, 0xe000
	v_exp_f32_e32 v4, v4
	v_exp_f32_e32 v5, v5
	v_cvt_pk_bf16_f32 v21, v169, v170
	v_add_co_u32_e32 v170, vcc, s8, v186
	v_cvt_pk_bf16_f32 v22, v171, v172
	s_nop 0
	v_addc_co_u32_e32 v171, vcc, 0, v187, vcc
	v_cvt_pk_bf16_f32 v23, v173, v174
	v_add_co_u32_e32 v174, vcc, s84, v186
	v_cvt_pk_bf16_f32 v36, v175, v176
	s_nop 0
	v_addc_co_u32_e32 v175, vcc, 0, v187, vcc
	s_mov_b32 s8, 0x12000
	v_cvt_pk_bf16_f32 v37, v177, v178
	v_cvt_pk_bf16_f32 v38, v24, v25
	v_cvt_pk_bf16_f32 v24, v179, v180
	v_cvt_pk_bf16_f32 v25, v181, v182
	v_cvt_pk_bf16_f32 v27, v34, v35
	v_cvt_pk_bf16_f32 v44, v183, v184
	v_cvt_pk_bf16_f32 v46, v40, v41
	v_cvt_pk_bf16_f32 v47, v42, v43
	v_cvt_pk_bf16_f32 v33, v189, v190
	v_cvt_pk_bf16_f32 v34, v48, v49
	v_cvt_pk_bf16_f32 v35, v50, v51
	v_cvt_pk_bf16_f32 v52, v52, v53
	v_cvt_pk_bf16_f32 v53, v54, v55
	v_cvt_pk_bf16_f32 v54, v56, v57
	v_cvt_pk_bf16_f32 v55, v58, v59
	v_cvt_pk_bf16_f32 v40, v136, v17
	v_cvt_pk_bf16_f32 v41, v133, v15
	v_cvt_pk_bf16_f32 v42, v19, v14
	v_cvt_pk_bf16_f32 v43, v18, v6
	v_cvt_pk_bf16_f32 v60, v7, v8
	v_cvt_pk_bf16_f32 v61, v9, v10
	v_cvt_pk_bf16_f32 v62, v11, v12
	v_cvt_pk_bf16_f32 v63, v13, v16
	v_cvt_pk_bf16_f32 v48, v132, v135
	v_cvt_pk_bf16_f32 v49, v137, v138
	v_cvt_pk_bf16_f32 v50, v139, v140
	v_cvt_pk_bf16_f32 v51, v141, v142
	v_cvt_pk_bf16_f32 v68, v84, v143
	v_cvt_pk_bf16_f32 v69, v86, v144
	v_cvt_pk_bf16_f32 v70, v88, v145
	v_cvt_pk_bf16_f32 v71, v90, v146
	v_cvt_pk_bf16_f32 v56, v92, v147
	v_cvt_pk_bf16_f32 v57, v94, v149
	v_cvt_pk_bf16_f32 v58, v96, v150
	v_cvt_pk_bf16_f32 v59, v98, v151
	v_cvt_pk_bf16_f32 v72, v100, v152
	v_cvt_pk_bf16_f32 v73, v102, v153
	v_cvt_pk_bf16_f32 v74, v104, v154
	v_cvt_pk_bf16_f32 v75, v106, v155
	v_cvt_pk_bf16_f32 v64, v108, v156
	v_cvt_pk_bf16_f32 v65, v110, v157
	v_cvt_pk_bf16_f32 v66, v112, v4
	v_cvt_pk_bf16_f32 v67, v5, v97
	v_cvt_pk_bf16_f32 v76, v101, v105
	v_cvt_pk_bf16_f32 v77, v109, v113
	v_cvt_pk_bf16_f32 v78, v148, v111
	v_cvt_pk_bf16_f32 v79, v115, v89
	v_cvt_pk_bf16_f32 v80, v93, v99
	v_cvt_pk_bf16_f32 v81, v103, v107
	v_cvt_pk_bf16_f32 v82, v91, v95
	v_cvt_pk_bf16_f32 v83, v85, v87
	v_add_co_u32_e32 v178, vcc, s8, v186
	v_permlane32_swap_b32_e32 v28, v30
	v_permlane32_swap_b32_e32 v29, v31
	v_permlane32_swap_b32_e32 v20, v22
	v_permlane32_swap_b32_e32 v21, v23
	v_permlane32_swap_b32_e32 v36, v38
	v_permlane32_swap_b32_e32 v37, v39
	v_permlane32_swap_b32_e32 v24, v26
	v_permlane32_swap_b32_e32 v25, v27
	v_permlane32_swap_b32_e32 v44, v46
	v_permlane32_swap_b32_e32 v45, v47
	v_permlane32_swap_b32_e32 v32, v34
	v_permlane32_swap_b32_e32 v33, v35
	v_permlane32_swap_b32_e32 v52, v54
	v_permlane32_swap_b32_e32 v53, v55
	v_permlane32_swap_b32_e32 v40, v42
	v_permlane32_swap_b32_e32 v41, v43
	v_permlane32_swap_b32_e32 v60, v62
	v_permlane32_swap_b32_e32 v61, v63
	v_permlane32_swap_b32_e32 v48, v50
	v_permlane32_swap_b32_e32 v49, v51
	v_permlane32_swap_b32_e32 v68, v70
	v_permlane32_swap_b32_e32 v69, v71
	v_permlane32_swap_b32_e32 v56, v58
	v_permlane32_swap_b32_e32 v57, v59
	v_permlane32_swap_b32_e32 v72, v74
	v_permlane32_swap_b32_e32 v73, v75
	v_permlane32_swap_b32_e32 v64, v66
	v_permlane32_swap_b32_e32 v65, v67
	v_permlane32_swap_b32_e32 v76, v78
	v_permlane32_swap_b32_e32 v77, v79
	v_permlane32_swap_b32_e32 v80, v82
	v_permlane32_swap_b32_e32 v81, v83
	v_addc_co_u32_e32 v179, vcc, 0, v187, vcc
	s_mov_b32 s8, 0x14000
	global_load_dwordx4 v[116:119], v[186:187], off
	s_nop 0
	global_load_dwordx4 v[120:123], v[120:121], off
	s_nop 0
	global_load_dwordx4 v[124:127], v[124:125], off
	s_nop 0
	global_load_dwordx4 v[128:131], v[128:129], off
	s_nop 0
	global_load_dwordx4 v[158:161], v[158:159], off
	s_nop 0
	global_load_dwordx4 v[162:165], v[162:163], off
	s_nop 0
	global_load_dwordx4 v[166:169], v[166:167], off
	s_nop 0
	global_load_dwordx4 v[170:173], v[170:171], off
	s_nop 0
	global_load_dwordx4 v[174:177], v[174:175], off
	s_nop 0
	global_load_dwordx4 v[178:181], v[178:179], off
	v_add_co_u32_e32 v182, vcc, s8, v186
	s_mov_b32 s8, 0x16000
	s_nop 0
	v_addc_co_u32_e32 v183, vcc, 0, v187, vcc
	v_add_co_u32_e32 v188, vcc, s8, v186
	s_mov_b32 s8, 0x18000
	s_nop 0
	v_addc_co_u32_e32 v189, vcc, 0, v187, vcc
	v_add_co_u32_e32 v190, vcc, s8, v186
	s_mov_b32 s8, 0x1a000
	s_nop 0
	v_addc_co_u32_e32 v191, vcc, 0, v187, vcc
	v_add_co_u32_e32 v198, vcc, s8, v186
	s_mov_b32 s8, 0x1c000
	s_nop 0
	v_addc_co_u32_e32 v199, vcc, 0, v187, vcc
	v_add_co_u32_e32 v232, vcc, s8, v186
	s_mov_b32 s8, 0x1e000
	s_nop 0
; __device__ __forceinline__ int crow(int r, int hi) { return (r & 3) + 8 * (r >> 2) + 4 * hi; }
; __device__ __forceinline__ void unit(const bf16_t* proj, const bf16_t* mk, const bf16_t* mvt, bf16_t* Y3, int un, LAS unsigned char* lds) {
;     ...
;         for (int r = 0; r < 16; ++r) { s[kb][r] = __builtin_amdgcn_exp2f(fmaf(s[kb][r], C, -mc)); l += s[kb][r]; }
;     { auto rr = __builtin_amdgcn_permlane32_swap(__float_as_uint(l), __float_as_uint(l), false, false); l = __uint_as_float(rr[0]) + __uint_as_float(rr[1]); }
;     const float linv = 1.0f / l;
;     att::bf16x8 pa[16];
;     ...
; #pragma unroll
;     for (int kb = 0; kb < 8; ++kb) { MEM_PK4(s[kb], 0, pa[2 * kb]); MEM_PK4(s[kb], 8, pa[2 * kb + 1]); }
;     ...
; #pragma unroll
;     for (int i = 0; i < 16; ++i) { u32x4 w_ = __builtin_bit_cast(u32x4, pa[i]); asm volatile("" : "+v"(w_)); pa[i] = __builtin_bit_cast(att::bf16x8, w_); }
;     float rli[16];
; #pragma unroll
;     for (int r = 0; r < 16; ++r) rli[r] = __shfl(linv, att::crow(r, hi));
;     stage_load(st, mvt + (size_t)((b * 4 + h) * 256) * 256, 256, wave, lane);
;     asm volatile("" ::: "memory");
;     __syncthreads();
;     stage_store(st, lds, wave, lane);
;     __syncthreads();
; #pragma unroll
;     for (int hf = 0; hf < 4; ++hf) { unsigned zz[32];
; #pragma unroll
;         for (int dbi = 0; dbi < 2; ++dbi)
; #pragma unroll
;             for (int r = 0; r < 16; ++r) zz[dbi * 16 + r] = *(const unsigned*)(proj + (size_t)(bt0 + att::crow(r, hi)) * NC + C_ZM + h * 256 + (hf * 2 + dbi) * 32 + (r32 & ~1));
	v_addc_co_u32_e32 v233, vcc, 0, v187, vcc
	global_load_dwordx4 v[182:185], v[182:183], off
	v_add_co_u32_e32 v236, vcc, s8, v186
	global_load_dwordx4 v[190:193], v[190:191], off
	s_nop 0
	v_addc_co_u32_e32 v237, vcc, 0, v187, vcc
	global_load_dwordx4 v[186:189], v[188:189], off
	v_add_f32_e32 v2, v136, v134
	global_load_dwordx4 v[246:249], v[198:199], off
	v_add_f32_e32 v2, v17, v2
	global_load_dwordx4 v[232:235], v[232:233], off
	v_add_f32_e32 v2, v133, v2
	global_load_dwordx4 v[236:239], v[236:237], off
	v_add_f32_e32 v2, v15, v2
	v_add_f32_e32 v2, v19, v2
	v_add_f32_e32 v2, v14, v2
	v_add_f32_e32 v2, v18, v2
	v_add_f32_e32 v2, v6, v2
	v_add_f32_e32 v2, v7, v2
	v_add_f32_e32 v2, v8, v2
	v_add_f32_e32 v2, v9, v2
	v_add_f32_e32 v2, v10, v2
	v_add_f32_e32 v2, v11, v2
	v_add_f32_e32 v2, v12, v2
	v_add_f32_e32 v2, v13, v2
	v_add_f32_e32 v2, v16, v2
	v_add_f32_e32 v2, v132, v2
	v_add_f32_e32 v2, v135, v2
	v_add_f32_e32 v2, v137, v2
	v_add_f32_e32 v2, v138, v2
	v_add_f32_e32 v2, v139, v2
	v_add_f32_e32 v2, v140, v2
	v_add_f32_e32 v2, v141, v2
	v_add_f32_e32 v2, v142, v2
	v_add_f32_e32 v2, v84, v2
	v_add_f32_e32 v2, v143, v2
	v_add_f32_e32 v2, v86, v2
	v_add_f32_e32 v2, v144, v2
	v_add_f32_e32 v2, v88, v2
	v_add_f32_e32 v2, v145, v2
	v_add_f32_e32 v2, v90, v2
	v_add_f32_e32 v2, v146, v2
	v_add_f32_e32 v2, v92, v2
	v_add_f32_e32 v2, v147, v2
	v_add_f32_e32 v2, v94, v2
	v_add_f32_e32 v2, v149, v2
	v_add_f32_e32 v2, v96, v2
	v_add_f32_e32 v2, v150, v2
	v_add_f32_e32 v2, v98, v2
	v_add_f32_e32 v2, v151, v2
	v_add_f32_e32 v2, v100, v2
	v_add_f32_e32 v2, v152, v2
	v_add_f32_e32 v2, v102, v2
	v_add_f32_e32 v2, v153, v2
	v_add_f32_e32 v2, v104, v2
	v_add_f32_e32 v2, v154, v2
	v_add_f32_e32 v2, v106, v2
	v_add_f32_e32 v2, v155, v2
	v_add_f32_e32 v2, v108, v2
	v_add_f32_e32 v2, v156, v2
	v_add_f32_e32 v2, v110, v2
	v_lshlrev_b32_e32 v156, 2, v200
	v_add_f32_e32 v2, v157, v2
	v_or_b32_e32 v84, s1, v156
	v_add_f32_e32 v149, v112, v2
	v_and_b32_e32 v2, 30, v220
	v_mad_i64_i32 v[6:7], s[8:9], v84, s11, v[196:197]
	v_lshl_add_u64 v[6:7], v[6:7], 0, s[2:3]
	v_lshlrev_b32_e32 v2, 1, v2
	v_or_b32_e32 v86, 1, v84
	v_lshl_add_u64 v[6:7], v[6:7], 0, v[2:3]
	v_mad_i64_i32 v[8:9], s[8:9], v86, s11, v[196:197]
	s_barrier
	s_waitcnt vmcnt(15)
	ds_write_b128 v222, v[116:119]
	s_waitcnt vmcnt(14)
	ds_write_b128 v224, v[120:123]
	s_waitcnt vmcnt(13)
	ds_write_b128 v222, v[124:127] offset:16384
	s_waitcnt vmcnt(12)
	ds_write_b128 v226, v[128:131]
	s_waitcnt vmcnt(11)
	ds_write_b128 v222, v[158:161] offset:32768
	s_waitcnt vmcnt(10)
	ds_write_b128 v228, v[162:165]
	s_waitcnt vmcnt(9)
	ds_write_b128 v222, v[166:169] offset:49152
	s_waitcnt vmcnt(8)
	ds_write_b128 v230, v[170:173]
	s_waitcnt vmcnt(7)
	ds_write_b128 v223, v[174:177]
	s_waitcnt vmcnt(6)
	ds_write_b128 v240, v[178:181]
	s_waitcnt vmcnt(5)
	ds_write_b128 v245, v[182:185]
	s_waitcnt vmcnt(3)
	ds_write_b128 v250, v[186:189]
	ds_write_b128 v251, v[190:193]
	s_waitcnt vmcnt(2)
	ds_write_b128 v194, v[246:249]
	s_waitcnt vmcnt(1)
	ds_write_b128 v195, v[232:235]
	s_waitcnt vmcnt(0)
	ds_write_b128 v244, v[236:239]
	v_lshl_add_u64 v[116:117], v[6:7], 0, s[12:13]
	v_add_co_u32_e32 v6, vcc, s10, v6
	v_lshl_add_u64 v[8:9], v[8:9], 0, s[2:3]
	v_or_b32_e32 v88, 2, v84
	v_addc_co_u32_e32 v7, vcc, 0, v7, vcc
	v_lshl_add_u64 v[8:9], v[8:9], 0, v[2:3]
	v_mad_i64_i32 v[10:11], s[8:9], v88, s11, v[196:197]
	v_lshl_add_u64 v[118:119], v[8:9], 0, s[12:13]
	v_add_co_u32_e32 v8, vcc, s10, v8
	v_lshl_add_u64 v[10:11], v[10:11], 0, s[2:3]
	v_or_b32_e32 v90, 3, v84
	v_addc_co_u32_e32 v9, vcc, 0, v9, vcc
	v_lshl_add_u64 v[10:11], v[10:11], 0, v[2:3]
	v_mad_i64_i32 v[12:13], s[8:9], v90, s11, v[196:197]
	v_lshl_add_u64 v[120:121], v[10:11], 0, s[12:13]
	v_add_co_u32_e32 v10, vcc, s10, v10
	v_lshl_add_u64 v[12:13], v[12:13], 0, s[2:3]
	v_or_b32_e32 v92, 8, v84
	v_addc_co_u32_e32 v11, vcc, 0, v11, vcc
	v_lshl_add_u64 v[12:13], v[12:13], 0, v[2:3]
	v_mad_i64_i32 v[14:15], s[8:9], v92, s11, v[196:197]
	v_lshl_add_u64 v[124:125], v[12:13], 0, s[12:13]
	v_add_co_u32_e32 v12, vcc, s10, v12
	v_lshl_add_u64 v[14:15], v[14:15], 0, s[2:3]
	v_or_b32_e32 v94, 9, v84
	v_addc_co_u32_e32 v13, vcc, 0, v13, vcc
	v_lshl_add_u64 v[14:15], v[14:15], 0, v[2:3]
	v_mad_i64_i32 v[16:17], s[8:9], v94, s11, v[196:197]
	v_lshl_add_u64 v[122:123], v[14:15], 0, s[12:13]
	v_add_co_u32_e32 v14, vcc, s10, v14
	v_lshl_add_u64 v[16:17], v[16:17], 0, s[2:3]
	v_or_b32_e32 v96, 10, v84
	v_addc_co_u32_e32 v15, vcc, 0, v15, vcc
	v_lshl_add_u64 v[16:17], v[16:17], 0, v[2:3]
	v_mad_i64_i32 v[18:19], s[8:9], v96, s11, v[196:197]
	v_lshl_add_u64 v[126:127], v[16:17], 0, s[12:13]
	v_add_co_u32_e32 v16, vcc, s10, v16
	v_lshl_add_u64 v[18:19], v[18:19], 0, s[2:3]
	v_or_b32_e32 v98, 11, v84
	v_addc_co_u32_e32 v17, vcc, 0, v17, vcc
	v_lshl_add_u64 v[18:19], v[18:19], 0, v[2:3]
	v_mad_i64_i32 v[130:131], s[8:9], v98, s11, v[196:197]
	v_lshl_add_u64 v[128:129], v[18:19], 0, s[12:13]
	v_add_co_u32_e32 v18, vcc, s10, v18
	v_lshl_add_u64 v[130:131], v[130:131], 0, s[2:3]
	s_nop 0
	v_addc_co_u32_e32 v19, vcc, 0, v19, vcc
	v_lshl_add_u64 v[132:133], v[130:131], 0, v[2:3]
	v_lshl_add_u64 v[130:131], v[132:133], 0, s[12:13]
	v_add_co_u32_e32 v132, vcc, s10, v132
	v_or_b32_e32 v100, 16, v84
	s_waitcnt lgkmcnt(0)
	s_barrier
; __device__ __forceinline__ int crow(int r, int hi) { return (r & 3) + 8 * (r >> 2) + 4 * hi; }
; __device__ __forceinline__ void unit(const bf16_t* proj, const bf16_t* mk, const bf16_t* mvt, bf16_t* Y3, int un, LAS unsigned char* lds) {
;     ...
;     for (int hf = 0; hf < 4; ++hf) { unsigned zz[32];
; #pragma unroll
;         for (int dbi = 0; dbi < 2; ++dbi)
; #pragma unroll
;             for (int r = 0; r < 16; ++r) zz[dbi * 16 + r] = *(const unsigned*)(proj + (size_t)(bt0 + att::crow(r, hi)) * NC + C_ZM + h * 256 + (hf * 2 + dbi) * 32 + (r32 & ~1));
;         asm volatile("" ::: "memory");
; #pragma unroll
;         for (int dbi = 0; dbi < 2; ++dbi) { const int db = hf * 2 + dbi; att::f32x16 o = att::f32x16{};
; #pragma unroll
;             for (int q4 = 0; q4 < 4; ++q4) { att::bf16x8 vf[4]; int rv = r32; asm volatile("" : "+v"(rv));
; #pragma unroll
;                 for (int i = 0; i < 4; ++i) vf[i] = frag(lds, db * 32 + rv, 2 * (q4 * 4 + i) + hi);
;                 asm volatile("" ::: "memory");
; #pragma unroll
;                 for (int i = 0; i < 4; ++i) o = __builtin_amdgcn_mfma_f32_32x32x16_bf16(pa[q4 * 4 + i], vf[i], o, 0, 0, 0); }
	v_addc_co_u32_e32 v133, vcc, 0, v133, vcc
	global_load_dword v224, v[6:7], off
	global_load_dword v223, v[8:9], off
	global_load_dword v193, v[10:11], off
	global_load_dword v192, v[12:13], off
	global_load_dword v222, v[14:15], off
	global_load_dword v199, v[16:17], off
	global_load_dword v198, v[18:19], off
	global_load_dword v191, v[132:133], off
	v_mad_i64_i32 v[6:7], s[8:9], v100, s11, v[196:197]
	v_lshl_add_u64 v[6:7], v[6:7], 0, s[2:3]
	v_or_b32_e32 v102, 17, v84
	v_lshl_add_u64 v[6:7], v[6:7], 0, v[2:3]
	v_mad_i64_i32 v[8:9], s[8:9], v102, s11, v[196:197]
	v_lshl_add_u64 v[132:133], v[6:7], 0, s[12:13]
	v_add_co_u32_e32 v6, vcc, s10, v6
	v_lshl_add_u64 v[8:9], v[8:9], 0, s[2:3]
	v_or_b32_e32 v104, 18, v84
	v_addc_co_u32_e32 v7, vcc, 0, v7, vcc
	v_lshl_add_u64 v[8:9], v[8:9], 0, v[2:3]
	v_mad_i64_i32 v[10:11], s[8:9], v104, s11, v[196:197]
	v_lshl_add_u64 v[134:135], v[8:9], 0, s[12:13]
	v_add_co_u32_e32 v8, vcc, s10, v8
	v_lshl_add_u64 v[10:11], v[10:11], 0, s[2:3]
	v_or_b32_e32 v106, 19, v84
	v_addc_co_u32_e32 v9, vcc, 0, v9, vcc
	v_lshl_add_u64 v[10:11], v[10:11], 0, v[2:3]
	v_mad_i64_i32 v[12:13], s[8:9], v106, s11, v[196:197]
	v_lshl_add_u64 v[136:137], v[10:11], 0, s[12:13]
	v_add_co_u32_e32 v10, vcc, s10, v10
	v_lshl_add_u64 v[12:13], v[12:13], 0, s[2:3]
	v_or_b32_e32 v108, 24, v84
	v_addc_co_u32_e32 v11, vcc, 0, v11, vcc
	v_lshl_add_u64 v[12:13], v[12:13], 0, v[2:3]
	v_mad_i64_i32 v[14:15], s[8:9], v108, s11, v[196:197]
	v_lshl_add_u64 v[140:141], v[12:13], 0, s[12:13]
	v_add_co_u32_e32 v12, vcc, s10, v12
	v_lshl_add_u64 v[14:15], v[14:15], 0, s[2:3]
	v_or_b32_e32 v110, 25, v84
	v_addc_co_u32_e32 v13, vcc, 0, v13, vcc
	v_lshl_add_u64 v[14:15], v[14:15], 0, v[2:3]
	v_mad_i64_i32 v[16:17], s[8:9], v110, s11, v[196:197]
	v_lshl_add_u64 v[138:139], v[14:15], 0, s[12:13]
	v_add_co_u32_e32 v14, vcc, s10, v14
	v_lshl_add_u64 v[16:17], v[16:17], 0, s[2:3]
	v_or_b32_e32 v112, 26, v84
	v_addc_co_u32_e32 v15, vcc, 0, v15, vcc
	v_lshl_add_u64 v[16:17], v[16:17], 0, v[2:3]
	v_mad_i64_i32 v[18:19], s[8:9], v112, s11, v[196:197]
	v_lshl_add_u64 v[142:143], v[16:17], 0, s[12:13]
	v_add_co_u32_e32 v16, vcc, s10, v16
	v_lshl_add_u64 v[18:19], v[18:19], 0, s[2:3]
	v_or_b32_e32 v114, 27, v84
	v_addc_co_u32_e32 v17, vcc, 0, v17, vcc
	v_lshl_add_u64 v[18:19], v[18:19], 0, v[2:3]
	v_mad_i64_i32 v[146:147], s[8:9], v114, s11, v[196:197]
	v_lshl_add_u64 v[144:145], v[18:19], 0, s[12:13]
	v_add_co_u32_e32 v18, vcc, s10, v18
	v_lshl_add_u64 v[146:147], v[146:147], 0, s[2:3]
	s_nop 0
	v_addc_co_u32_e32 v19, vcc, 0, v19, vcc
	v_lshl_add_u64 v[150:151], v[146:147], 0, v[2:3]
	v_lshl_add_u64 v[146:147], v[150:151], 0, s[12:13]
	v_add_co_u32_e32 v150, vcc, s10, v150
	v_mov_b32_e32 v2, v1
	s_nop 0
	v_addc_co_u32_e32 v151, vcc, 0, v151, vcc
	global_load_dword v197, v[6:7], off
	global_load_dword v196, v[8:9], off
	global_load_dword v190, v[10:11], off
	global_load_dword v189, v[12:13], off
	global_load_dword v188, v[14:15], off
	global_load_dword v187, v[16:17], off
	global_load_dword v186, v[18:19], off
	global_load_dword v185, v[150:151], off
	global_load_dword v184, v[116:117], off offset:64
	global_load_dword v183, v[118:119], off offset:64
	global_load_dword v182, v[120:121], off offset:64
	global_load_dword v181, v[124:125], off offset:64
	global_load_dword v180, v[122:123], off offset:64
	global_load_dword v179, v[126:127], off offset:64
	global_load_dword v178, v[128:129], off offset:64
	global_load_dword v177, v[130:131], off offset:64
	global_load_dword v176, v[132:133], off offset:64
	global_load_dword v175, v[134:135], off offset:64
	global_load_dword v174, v[136:137], off offset:64
	global_load_dword v173, v[140:141], off offset:64
	global_load_dword v172, v[138:139], off offset:64
	global_load_dword v171, v[142:143], off offset:64
	global_load_dword v170, v[144:145], off offset:64
	global_load_dword v169, v[146:147], off offset:64
	v_add_f32_e32 v4, v4, v149
	v_lshl_add_u32 v154, v2, 9, 0
	v_bitop3_b32 v6, v2, v200, 31 bitop3:0x6c
	v_lshl_add_u32 v6, v6, 4, v154
	ds_read_b128 v[6:9], v6
	v_add_f32_e32 v149, v5, v4
	v_bitop3_b32 v4, v2, v209, 31 bitop3:0x6c
	v_lshl_add_u32 v150, v4, 4, v154
	ds_read_b128 v[150:153], v150
	s_waitcnt lgkmcnt(1)
	s_setprio 1
	v_mfma_f32_32x32x16_bf16 v[4:19], v[28:31], v[6:9], 0
	v_add_f32_e32 v97, v97, v149
	v_add_f32_e32 v97, v101, v97
	v_add_f32_e32 v97, v105, v97
	v_add_f32_e32 v97, v109, v97
	v_bitop3_b32 v101, v2, v218, 31 bitop3:0x6c
	v_add_f32_e32 v97, v113, v97
	v_lshl_add_u32 v101, v101, 4, v154
	s_waitcnt lgkmcnt(0)
	v_mfma_f32_32x32x16_bf16 v[4:19], v[20:23], v[150:153], v[4:19]
	v_add_f32_e32 v97, v148, v97
	ds_read_b128 v[148:151], v101
	v_bitop3_b32 v2, v2, v214, 31 bitop3:0x6c
	v_lshl_add_u32 v2, v2, 4, v154
	v_add_f32_e32 v97, v111, v97
	v_add_f32_e32 v97, v115, v97
	s_waitcnt lgkmcnt(0)
	v_mfma_f32_32x32x16_bf16 v[4:19], v[36:39], v[148:151], v[4:19]
	ds_read_b128 v[148:151], v2
	v_add_f32_e32 v2, v89, v97
	v_mov_b32_e32 v89, v1
	v_add_f32_e32 v2, v93, v2
	v_add_f32_e32 v2, v99, v2
	s_waitcnt lgkmcnt(0)
; __device__ __forceinline__ float bflo(unsigned w) { return __uint_as_float(w << 16); }
; __device__ __forceinline__ float bfhi(unsigned w) { return __uint_as_float(w & 0xffff0000u); }
; __device__ __forceinline__ unsigned pk2(float lo, float hi) { return f2bf(lo) | (f2bf(hi) << 16); }
; __device__ __forceinline__ int crow(int r, int hi) { return (r & 3) + 8 * (r >> 2) + 4 * hi; }
; __device__ __forceinline__ void unit(const bf16_t* proj, const bf16_t* mk, const bf16_t* mvt, bf16_t* Y3, int un, LAS unsigned char* lds) {
;     ...
;     { auto rr = __builtin_amdgcn_permlane32_swap(__float_as_uint(l), __float_as_uint(l), false, false); l = __uint_as_float(rr[0]) + __uint_as_float(rr[1]); }
;     const float linv = 1.0f / l;
;     att::bf16x8 pa[16];
;     ...
; #pragma unroll
;     for (int kb = 0; kb < 8; ++kb) { MEM_PK4(s[kb], 0, pa[2 * kb]); MEM_PK4(s[kb], 8, pa[2 * kb + 1]); }
;     ...
; #pragma unroll
;     for (int i = 0; i < 16; ++i) { u32x4 w_ = __builtin_bit_cast(u32x4, pa[i]); asm volatile("" : "+v"(w_)); pa[i] = __builtin_bit_cast(att::bf16x8, w_); }
;     float rli[16];
; #pragma unroll
;     for (int r = 0; r < 16; ++r) rli[r] = __shfl(linv, att::crow(r, hi));
;     ...
;         for (int dbi = 0; dbi < 2; ++dbi) { const int db = hf * 2 + dbi; att::f32x16 o = att::f32x16{};
; #pragma unroll
;             for (int q4 = 0; q4 < 4; ++q4) { att::bf16x8 vf[4]; int rv = r32; asm volatile("" : "+v"(rv));
; #pragma unroll
;                 for (int i = 0; i < 4; ++i) vf[i] = frag(lds, db * 32 + rv, 2 * (q4 * 4 + i) + hi);
;                 asm volatile("" ::: "memory");
; #pragma unroll
;                 for (int i = 0; i < 4; ++i) o = __builtin_amdgcn_mfma_f32_32x32x16_bf16(pa[q4 * 4 + i], vf[i], o, 0, 0, 0); }
; #pragma unroll
;             for (int r = 0; r < 16; ++r) { const int bt = bt0 + att::crow(r, hi), col = h * 256 + db * 32 + r32; const float val = o[r] * rli[r], vn = __shfl_xor(val, 1);
;                 if ((r32 & 1) == 0) *(unsigned*)(Y3 + (size_t)bt * YS + col) = pk2(val * bflo(zz[dbi * 16 + r]), vn * bfhi(zz[dbi * 16 + r])); } } }
	v_mfma_f32_32x32x16_bf16 v[4:19], v[24:27], v[148:151], v[4:19]
	v_lshl_add_u32 v93, v89, 9, 0
	v_bitop3_b32 v97, v89, v217, 31 bitop3:0x6c
	v_lshl_add_u32 v97, v97, 4, v93
	ds_read_b128 v[148:151], v97
	v_add_f32_e32 v2, v103, v2
	v_add_f32_e32 v2, v107, v2
	v_add_f32_e32 v2, v91, v2
	s_waitcnt lgkmcnt(0)
	v_mfma_f32_32x32x16_bf16 v[4:19], v[44:47], v[148:151], v[4:19]
	v_bitop3_b32 v91, v89, v206, 31 bitop3:0x6c
	v_lshl_add_u32 v91, v91, 4, v93
	ds_read_b128 v[148:151], v91
	v_add_f32_e32 v2, v95, v2
	v_add_f32_e32 v2, v85, v2
	v_add_f32_e32 v2, v87, v2
	v_mov_b32_e32 v85, v2
	s_nop 1
	v_permlane32_swap_b32_e32 v2, v85
	s_waitcnt lgkmcnt(0)
	v_mfma_f32_32x32x16_bf16 v[4:19], v[32:35], v[148:151], v[4:19]
	v_add_f32_e32 v2, v2, v85
	v_bitop3_b32 v85, v89, v216, 31 bitop3:0x6c
	v_lshl_add_u32 v85, v85, 4, v93
	ds_read_b128 v[148:151], v85
	v_bitop3_b32 v87, v89, v211, 31 bitop3:0x6c
	v_lshl_add_u32 v87, v87, 4, v93
	v_mov_b32_e32 v91, v1
	s_waitcnt lgkmcnt(0)
	v_mfma_f32_32x32x16_bf16 v[4:19], v[52:55], v[148:151], v[4:19]
	ds_read_b128 v[148:151], v87
	v_div_scale_f32 v85, s[8:9], v2, v2, 1.0
	v_lshl_add_u32 v93, v91, 9, 0
	v_bitop3_b32 v95, v91, v215, 31 bitop3:0x6c
	s_waitcnt lgkmcnt(0)
	v_mfma_f32_32x32x16_bf16 v[4:19], v[40:43], v[148:151], v[4:19]
	v_lshl_add_u32 v95, v95, 4, v93
	ds_read_b128 v[148:151], v95
	v_rcp_f32_e32 v89, v85
	v_bitop3_b32 v97, v91, v202, 31 bitop3:0x6c
	v_lshl_add_u32 v97, v97, 4, v93
	ds_read_b128 v[152:155], v97
	v_fma_f32 v87, -v85, v89, 1.0
	s_waitcnt lgkmcnt(1)
	v_mfma_f32_32x32x16_bf16 v[4:19], v[60:63], v[148:151], v[4:19]
	v_fmac_f32_e32 v89, v87, v89
	v_div_scale_f32 v87, vcc, 1.0, v2, 1.0
	v_mul_f32_e32 v95, v87, v89
	v_fma_f32 v97, -v85, v95, v87
	v_fmac_f32_e32 v95, v97, v89
	v_fma_f32 v85, -v85, v95, v87
	v_div_fmas_f32 v85, v85, v89, v95
	s_waitcnt lgkmcnt(0)
	v_mfma_f32_32x32x16_bf16 v[4:19], v[48:51], v[152:155], v[4:19]
	v_div_fixup_f32 v2, v85, v2, 1.0
	v_bitop3_b32 v85, v91, v213, 31 bitop3:0x6c
	v_lshl_add_u32 v85, v85, 4, v93
	ds_read_b128 v[148:151], v85
	v_bitop3_b32 v89, v91, v208, 31 bitop3:0x6c
	v_lshl_add_u32 v89, v89, 4, v93
	ds_read_b128 v[152:155], v89
	s_waitcnt lgkmcnt(1)
	v_mfma_f32_32x32x16_bf16 v[4:19], v[68:71], v[148:151], v[4:19]
	v_mov_b32_e32 v89, v1
	v_and_b32_e32 v87, 64, v229
	v_lshl_add_u32 v91, v89, 9, 0
	v_bitop3_b32 v93, v89, v212, 31 bitop3:0x6c
	v_lshl_add_u32 v93, v93, 4, v91
	s_waitcnt lgkmcnt(0)
	v_mfma_f32_32x32x16_bf16 v[4:19], v[56:59], v[152:155], v[4:19]
	ds_read_b128 v[148:151], v93
	v_bitop3_b32 v93, v89, v201, 31 bitop3:0x6c
	v_lshl_add_u32 v93, v93, 4, v91
	ds_read_b128 v[152:155], v93
	v_bitop3_b32 v93, v89, v210, 31 bitop3:0x6c
	v_lshl_add_u32 v93, v93, 4, v91
	v_bitop3_b32 v89, v89, v204, 31 bitop3:0x6c
	s_waitcnt lgkmcnt(1)
	v_mfma_f32_32x32x16_bf16 v[4:19], v[72:75], v[148:151], v[4:19]
	ds_read_b128 v[148:151], v93
	v_lshl_add_u32 v89, v89, 4, v91
	ds_read_b128 v[232:235], v89
	v_or_b32_e32 v85, v87, v156
	v_lshlrev_b32_e32 v85, 2, v85
	ds_bpermute_b32 v168, v85, v2
	ds_bpermute_b32 v167, v85, v2 offset:4
	s_waitcnt lgkmcnt(4)
	v_mfma_f32_32x32x16_bf16 v[4:19], v[64:67], v[152:155], v[4:19]
	ds_bpermute_b32 v166, v85, v2 offset:8
	ds_bpermute_b32 v165, v85, v2 offset:12
	ds_bpermute_b32 v164, v85, v2 offset:32
	ds_bpermute_b32 v163, v85, v2 offset:36
	ds_bpermute_b32 v162, v85, v2 offset:40
	ds_bpermute_b32 v161, v85, v2 offset:44
	ds_bpermute_b32 v160, v85, v2 offset:64
	s_waitcnt lgkmcnt(10)
	v_mfma_f32_32x32x16_bf16 v[4:19], v[76:79], v[148:151], v[4:19]
	ds_bpermute_b32 v159, v85, v2 offset:68
	ds_bpermute_b32 v158, v85, v2 offset:72
	ds_bpermute_b32 v157, v85, v2 offset:76
	ds_bpermute_b32 v156, v85, v2 offset:96
	ds_bpermute_b32 v155, v85, v2 offset:100
	ds_bpermute_b32 v154, v85, v2 offset:104
	ds_bpermute_b32 v152, v85, v2 offset:108
	s_waitcnt lgkmcnt(14)
	v_mfma_f32_32x32x16_bf16 v[4:19], v[80:83], v[232:235], v[4:19]
	s_setprio 0
	v_and_b32_e32 v2, 1, v220
	v_xor_b32_e32 v89, 1, v229
	v_add_u32_e32 v87, 64, v87
	v_cmp_eq_u32_e32 vcc, 0, v2
	v_or_b32_e32 v2, s0, v1
	v_cmp_lt_i32_e64 s[0:1], v89, v87
	v_ashrrev_i32_e32 v85, 31, v84
	s_nop 4
	v_mul_f32_e32 v150, v4, v168
	v_cndmask_b32_e64 v87, v229, v89, s[0:1]
	v_lshlrev_b32_e32 v153, 2, v87
	ds_bpermute_b32 v151, v153, v150
	v_readlane_b32 s0, v254, 35
	v_lshlrev_b32_e32 v2, 1, v2
	v_readlane_b32 s1, v254, 36
	v_lshlrev_b64 v[84:85], 13, v[84:85]
	s_nop 0
	v_lshl_add_u64 v[148:149], s[0:1], 0, v[2:3]
	v_lshl_add_u64 v[84:85], v[148:149], 0, v[84:85]
	s_and_saveexec_b64 s[0:1], vcc
	s_cbranch_execz .LBB0_1120
	s_waitcnt vmcnt(31)
	v_lshlrev_b32_e32 v194, 16, v224
	v_and_b32_e32 v195, 0xffff0000, v224
	s_waitcnt lgkmcnt(0)
	v_pk_mul_f32 v[150:151], v[150:151], v[194:195]
	s_nop 0
	v_and_b32_sdwa v4, v150, v227 dst_sel:DWORD dst_unused:UNUSED_PAD src0_sel:WORD_1 src1_sel:DWORD
	v_and_b32_sdwa v2, v151, v227 dst_sel:DWORD dst_unused:UNUSED_PAD src0_sel:WORD_1 src1_sel:DWORD
	v_add3_u32 v4, v150, v4, s97
	v_add3_u32 v2, v151, v2, s97
	v_lshrrev_b32_e32 v4, 16, v4
	v_and_or_b32 v2, v2, s85, v4
	global_store_dword v[84:85], v2, off

; __device__ __forceinline__ float bflo(unsigned w) { return __uint_as_float(w << 16); }
; __device__ __forceinline__ float bfhi(unsigned w) { return __uint_as_float(w & 0xffff0000u); }
; __device__ __forceinline__ unsigned pk2(float lo, float hi) { return f2bf(lo) | (f2bf(hi) << 16); }
; __device__ __forceinline__ int crow(int r, int hi) { return (r & 3) + 8 * (r >> 2) + 4 * hi; }
; __device__ __forceinline__ void unit(const bf16_t* proj, const bf16_t* mk, const bf16_t* mvt, bf16_t* Y3, int un, LAS unsigned char* lds) {
;     ...
;         for (int dbi = 0; dbi < 2; ++dbi) { const int db = hf * 2 + dbi; att::f32x16 o = att::f32x16{};
; #pragma unroll
;             for (int q4 = 0; q4 < 4; ++q4) { att::bf16x8 vf[4]; int rv = r32; asm volatile("" : "+v"(rv));
; #pragma unroll
;                 for (int i = 0; i < 4; ++i) vf[i] = frag(lds, db * 32 + rv, 2 * (q4 * 4 + i) + hi);
;                 asm volatile("" ::: "memory");
; #pragma unroll
;                 for (int i = 0; i < 4; ++i) o = __builtin_amdgcn_mfma_f32_32x32x16_bf16(pa[q4 * 4 + i], vf[i], o, 0, 0, 0); }
; #pragma unroll
;             for (int r = 0; r < 16; ++r) { const int bt = bt0 + att::crow(r, hi), col = h * 256 + db * 32 + r32; const float val = o[r] * rli[r], vn = __shfl_xor(val, 1);
;                 if ((r32 & 1) == 0) *(unsigned*)(Y3 + (size_t)bt * YS + col) = pk2(val * bflo(zz[dbi * 16 + r]), vn * bfhi(zz[dbi * 16 + r])); } } }
.LBB0_1150:
	s_or_b64 exec, exec, s[0:1]
	v_mov_b32_e32 v2, v1
	s_waitcnt vmcnt(16)
	v_lshl_add_u32 v185, v2, 9, 0
	s_waitcnt lgkmcnt(0)
	v_bitop3_b32 v4, v2, v200, 31 bitop3:0x6c
	v_lshl_add_u32 v4, v4, 4, v185
	ds_read_b128 v[4:7], v4 offset:16384
	v_bitop3_b32 v148, v2, v209, 31 bitop3:0x6c
	v_lshl_add_u32 v148, v148, 4, v185
	ds_read_b128 v[148:151], v148 offset:16384
	s_waitcnt lgkmcnt(1)
	s_setprio 1
	v_mfma_f32_32x32x16_bf16 v[4:19], v[28:31], v[4:7], 0
	s_waitcnt lgkmcnt(0)
	v_mfma_f32_32x32x16_bf16 v[4:19], v[20:23], v[148:151], v[4:19]
	v_bitop3_b32 v148, v2, v218, 31 bitop3:0x6c
	v_lshl_add_u32 v148, v148, 4, v185
	ds_read_b128 v[148:151], v148 offset:16384
	v_bitop3_b32 v2, v2, v214, 31 bitop3:0x6c
	v_lshl_add_u32 v2, v2, 4, v185
	s_waitcnt lgkmcnt(0)
	v_mfma_f32_32x32x16_bf16 v[4:19], v[36:39], v[148:151], v[4:19]
	ds_read_b128 v[148:151], v2 offset:16384
	v_mov_b32_e32 v2, v1
	s_nop 0
	v_lshl_add_u32 v185, v2, 9, 0
	s_waitcnt lgkmcnt(0)
	v_mfma_f32_32x32x16_bf16 v[4:19], v[24:27], v[148:151], v[4:19]
	v_bitop3_b32 v148, v2, v217, 31 bitop3:0x6c
	v_lshl_add_u32 v148, v148, 4, v185
	ds_read_b128 v[148:151], v148 offset:16384
	s_waitcnt lgkmcnt(0)
	v_mfma_f32_32x32x16_bf16 v[4:19], v[44:47], v[148:151], v[4:19]
	v_bitop3_b32 v148, v2, v206, 31 bitop3:0x6c
	v_lshl_add_u32 v148, v148, 4, v185
	ds_read_b128 v[148:151], v148 offset:16384
	s_waitcnt lgkmcnt(0)
	v_mfma_f32_32x32x16_bf16 v[4:19], v[32:35], v[148:151], v[4:19]
	v_bitop3_b32 v148, v2, v216, 31 bitop3:0x6c
	v_lshl_add_u32 v148, v148, 4, v185
	ds_read_b128 v[148:151], v148 offset:16384
	v_bitop3_b32 v2, v2, v211, 31 bitop3:0x6c
	v_lshl_add_u32 v2, v2, 4, v185
	s_waitcnt lgkmcnt(0)
	v_mfma_f32_32x32x16_bf16 v[4:19], v[52:55], v[148:151], v[4:19]
	ds_read_b128 v[148:151], v2 offset:16384
	v_mov_b32_e32 v2, v1
	s_nop 0
	v_lshl_add_u32 v185, v2, 9, 0
	s_waitcnt lgkmcnt(0)
	v_mfma_f32_32x32x16_bf16 v[4:19], v[40:43], v[148:151], v[4:19]
	v_bitop3_b32 v148, v2, v215, 31 bitop3:0x6c
	v_lshl_add_u32 v148, v148, 4, v185
	ds_read_b128 v[148:151], v148 offset:16384
	s_waitcnt lgkmcnt(0)
	v_mfma_f32_32x32x16_bf16 v[4:19], v[60:63], v[148:151], v[4:19]
	v_bitop3_b32 v148, v2, v202, 31 bitop3:0x6c
	v_lshl_add_u32 v148, v148, 4, v185
	ds_read_b128 v[148:151], v148 offset:16384
	s_waitcnt lgkmcnt(0)
	v_mfma_f32_32x32x16_bf16 v[4:19], v[48:51], v[148:151], v[4:19]
	v_bitop3_b32 v148, v2, v213, 31 bitop3:0x6c
	v_lshl_add_u32 v148, v148, 4, v185
	ds_read_b128 v[148:151], v148 offset:16384
	v_bitop3_b32 v2, v2, v208, 31 bitop3:0x6c
	v_lshl_add_u32 v2, v2, 4, v185
	s_waitcnt lgkmcnt(0)
	v_mfma_f32_32x32x16_bf16 v[4:19], v[68:71], v[148:151], v[4:19]
	ds_read_b128 v[148:151], v2 offset:16384
	v_mov_b32_e32 v2, v1
	s_nop 0
	v_lshl_add_u32 v185, v2, 9, 0
	s_waitcnt lgkmcnt(0)
	v_mfma_f32_32x32x16_bf16 v[4:19], v[56:59], v[148:151], v[4:19]
	v_bitop3_b32 v148, v2, v212, 31 bitop3:0x6c
	v_lshl_add_u32 v148, v148, 4, v185
	ds_read_b128 v[148:151], v148 offset:16384
	s_waitcnt lgkmcnt(0)
	v_mfma_f32_32x32x16_bf16 v[4:19], v[72:75], v[148:151], v[4:19]
	v_bitop3_b32 v148, v2, v201, 31 bitop3:0x6c
	v_lshl_add_u32 v148, v148, 4, v185
	ds_read_b128 v[148:151], v148 offset:16384
	s_waitcnt lgkmcnt(0)
	v_mfma_f32_32x32x16_bf16 v[4:19], v[64:67], v[148:151], v[4:19]
	v_bitop3_b32 v148, v2, v210, 31 bitop3:0x6c
	v_lshl_add_u32 v148, v148, 4, v185
	ds_read_b128 v[148:151], v148 offset:16384
	v_bitop3_b32 v2, v2, v204, 31 bitop3:0x6c
	v_lshl_add_u32 v2, v2, 4, v185
	s_waitcnt lgkmcnt(0)
	v_mfma_f32_32x32x16_bf16 v[4:19], v[76:79], v[148:151], v[4:19]
	ds_read_b128 v[148:151], v2 offset:16384
	s_waitcnt lgkmcnt(0)
	v_mfma_f32_32x32x16_bf16 v[4:19], v[80:83], v[148:151], v[4:19]
	s_setprio 0
	s_nop 11
	v_mul_f32_e32 v148, v4, v168
	ds_bpermute_b32 v149, v153, v148
	s_and_saveexec_b64 s[0:1], vcc
	s_cbranch_execz .LBB0_1152
	s_waitcnt vmcnt(15)
	v_lshlrev_b32_e32 v150, 16, v184
	v_and_b32_e32 v151, 0xffff0000, v184
	s_waitcnt lgkmcnt(0)
	v_pk_mul_f32 v[148:149], v[148:149], v[150:151]
	s_nop 0
	v_and_b32_sdwa v4, v148, v227 dst_sel:DWORD dst_unused:UNUSED_PAD src0_sel:WORD_1 src1_sel:DWORD
	v_and_b32_sdwa v2, v149, v227 dst_sel:DWORD dst_unused:UNUSED_PAD src0_sel:WORD_1 src1_sel:DWORD
	v_add3_u32 v4, v148, v4, s97
	v_add3_u32 v2, v149, v2, s97
	v_lshrrev_b32_e32 v4, 16, v4
	v_and_or_b32 v2, v2, s85, v4
	global_store_dword v[84:85], v2, off offset:64

; __device__ __forceinline__ float bflo(unsigned w) { return __uint_as_float(w << 16); }
; __device__ __forceinline__ float bfhi(unsigned w) { return __uint_as_float(w & 0xffff0000u); }
; __device__ __forceinline__ unsigned pk2(float lo, float hi) { return f2bf(lo) | (f2bf(hi) << 16); }
; __device__ __forceinline__ int crow(int r, int hi) { return (r & 3) + 8 * (r >> 2) + 4 * hi; }
; __device__ __forceinline__ void unit(const bf16_t* proj, const bf16_t* mk, const bf16_t* mvt, bf16_t* Y3, int un, LAS unsigned char* lds) {
;     ...
;     for (int hf = 0; hf < 4; ++hf) { unsigned zz[32];
; #pragma unroll
;         for (int dbi = 0; dbi < 2; ++dbi)
; #pragma unroll
;             for (int r = 0; r < 16; ++r) zz[dbi * 16 + r] = *(const unsigned*)(proj + (size_t)(bt0 + att::crow(r, hi)) * NC + C_ZM + h * 256 + (hf * 2 + dbi) * 32 + (r32 & ~1));
;         asm volatile("" ::: "memory");
; #pragma unroll
;         for (int dbi = 0; dbi < 2; ++dbi) { const int db = hf * 2 + dbi; att::f32x16 o = att::f32x16{};
; #pragma unroll
;             for (int q4 = 0; q4 < 4; ++q4) { att::bf16x8 vf[4]; int rv = r32; asm volatile("" : "+v"(rv));
; #pragma unroll
;                 for (int i = 0; i < 4; ++i) vf[i] = frag(lds, db * 32 + rv, 2 * (q4 * 4 + i) + hi);
;                 asm volatile("" ::: "memory");
; #pragma unroll
;                 for (int i = 0; i < 4; ++i) o = __builtin_amdgcn_mfma_f32_32x32x16_bf16(pa[q4 * 4 + i], vf[i], o, 0, 0, 0); }
; #pragma unroll
;             for (int r = 0; r < 16; ++r) { const int bt = bt0 + att::crow(r, hi), col = h * 256 + db * 32 + r32; const float val = o[r] * rli[r], vn = __shfl_xor(val, 1);
;                 if ((r32 & 1) == 0) *(unsigned*)(Y3 + (size_t)bt * YS + col) = pk2(val * bflo(zz[dbi * 16 + r]), vn * bfhi(zz[dbi * 16 + r])); } } }
.LBB0_1182:
	s_or_b64 exec, exec, s[0:1]
	v_mov_b32_e32 v148, v1
	global_load_dword v199, v[116:117], off offset:128
	global_load_dword v198, v[118:119], off offset:128
	global_load_dword v197, v[120:121], off offset:128
	global_load_dword v196, v[124:125], off offset:128
	global_load_dword v178, v[124:125], off offset:192
	global_load_dword v179, v[120:121], off offset:192
	global_load_dword v180, v[118:119], off offset:192
	global_load_dword v181, v[116:117], off offset:192
	global_load_dword v193, v[122:123], off offset:128
	global_load_dword v192, v[126:127], off offset:128
	global_load_dword v191, v[128:129], off offset:128
	global_load_dword v190, v[130:131], off offset:128
	global_load_dword v174, v[130:131], off offset:192
	global_load_dword v175, v[128:129], off offset:192
	global_load_dword v176, v[126:127], off offset:192
	global_load_dword v177, v[122:123], off offset:192
	global_load_dword v189, v[132:133], off offset:128
	global_load_dword v188, v[134:135], off offset:128
	global_load_dword v187, v[136:137], off offset:128
	global_load_dword v186, v[140:141], off offset:128
	global_load_dword v170, v[140:141], off offset:192
	global_load_dword v171, v[136:137], off offset:192
	global_load_dword v172, v[134:135], off offset:192
	global_load_dword v173, v[132:133], off offset:192
	global_load_dword v185, v[138:139], off offset:128
	global_load_dword v184, v[142:143], off offset:128
	global_load_dword v183, v[144:145], off offset:128
	global_load_dword v182, v[146:147], off offset:128
	global_load_dword v2, v[146:147], off offset:192
	global_load_dword v150, v[144:145], off offset:192
	global_load_dword v151, v[142:143], off offset:192
	global_load_dword v169, v[138:139], off offset:192
	s_nop 0
	v_lshl_add_u32 v149, v148, 9, 0
	s_waitcnt lgkmcnt(0)
	v_bitop3_b32 v4, v148, v200, 31 bitop3:0x6c
	v_lshl_add_u32 v4, v4, 4, v149
	ds_read_b128 v[4:7], v4 offset:32768
	v_bitop3_b32 v194, v148, v209, 31 bitop3:0x6c
	v_lshl_add_u32 v194, v194, 4, v149
	ds_read_b128 v[232:235], v194 offset:32768
	s_waitcnt lgkmcnt(1)
	s_setprio 1
	v_mfma_f32_32x32x16_bf16 v[4:19], v[28:31], v[4:7], 0
	v_bitop3_b32 v194, v148, v218, 31 bitop3:0x6c
	v_lshl_add_u32 v194, v194, 4, v149
	v_bitop3_b32 v148, v148, v214, 31 bitop3:0x6c
	v_lshl_add_u32 v148, v148, 4, v149
	s_waitcnt lgkmcnt(0)
	v_mfma_f32_32x32x16_bf16 v[4:19], v[20:23], v[232:235], v[4:19]
	ds_read_b128 v[232:235], v194 offset:32768
	s_waitcnt lgkmcnt(0)
	v_mfma_f32_32x32x16_bf16 v[4:19], v[36:39], v[232:235], v[4:19]
	ds_read_b128 v[232:235], v148 offset:32768
	v_mov_b32_e32 v148, v1
	s_nop 0
	v_lshl_add_u32 v149, v148, 9, 0
	v_bitop3_b32 v194, v148, v217, 31 bitop3:0x6c
	s_waitcnt lgkmcnt(0)
	v_mfma_f32_32x32x16_bf16 v[4:19], v[24:27], v[232:235], v[4:19]
	v_lshl_add_u32 v194, v194, 4, v149
	ds_read_b128 v[232:235], v194 offset:32768
	v_bitop3_b32 v194, v148, v206, 31 bitop3:0x6c
	v_lshl_add_u32 v194, v194, 4, v149
	s_waitcnt lgkmcnt(0)
	v_mfma_f32_32x32x16_bf16 v[4:19], v[44:47], v[232:235], v[4:19]
	ds_read_b128 v[232:235], v194 offset:32768
	v_bitop3_b32 v194, v148, v216, 31 bitop3:0x6c
	v_lshl_add_u32 v194, v194, 4, v149
	v_bitop3_b32 v148, v148, v211, 31 bitop3:0x6c
	v_lshl_add_u32 v148, v148, 4, v149
	s_waitcnt lgkmcnt(0)
	v_mfma_f32_32x32x16_bf16 v[4:19], v[32:35], v[232:235], v[4:19]
	ds_read_b128 v[232:235], v194 offset:32768
	s_waitcnt lgkmcnt(0)
	v_mfma_f32_32x32x16_bf16 v[4:19], v[52:55], v[232:235], v[4:19]
	ds_read_b128 v[232:235], v148 offset:32768
	v_mov_b32_e32 v148, v1
	s_nop 0
	v_lshl_add_u32 v149, v148, 9, 0
	v_bitop3_b32 v194, v148, v215, 31 bitop3:0x6c
	s_waitcnt lgkmcnt(0)
	v_mfma_f32_32x32x16_bf16 v[4:19], v[40:43], v[232:235], v[4:19]
	v_lshl_add_u32 v194, v194, 4, v149
	ds_read_b128 v[232:235], v194 offset:32768
	v_bitop3_b32 v194, v148, v202, 31 bitop3:0x6c
	v_lshl_add_u32 v194, v194, 4, v149
	s_waitcnt lgkmcnt(0)
	v_mfma_f32_32x32x16_bf16 v[4:19], v[60:63], v[232:235], v[4:19]
	ds_read_b128 v[232:235], v194 offset:32768
	v_bitop3_b32 v194, v148, v213, 31 bitop3:0x6c
	v_lshl_add_u32 v194, v194, 4, v149
	v_bitop3_b32 v148, v148, v208, 31 bitop3:0x6c
	v_lshl_add_u32 v148, v148, 4, v149
	s_waitcnt lgkmcnt(0)
	v_mfma_f32_32x32x16_bf16 v[4:19], v[48:51], v[232:235], v[4:19]
	ds_read_b128 v[232:235], v194 offset:32768
	s_waitcnt lgkmcnt(0)
	v_mfma_f32_32x32x16_bf16 v[4:19], v[68:71], v[232:235], v[4:19]
	ds_read_b128 v[232:235], v148 offset:32768
	v_mov_b32_e32 v148, v1
	s_nop 0
	v_lshl_add_u32 v149, v148, 9, 0
	v_bitop3_b32 v194, v148, v212, 31 bitop3:0x6c
	s_waitcnt lgkmcnt(0)
	v_mfma_f32_32x32x16_bf16 v[4:19], v[56:59], v[232:235], v[4:19]
	v_lshl_add_u32 v194, v194, 4, v149
	ds_read_b128 v[232:235], v194 offset:32768
	v_bitop3_b32 v194, v148, v201, 31 bitop3:0x6c
	v_lshl_add_u32 v194, v194, 4, v149
	s_waitcnt lgkmcnt(0)
	v_mfma_f32_32x32x16_bf16 v[4:19], v[72:75], v[232:235], v[4:19]
	ds_read_b128 v[232:235], v194 offset:32768
	v_bitop3_b32 v194, v148, v210, 31 bitop3:0x6c
	v_lshl_add_u32 v194, v194, 4, v149
	v_bitop3_b32 v148, v148, v204, 31 bitop3:0x6c
	v_lshl_add_u32 v148, v148, 4, v149
	s_waitcnt lgkmcnt(0)
	v_mfma_f32_32x32x16_bf16 v[4:19], v[64:67], v[232:235], v[4:19]
	ds_read_b128 v[232:235], v194 offset:32768
	s_waitcnt lgkmcnt(0)
	v_mfma_f32_32x32x16_bf16 v[4:19], v[76:79], v[232:235], v[4:19]
	ds_read_b128 v[232:235], v148 offset:32768
	s_waitcnt lgkmcnt(0)
	v_mfma_f32_32x32x16_bf16 v[4:19], v[80:83], v[232:235], v[4:19]
	s_setprio 0
	s_nop 11
	v_mul_f32_e32 v148, v4, v168
	ds_bpermute_b32 v149, v153, v148
	s_and_saveexec_b64 s[0:1], vcc
	s_cbranch_execz .LBB0_1184
	s_waitcnt vmcnt(31)
	v_lshlrev_b32_e32 v194, 16, v199
	v_and_b32_e32 v195, 0xffff0000, v199
	s_waitcnt lgkmcnt(0)
	v_pk_mul_f32 v[148:149], v[148:149], v[194:195]
	s_nop 0
	v_and_b32_sdwa v194, v148, v227 dst_sel:DWORD dst_unused:UNUSED_PAD src0_sel:WORD_1 src1_sel:DWORD
	v_and_b32_sdwa v4, v149, v227 dst_sel:DWORD dst_unused:UNUSED_PAD src0_sel:WORD_1 src1_sel:DWORD
	v_add3_u32 v148, v148, v194, s97
	v_add3_u32 v4, v149, v4, s97
	v_lshrrev_b32_e32 v148, 16, v148
	v_and_or_b32 v4, v4, s85, v148
	global_store_dword v[84:85], v4, off offset:128

; __device__ __forceinline__ float bflo(unsigned w) { return __uint_as_float(w << 16); }
; __device__ __forceinline__ float bfhi(unsigned w) { return __uint_as_float(w & 0xffff0000u); }
; __device__ __forceinline__ unsigned pk2(float lo, float hi) { return f2bf(lo) | (f2bf(hi) << 16); }
; __device__ __forceinline__ int crow(int r, int hi) { return (r & 3) + 8 * (r >> 2) + 4 * hi; }
; __device__ __forceinline__ void unit(const bf16_t* proj, const bf16_t* mk, const bf16_t* mvt, bf16_t* Y3, int un, LAS unsigned char* lds) {
;     ...
;         for (int dbi = 0; dbi < 2; ++dbi) { const int db = hf * 2 + dbi; att::f32x16 o = att::f32x16{};
; #pragma unroll
;             for (int q4 = 0; q4 < 4; ++q4) { att::bf16x8 vf[4]; int rv = r32; asm volatile("" : "+v"(rv));
; #pragma unroll
;                 for (int i = 0; i < 4; ++i) vf[i] = frag(lds, db * 32 + rv, 2 * (q4 * 4 + i) + hi);
;                 asm volatile("" ::: "memory");
; #pragma unroll
;                 for (int i = 0; i < 4; ++i) o = __builtin_amdgcn_mfma_f32_32x32x16_bf16(pa[q4 * 4 + i], vf[i], o, 0, 0, 0); }
; #pragma unroll
;             for (int r = 0; r < 16; ++r) { const int bt = bt0 + att::crow(r, hi), col = h * 256 + db * 32 + r32; const float val = o[r] * rli[r], vn = __shfl_xor(val, 1);
;                 if ((r32 & 1) == 0) *(unsigned*)(Y3 + (size_t)bt * YS + col) = pk2(val * bflo(zz[dbi * 16 + r]), vn * bfhi(zz[dbi * 16 + r])); } } }
.LBB0_1214:
	s_or_b64 exec, exec, s[0:1]
	v_mov_b32_e32 v148, v1
	s_nop 0
	v_lshl_add_u32 v149, v148, 9, 0
	s_waitcnt lgkmcnt(0)
	v_bitop3_b32 v4, v148, v200, 31 bitop3:0x6c
	v_lshl_add_u32 v4, v4, 4, v149
	ds_read_b128 v[4:7], v4 offset:49152
	s_waitcnt vmcnt(4)
	v_bitop3_b32 v182, v148, v209, 31 bitop3:0x6c
	v_lshl_add_u32 v182, v182, 4, v149
	ds_read_b128 v[182:185], v182 offset:49152
	s_waitcnt lgkmcnt(1)
	s_setprio 1
	v_mfma_f32_32x32x16_bf16 v[4:19], v[28:31], v[4:7], 0
	s_waitcnt lgkmcnt(0)
	v_mfma_f32_32x32x16_bf16 v[4:19], v[20:23], v[182:185], v[4:19]
	v_bitop3_b32 v182, v148, v218, 31 bitop3:0x6c
	v_lshl_add_u32 v182, v182, 4, v149
	ds_read_b128 v[182:185], v182 offset:49152
	v_bitop3_b32 v148, v148, v214, 31 bitop3:0x6c
	v_lshl_add_u32 v148, v148, 4, v149
	s_waitcnt lgkmcnt(0)
	v_mfma_f32_32x32x16_bf16 v[4:19], v[36:39], v[182:185], v[4:19]
	ds_read_b128 v[182:185], v148 offset:49152
	v_mov_b32_e32 v148, v1
	s_nop 0
	v_lshl_add_u32 v149, v148, 9, 0
	s_waitcnt lgkmcnt(0)
	v_mfma_f32_32x32x16_bf16 v[4:19], v[24:27], v[182:185], v[4:19]
	v_bitop3_b32 v182, v148, v217, 31 bitop3:0x6c
	v_lshl_add_u32 v182, v182, 4, v149
	ds_read_b128 v[182:185], v182 offset:49152
	s_waitcnt lgkmcnt(0)
	v_mfma_f32_32x32x16_bf16 v[4:19], v[44:47], v[182:185], v[4:19]
	v_bitop3_b32 v182, v148, v206, 31 bitop3:0x6c
	v_lshl_add_u32 v182, v182, 4, v149
	ds_read_b128 v[182:185], v182 offset:49152
	s_waitcnt lgkmcnt(0)
	v_mfma_f32_32x32x16_bf16 v[4:19], v[32:35], v[182:185], v[4:19]
	v_bitop3_b32 v182, v148, v216, 31 bitop3:0x6c
	v_lshl_add_u32 v182, v182, 4, v149
	ds_read_b128 v[182:185], v182 offset:49152
	v_bitop3_b32 v148, v148, v211, 31 bitop3:0x6c
	v_lshl_add_u32 v148, v148, 4, v149
	s_waitcnt lgkmcnt(0)
	v_mfma_f32_32x32x16_bf16 v[4:19], v[52:55], v[182:185], v[4:19]
	ds_read_b128 v[182:185], v148 offset:49152
	v_mov_b32_e32 v148, v1
	s_nop 0
	v_lshl_add_u32 v149, v148, 9, 0
	s_waitcnt lgkmcnt(0)
	v_mfma_f32_32x32x16_bf16 v[4:19], v[40:43], v[182:185], v[4:19]
	v_bitop3_b32 v182, v148, v215, 31 bitop3:0x6c
	v_lshl_add_u32 v182, v182, 4, v149
	ds_read_b128 v[182:185], v182 offset:49152
	s_waitcnt lgkmcnt(0)
	v_mfma_f32_32x32x16_bf16 v[4:19], v[60:63], v[182:185], v[4:19]
	v_bitop3_b32 v182, v148, v202, 31 bitop3:0x6c
	v_lshl_add_u32 v182, v182, 4, v149
	ds_read_b128 v[182:185], v182 offset:49152
	s_waitcnt lgkmcnt(0)
	v_mfma_f32_32x32x16_bf16 v[4:19], v[48:51], v[182:185], v[4:19]
	v_bitop3_b32 v182, v148, v213, 31 bitop3:0x6c
	v_lshl_add_u32 v182, v182, 4, v149
	ds_read_b128 v[182:185], v182 offset:49152
	v_bitop3_b32 v148, v148, v208, 31 bitop3:0x6c
	v_lshl_add_u32 v148, v148, 4, v149
	s_waitcnt lgkmcnt(0)
	v_mfma_f32_32x32x16_bf16 v[4:19], v[68:71], v[182:185], v[4:19]
	ds_read_b128 v[182:185], v148 offset:49152
	v_mov_b32_e32 v148, v1
	s_nop 0
	v_lshl_add_u32 v149, v148, 9, 0
	s_waitcnt lgkmcnt(0)
	v_mfma_f32_32x32x16_bf16 v[4:19], v[56:59], v[182:185], v[4:19]
	v_bitop3_b32 v182, v148, v212, 31 bitop3:0x6c
	v_lshl_add_u32 v182, v182, 4, v149
	ds_read_b128 v[182:185], v182 offset:49152
	s_waitcnt lgkmcnt(0)
	v_mfma_f32_32x32x16_bf16 v[4:19], v[72:75], v[182:185], v[4:19]
	v_bitop3_b32 v182, v148, v201, 31 bitop3:0x6c
	v_lshl_add_u32 v182, v182, 4, v149
	ds_read_b128 v[182:185], v182 offset:49152
	s_waitcnt lgkmcnt(0)
	v_mfma_f32_32x32x16_bf16 v[4:19], v[64:67], v[182:185], v[4:19]
	v_bitop3_b32 v182, v148, v210, 31 bitop3:0x6c
	v_lshl_add_u32 v182, v182, 4, v149
	ds_read_b128 v[182:185], v182 offset:49152
	v_bitop3_b32 v148, v148, v204, 31 bitop3:0x6c
	v_lshl_add_u32 v148, v148, 4, v149
	s_waitcnt lgkmcnt(0)
	v_mfma_f32_32x32x16_bf16 v[4:19], v[76:79], v[182:185], v[4:19]
	ds_read_b128 v[182:185], v148 offset:49152
	s_waitcnt lgkmcnt(0)
	v_mfma_f32_32x32x16_bf16 v[4:19], v[80:83], v[182:185], v[4:19]
	s_setprio 0
	s_nop 11
	v_mul_f32_e32 v148, v4, v168
	ds_bpermute_b32 v149, v153, v148
	s_and_saveexec_b64 s[0:1], vcc
	s_cbranch_execz .LBB0_1216
	v_lshlrev_b32_e32 v182, 16, v181
	v_and_b32_e32 v183, 0xffff0000, v181
	s_waitcnt lgkmcnt(0)
	v_pk_mul_f32 v[148:149], v[148:149], v[182:183]
	s_nop 0
	v_and_b32_sdwa v181, v148, v227 dst_sel:DWORD dst_unused:UNUSED_PAD src0_sel:WORD_1 src1_sel:DWORD
	v_and_b32_sdwa v4, v149, v227 dst_sel:DWORD dst_unused:UNUSED_PAD src0_sel:WORD_1 src1_sel:DWORD
	v_add3_u32 v148, v148, v181, s97
	v_add3_u32 v4, v149, v4, s97
	v_lshrrev_b32_e32 v148, 16, v148
	v_and_or_b32 v4, v4, s85, v148
	global_store_dword v[84:85], v4, off offset:192

; __device__ __forceinline__ float bflo(unsigned w) { return __uint_as_float(w << 16); }
; __device__ __forceinline__ float bfhi(unsigned w) { return __uint_as_float(w & 0xffff0000u); }
; __device__ __forceinline__ unsigned pk2(float lo, float hi) { return f2bf(lo) | (f2bf(hi) << 16); }
; __device__ __forceinline__ int crow(int r, int hi) { return (r & 3) + 8 * (r >> 2) + 4 * hi; }
; __device__ __forceinline__ void unit(const bf16_t* proj, const bf16_t* mk, const bf16_t* mvt, bf16_t* Y3, int un, LAS unsigned char* lds) {
;     ...
;     for (int hf = 0; hf < 4; ++hf) { unsigned zz[32];
; #pragma unroll
;         for (int dbi = 0; dbi < 2; ++dbi)
; #pragma unroll
;             for (int r = 0; r < 16; ++r) zz[dbi * 16 + r] = *(const unsigned*)(proj + (size_t)(bt0 + att::crow(r, hi)) * NC + C_ZM + h * 256 + (hf * 2 + dbi) * 32 + (r32 & ~1));
;         asm volatile("" ::: "memory");
; #pragma unroll
;         for (int dbi = 0; dbi < 2; ++dbi) { const int db = hf * 2 + dbi; att::f32x16 o = att::f32x16{};
; #pragma unroll
;             for (int q4 = 0; q4 < 4; ++q4) { att::bf16x8 vf[4]; int rv = r32; asm volatile("" : "+v"(rv));
; #pragma unroll
;                 for (int i = 0; i < 4; ++i) vf[i] = frag(lds, db * 32 + rv, 2 * (q4 * 4 + i) + hi);
;                 asm volatile("" ::: "memory");
; #pragma unroll
;                 for (int i = 0; i < 4; ++i) o = __builtin_amdgcn_mfma_f32_32x32x16_bf16(pa[q4 * 4 + i], vf[i], o, 0, 0, 0); }
; #pragma unroll
;             for (int r = 0; r < 16; ++r) { const int bt = bt0 + att::crow(r, hi), col = h * 256 + db * 32 + r32; const float val = o[r] * rli[r], vn = __shfl_xor(val, 1);
;                 if ((r32 & 1) == 0) *(unsigned*)(Y3 + (size_t)bt * YS + col) = pk2(val * bflo(zz[dbi * 16 + r]), vn * bfhi(zz[dbi * 16 + r])); } } }
.LBB0_1246:
	s_or_b64 exec, exec, s[0:1]
	v_mov_b32_e32 v148, v1
	global_load_dword v199, v[116:117], off offset:256
	global_load_dword v198, v[118:119], off offset:256
	global_load_dword v197, v[120:121], off offset:256
	global_load_dword v196, v[124:125], off offset:256
	global_load_dword v178, v[124:125], off offset:320
	global_load_dword v179, v[120:121], off offset:320
	global_load_dword v180, v[118:119], off offset:320
	global_load_dword v181, v[116:117], off offset:320
	global_load_dword v193, v[122:123], off offset:256
	global_load_dword v192, v[126:127], off offset:256
	global_load_dword v191, v[128:129], off offset:256
	global_load_dword v190, v[130:131], off offset:256
	global_load_dword v174, v[130:131], off offset:320
	global_load_dword v175, v[128:129], off offset:320
	global_load_dword v176, v[126:127], off offset:320
	global_load_dword v177, v[122:123], off offset:320
	global_load_dword v189, v[132:133], off offset:256
	global_load_dword v188, v[134:135], off offset:256
	global_load_dword v187, v[136:137], off offset:256
	global_load_dword v186, v[140:141], off offset:256
	global_load_dword v170, v[140:141], off offset:320
	global_load_dword v171, v[136:137], off offset:320
	global_load_dword v172, v[134:135], off offset:320
	global_load_dword v173, v[132:133], off offset:320
	global_load_dword v185, v[138:139], off offset:256
	global_load_dword v184, v[142:143], off offset:256
	global_load_dword v183, v[144:145], off offset:256
	global_load_dword v182, v[146:147], off offset:256
	global_load_dword v2, v[146:147], off offset:320
	global_load_dword v150, v[144:145], off offset:320
	global_load_dword v151, v[142:143], off offset:320
	global_load_dword v169, v[138:139], off offset:320
	s_nop 0
	v_lshl_add_u32 v149, v148, 9, s7
	s_waitcnt lgkmcnt(0)
	v_bitop3_b32 v4, v148, v200, 31 bitop3:0x6c
	v_lshl_add_u32 v4, v4, 4, v149
	ds_read_b128 v[4:7], v4
	v_bitop3_b32 v194, v148, v209, 31 bitop3:0x6c
	v_lshl_add_u32 v194, v194, 4, v149
	ds_read_b128 v[232:235], v194
	s_waitcnt lgkmcnt(1)
	s_setprio 1
	v_mfma_f32_32x32x16_bf16 v[4:19], v[28:31], v[4:7], 0
	v_bitop3_b32 v194, v148, v218, 31 bitop3:0x6c
	v_lshl_add_u32 v194, v194, 4, v149
	v_bitop3_b32 v148, v148, v214, 31 bitop3:0x6c
	v_lshl_add_u32 v148, v148, 4, v149
	s_waitcnt lgkmcnt(0)
	v_mfma_f32_32x32x16_bf16 v[4:19], v[20:23], v[232:235], v[4:19]
	ds_read_b128 v[232:235], v194
	s_waitcnt lgkmcnt(0)
	v_mfma_f32_32x32x16_bf16 v[4:19], v[36:39], v[232:235], v[4:19]
	ds_read_b128 v[232:235], v148
	v_mov_b32_e32 v148, v1
	s_nop 0
	v_lshl_add_u32 v149, v148, 9, s7
	v_bitop3_b32 v194, v148, v217, 31 bitop3:0x6c
	s_waitcnt lgkmcnt(0)
	v_mfma_f32_32x32x16_bf16 v[4:19], v[24:27], v[232:235], v[4:19]
	v_lshl_add_u32 v194, v194, 4, v149
	ds_read_b128 v[232:235], v194
	v_bitop3_b32 v194, v148, v206, 31 bitop3:0x6c
	v_lshl_add_u32 v194, v194, 4, v149
	s_waitcnt lgkmcnt(0)
	v_mfma_f32_32x32x16_bf16 v[4:19], v[44:47], v[232:235], v[4:19]
	ds_read_b128 v[232:235], v194
	v_bitop3_b32 v194, v148, v216, 31 bitop3:0x6c
	v_lshl_add_u32 v194, v194, 4, v149
	v_bitop3_b32 v148, v148, v211, 31 bitop3:0x6c
	v_lshl_add_u32 v148, v148, 4, v149
	s_waitcnt lgkmcnt(0)
	v_mfma_f32_32x32x16_bf16 v[4:19], v[32:35], v[232:235], v[4:19]
	ds_read_b128 v[232:235], v194
	s_waitcnt lgkmcnt(0)
	v_mfma_f32_32x32x16_bf16 v[4:19], v[52:55], v[232:235], v[4:19]
	ds_read_b128 v[232:235], v148
	v_mov_b32_e32 v148, v1
	s_nop 0
	v_lshl_add_u32 v149, v148, 9, s7
	v_bitop3_b32 v194, v148, v215, 31 bitop3:0x6c
	s_waitcnt lgkmcnt(0)
	v_mfma_f32_32x32x16_bf16 v[4:19], v[40:43], v[232:235], v[4:19]
	v_lshl_add_u32 v194, v194, 4, v149
	ds_read_b128 v[232:235], v194
	v_bitop3_b32 v194, v148, v202, 31 bitop3:0x6c
	v_lshl_add_u32 v194, v194, 4, v149
	s_waitcnt lgkmcnt(0)
	v_mfma_f32_32x32x16_bf16 v[4:19], v[60:63], v[232:235], v[4:19]
	ds_read_b128 v[232:235], v194
	v_bitop3_b32 v194, v148, v213, 31 bitop3:0x6c
	v_lshl_add_u32 v194, v194, 4, v149
	v_bitop3_b32 v148, v148, v208, 31 bitop3:0x6c
	v_lshl_add_u32 v148, v148, 4, v149
	s_waitcnt lgkmcnt(0)
	v_mfma_f32_32x32x16_bf16 v[4:19], v[48:51], v[232:235], v[4:19]
	ds_read_b128 v[232:235], v194
	s_waitcnt lgkmcnt(0)
	v_mfma_f32_32x32x16_bf16 v[4:19], v[68:71], v[232:235], v[4:19]
	ds_read_b128 v[232:235], v148
	v_mov_b32_e32 v148, v1
	s_nop 0
	v_lshl_add_u32 v149, v148, 9, s7
	v_bitop3_b32 v194, v148, v212, 31 bitop3:0x6c
	s_waitcnt lgkmcnt(0)
	v_mfma_f32_32x32x16_bf16 v[4:19], v[56:59], v[232:235], v[4:19]
	v_lshl_add_u32 v194, v194, 4, v149
	ds_read_b128 v[232:235], v194
	v_bitop3_b32 v194, v148, v201, 31 bitop3:0x6c
	v_lshl_add_u32 v194, v194, 4, v149
	s_waitcnt lgkmcnt(0)
	v_mfma_f32_32x32x16_bf16 v[4:19], v[72:75], v[232:235], v[4:19]
	ds_read_b128 v[232:235], v194
	v_bitop3_b32 v194, v148, v210, 31 bitop3:0x6c
	v_lshl_add_u32 v194, v194, 4, v149
	v_bitop3_b32 v148, v148, v204, 31 bitop3:0x6c
	v_lshl_add_u32 v148, v148, 4, v149
	s_waitcnt lgkmcnt(0)
	v_mfma_f32_32x32x16_bf16 v[4:19], v[64:67], v[232:235], v[4:19]
	ds_read_b128 v[232:235], v194
	s_waitcnt lgkmcnt(0)
	v_mfma_f32_32x32x16_bf16 v[4:19], v[76:79], v[232:235], v[4:19]
	ds_read_b128 v[232:235], v148
	s_waitcnt lgkmcnt(0)
	v_mfma_f32_32x32x16_bf16 v[4:19], v[80:83], v[232:235], v[4:19]
	s_setprio 0
	s_nop 11
	v_mul_f32_e32 v148, v4, v168
	ds_bpermute_b32 v149, v153, v148
	s_and_saveexec_b64 s[0:1], vcc
	s_cbranch_execz .LBB0_1248
	s_waitcnt vmcnt(31)
	v_lshlrev_b32_e32 v194, 16, v199
	v_and_b32_e32 v195, 0xffff0000, v199
	s_waitcnt lgkmcnt(0)
	v_pk_mul_f32 v[148:149], v[148:149], v[194:195]
	s_nop 0
	v_and_b32_sdwa v194, v148, v227 dst_sel:DWORD dst_unused:UNUSED_PAD src0_sel:WORD_1 src1_sel:DWORD
	v_and_b32_sdwa v4, v149, v227 dst_sel:DWORD dst_unused:UNUSED_PAD src0_sel:WORD_1 src1_sel:DWORD
	v_add3_u32 v148, v148, v194, s97
	v_add3_u32 v4, v149, v4, s97
	v_lshrrev_b32_e32 v148, 16, v148
	v_and_or_b32 v4, v4, s85, v148
	global_store_dword v[84:85], v4, off offset:256

; __device__ __forceinline__ float bflo(unsigned w) { return __uint_as_float(w << 16); }
; __device__ __forceinline__ float bfhi(unsigned w) { return __uint_as_float(w & 0xffff0000u); }
; __device__ __forceinline__ unsigned pk2(float lo, float hi) { return f2bf(lo) | (f2bf(hi) << 16); }
; __device__ __forceinline__ int crow(int r, int hi) { return (r & 3) + 8 * (r >> 2) + 4 * hi; }
; __device__ __forceinline__ void unit(const bf16_t* proj, const bf16_t* mk, const bf16_t* mvt, bf16_t* Y3, int un, LAS unsigned char* lds) {
;     ...
;         for (int dbi = 0; dbi < 2; ++dbi) { const int db = hf * 2 + dbi; att::f32x16 o = att::f32x16{};
; #pragma unroll
;             for (int q4 = 0; q4 < 4; ++q4) { att::bf16x8 vf[4]; int rv = r32; asm volatile("" : "+v"(rv));
; #pragma unroll
;                 for (int i = 0; i < 4; ++i) vf[i] = frag(lds, db * 32 + rv, 2 * (q4 * 4 + i) + hi);
;                 asm volatile("" ::: "memory");
; #pragma unroll
;                 for (int i = 0; i < 4; ++i) o = __builtin_amdgcn_mfma_f32_32x32x16_bf16(pa[q4 * 4 + i], vf[i], o, 0, 0, 0); }
; #pragma unroll
;             for (int r = 0; r < 16; ++r) { const int bt = bt0 + att::crow(r, hi), col = h * 256 + db * 32 + r32; const float val = o[r] * rli[r], vn = __shfl_xor(val, 1);
;                 if ((r32 & 1) == 0) *(unsigned*)(Y3 + (size_t)bt * YS + col) = pk2(val * bflo(zz[dbi * 16 + r]), vn * bfhi(zz[dbi * 16 + r])); } } }
.LBB0_1278:
	s_or_b64 exec, exec, s[0:1]
	v_mov_b32_e32 v148, v1
	s_nop 0
	v_lshl_add_u32 v149, v148, 9, s6
	s_waitcnt lgkmcnt(0)
	v_bitop3_b32 v4, v148, v200, 31 bitop3:0x6c
	v_lshl_add_u32 v4, v4, 4, v149
	ds_read_b128 v[4:7], v4
	s_waitcnt vmcnt(4)
	v_bitop3_b32 v182, v148, v209, 31 bitop3:0x6c
	v_lshl_add_u32 v182, v182, 4, v149
	ds_read_b128 v[182:185], v182
	s_waitcnt lgkmcnt(1)
	s_setprio 1
	v_mfma_f32_32x32x16_bf16 v[4:19], v[28:31], v[4:7], 0
	s_waitcnt lgkmcnt(0)
	v_mfma_f32_32x32x16_bf16 v[4:19], v[20:23], v[182:185], v[4:19]
	v_bitop3_b32 v182, v148, v218, 31 bitop3:0x6c
	v_lshl_add_u32 v182, v182, 4, v149
	ds_read_b128 v[182:185], v182
	v_bitop3_b32 v148, v148, v214, 31 bitop3:0x6c
	v_lshl_add_u32 v148, v148, 4, v149
	s_waitcnt lgkmcnt(0)
	v_mfma_f32_32x32x16_bf16 v[4:19], v[36:39], v[182:185], v[4:19]
	ds_read_b128 v[182:185], v148
	v_mov_b32_e32 v148, v1
	s_nop 0
	v_lshl_add_u32 v149, v148, 9, s6
	s_waitcnt lgkmcnt(0)
	v_mfma_f32_32x32x16_bf16 v[4:19], v[24:27], v[182:185], v[4:19]
	v_bitop3_b32 v182, v148, v217, 31 bitop3:0x6c
	v_lshl_add_u32 v182, v182, 4, v149
	ds_read_b128 v[182:185], v182
	s_waitcnt lgkmcnt(0)
	v_mfma_f32_32x32x16_bf16 v[4:19], v[44:47], v[182:185], v[4:19]
	v_bitop3_b32 v182, v148, v206, 31 bitop3:0x6c
	v_lshl_add_u32 v182, v182, 4, v149
	ds_read_b128 v[182:185], v182
	s_waitcnt lgkmcnt(0)
	v_mfma_f32_32x32x16_bf16 v[4:19], v[32:35], v[182:185], v[4:19]
	v_bitop3_b32 v182, v148, v216, 31 bitop3:0x6c
	v_lshl_add_u32 v182, v182, 4, v149
	ds_read_b128 v[182:185], v182
	v_bitop3_b32 v148, v148, v211, 31 bitop3:0x6c
	v_lshl_add_u32 v148, v148, 4, v149
	s_waitcnt lgkmcnt(0)
	v_mfma_f32_32x32x16_bf16 v[4:19], v[52:55], v[182:185], v[4:19]
	ds_read_b128 v[182:185], v148
	v_mov_b32_e32 v148, v1
	s_nop 0
	v_lshl_add_u32 v149, v148, 9, s6
	s_waitcnt lgkmcnt(0)
	v_mfma_f32_32x32x16_bf16 v[4:19], v[40:43], v[182:185], v[4:19]
	v_bitop3_b32 v182, v148, v215, 31 bitop3:0x6c
	v_lshl_add_u32 v182, v182, 4, v149
	ds_read_b128 v[182:185], v182
	s_waitcnt lgkmcnt(0)
	v_mfma_f32_32x32x16_bf16 v[4:19], v[60:63], v[182:185], v[4:19]
	v_bitop3_b32 v182, v148, v202, 31 bitop3:0x6c
	v_lshl_add_u32 v182, v182, 4, v149
	ds_read_b128 v[182:185], v182
	s_waitcnt lgkmcnt(0)
	v_mfma_f32_32x32x16_bf16 v[4:19], v[48:51], v[182:185], v[4:19]
	v_bitop3_b32 v182, v148, v213, 31 bitop3:0x6c
	v_lshl_add_u32 v182, v182, 4, v149
	ds_read_b128 v[182:185], v182
	v_bitop3_b32 v148, v148, v208, 31 bitop3:0x6c
	v_lshl_add_u32 v148, v148, 4, v149
	s_waitcnt lgkmcnt(0)
	v_mfma_f32_32x32x16_bf16 v[4:19], v[68:71], v[182:185], v[4:19]
	ds_read_b128 v[182:185], v148
	v_mov_b32_e32 v148, v1
	s_nop 0
	v_lshl_add_u32 v149, v148, 9, s6
	s_waitcnt lgkmcnt(0)
	v_mfma_f32_32x32x16_bf16 v[4:19], v[56:59], v[182:185], v[4:19]
	v_bitop3_b32 v182, v148, v212, 31 bitop3:0x6c
	v_lshl_add_u32 v182, v182, 4, v149
	ds_read_b128 v[182:185], v182
	s_waitcnt lgkmcnt(0)
	v_mfma_f32_32x32x16_bf16 v[4:19], v[72:75], v[182:185], v[4:19]
	v_bitop3_b32 v182, v148, v201, 31 bitop3:0x6c
	v_lshl_add_u32 v182, v182, 4, v149
	ds_read_b128 v[182:185], v182
	s_waitcnt lgkmcnt(0)
	v_mfma_f32_32x32x16_bf16 v[4:19], v[64:67], v[182:185], v[4:19]
	v_bitop3_b32 v182, v148, v210, 31 bitop3:0x6c
	v_lshl_add_u32 v182, v182, 4, v149
	ds_read_b128 v[182:185], v182
	v_bitop3_b32 v148, v148, v204, 31 bitop3:0x6c
	v_lshl_add_u32 v148, v148, 4, v149
	s_waitcnt lgkmcnt(0)
	v_mfma_f32_32x32x16_bf16 v[4:19], v[76:79], v[182:185], v[4:19]
	ds_read_b128 v[182:185], v148
	s_waitcnt lgkmcnt(0)
	v_mfma_f32_32x32x16_bf16 v[4:19], v[80:83], v[182:185], v[4:19]
	s_setprio 0
	s_nop 11
	v_mul_f32_e32 v148, v4, v168
	ds_bpermute_b32 v149, v153, v148
	s_and_saveexec_b64 s[0:1], vcc
	s_cbranch_execz .LBB0_1280
	v_lshlrev_b32_e32 v182, 16, v181
	v_and_b32_e32 v183, 0xffff0000, v181
	s_waitcnt lgkmcnt(0)
	v_pk_mul_f32 v[148:149], v[148:149], v[182:183]
	s_nop 0
	v_and_b32_sdwa v181, v148, v227 dst_sel:DWORD dst_unused:UNUSED_PAD src0_sel:WORD_1 src1_sel:DWORD
	v_and_b32_sdwa v4, v149, v227 dst_sel:DWORD dst_unused:UNUSED_PAD src0_sel:WORD_1 src1_sel:DWORD
	v_add3_u32 v148, v148, v181, s97
	v_add3_u32 v4, v149, v4, s97
	v_lshrrev_b32_e32 v148, 16, v148
	v_and_or_b32 v4, v4, s85, v148
	global_store_dword v[84:85], v4, off offset:320

; __device__ __forceinline__ float bflo(unsigned w) { return __uint_as_float(w << 16); }
; __device__ __forceinline__ float bfhi(unsigned w) { return __uint_as_float(w & 0xffff0000u); }
; __device__ __forceinline__ unsigned pk2(float lo, float hi) { return f2bf(lo) | (f2bf(hi) << 16); }
; __device__ __forceinline__ int crow(int r, int hi) { return (r & 3) + 8 * (r >> 2) + 4 * hi; }
; __device__ __forceinline__ void unit(const bf16_t* proj, const bf16_t* mk, const bf16_t* mvt, bf16_t* Y3, int un, LAS unsigned char* lds) {
;     ...
;     for (int hf = 0; hf < 4; ++hf) { unsigned zz[32];
; #pragma unroll
;         for (int dbi = 0; dbi < 2; ++dbi)
; #pragma unroll
;             for (int r = 0; r < 16; ++r) zz[dbi * 16 + r] = *(const unsigned*)(proj + (size_t)(bt0 + att::crow(r, hi)) * NC + C_ZM + h * 256 + (hf * 2 + dbi) * 32 + (r32 & ~1));
;         asm volatile("" ::: "memory");
; #pragma unroll
;         for (int dbi = 0; dbi < 2; ++dbi) { const int db = hf * 2 + dbi; att::f32x16 o = att::f32x16{};
; #pragma unroll
;             for (int q4 = 0; q4 < 4; ++q4) { att::bf16x8 vf[4]; int rv = r32; asm volatile("" : "+v"(rv));
; #pragma unroll
;                 for (int i = 0; i < 4; ++i) vf[i] = frag(lds, db * 32 + rv, 2 * (q4 * 4 + i) + hi);
;                 asm volatile("" ::: "memory");
; #pragma unroll
;                 for (int i = 0; i < 4; ++i) o = __builtin_amdgcn_mfma_f32_32x32x16_bf16(pa[q4 * 4 + i], vf[i], o, 0, 0, 0); }
; #pragma unroll
;             for (int r = 0; r < 16; ++r) { const int bt = bt0 + att::crow(r, hi), col = h * 256 + db * 32 + r32; const float val = o[r] * rli[r], vn = __shfl_xor(val, 1);
;                 if ((r32 & 1) == 0) *(unsigned*)(Y3 + (size_t)bt * YS + col) = pk2(val * bflo(zz[dbi * 16 + r]), vn * bfhi(zz[dbi * 16 + r])); } } }
.LBB0_1310:
	s_or_b64 exec, exec, s[0:1]
	global_load_dword v180, v[116:117], off offset:384
	global_load_dword v179, v[118:119], off offset:384
	global_load_dword v178, v[120:121], off offset:384
	global_load_dword v177, v[124:125], off offset:384
	global_load_dword v148, v[124:125], off offset:448
	global_load_dword v149, v[120:121], off offset:448
	global_load_dword v150, v[118:119], off offset:448
	global_load_dword v151, v[116:117], off offset:448
	global_load_dword v176, v[122:123], off offset:384
	global_load_dword v175, v[126:127], off offset:384
	global_load_dword v174, v[128:129], off offset:384
	global_load_dword v173, v[130:131], off offset:384
	global_load_dword v125, v[130:131], off offset:448
	s_nop 0
	global_load_dword v128, v[128:129], off offset:448
	s_nop 0
	global_load_dword v126, v[126:127], off offset:448
	s_nop 0
	global_load_dword v127, v[122:123], off offset:448
	global_load_dword v172, v[132:133], off offset:384
	global_load_dword v171, v[134:135], off offset:384
	global_load_dword v170, v[136:137], off offset:384
	global_load_dword v169, v[140:141], off offset:384
	global_load_dword v121, v[140:141], off offset:448
	global_load_dword v122, v[136:137], off offset:448
	global_load_dword v123, v[134:135], off offset:448
	global_load_dword v124, v[132:133], off offset:448
	s_nop 0
	global_load_dword v132, v[138:139], off offset:384
	global_load_dword v131, v[142:143], off offset:384
	global_load_dword v130, v[144:145], off offset:384
	global_load_dword v129, v[146:147], off offset:384
	global_load_dword v2, v[146:147], off offset:448
	global_load_dword v118, v[144:145], off offset:448
	global_load_dword v119, v[142:143], off offset:448
	global_load_dword v120, v[138:139], off offset:448
	v_mov_b32_e32 v116, v1
	s_nop 0
	v_lshl_add_u32 v117, v116, 9, s5
	s_waitcnt lgkmcnt(0)
	v_bitop3_b32 v4, v116, v200, 31 bitop3:0x6c
	v_lshl_add_u32 v4, v4, 4, v117
	ds_read_b128 v[4:7], v4
	v_bitop3_b32 v133, v116, v209, 31 bitop3:0x6c
	v_lshl_add_u32 v133, v133, 4, v117
	ds_read_b128 v[134:137], v133
	s_waitcnt lgkmcnt(1)
	s_setprio 1
	v_mfma_f32_32x32x16_bf16 v[4:19], v[28:31], v[4:7], 0
	v_bitop3_b32 v133, v116, v218, 31 bitop3:0x6c
	v_lshl_add_u32 v133, v133, 4, v117
	v_bitop3_b32 v116, v116, v214, 31 bitop3:0x6c
	v_lshl_add_u32 v116, v116, 4, v117
	s_waitcnt lgkmcnt(0)
	v_mfma_f32_32x32x16_bf16 v[4:19], v[20:23], v[134:137], v[4:19]
	ds_read_b128 v[134:137], v133
	s_waitcnt lgkmcnt(0)
	v_mfma_f32_32x32x16_bf16 v[4:19], v[36:39], v[134:137], v[4:19]
	ds_read_b128 v[134:137], v116
	v_mov_b32_e32 v116, v1
	s_nop 0
	v_lshl_add_u32 v117, v116, 9, s5
	v_bitop3_b32 v133, v116, v217, 31 bitop3:0x6c
	s_waitcnt lgkmcnt(0)
	v_mfma_f32_32x32x16_bf16 v[4:19], v[24:27], v[134:137], v[4:19]
	v_lshl_add_u32 v133, v133, 4, v117
	ds_read_b128 v[134:137], v133
	v_bitop3_b32 v133, v116, v206, 31 bitop3:0x6c
	v_lshl_add_u32 v133, v133, 4, v117
	s_waitcnt lgkmcnt(0)
	v_mfma_f32_32x32x16_bf16 v[4:19], v[44:47], v[134:137], v[4:19]
	ds_read_b128 v[134:137], v133
	v_bitop3_b32 v133, v116, v216, 31 bitop3:0x6c
	v_lshl_add_u32 v133, v133, 4, v117
	v_bitop3_b32 v116, v116, v211, 31 bitop3:0x6c
	v_lshl_add_u32 v116, v116, 4, v117
	s_waitcnt lgkmcnt(0)
	v_mfma_f32_32x32x16_bf16 v[4:19], v[32:35], v[134:137], v[4:19]
	ds_read_b128 v[134:137], v133
	s_waitcnt lgkmcnt(0)
	v_mfma_f32_32x32x16_bf16 v[4:19], v[52:55], v[134:137], v[4:19]
	ds_read_b128 v[134:137], v116
	v_mov_b32_e32 v116, v1
	s_nop 0
	v_lshl_add_u32 v117, v116, 9, s5
	v_bitop3_b32 v133, v116, v215, 31 bitop3:0x6c
	s_waitcnt lgkmcnt(0)
	v_mfma_f32_32x32x16_bf16 v[4:19], v[40:43], v[134:137], v[4:19]
	v_lshl_add_u32 v133, v133, 4, v117
	ds_read_b128 v[134:137], v133
	v_bitop3_b32 v133, v116, v202, 31 bitop3:0x6c
	v_lshl_add_u32 v133, v133, 4, v117
	s_waitcnt lgkmcnt(0)
	v_mfma_f32_32x32x16_bf16 v[4:19], v[60:63], v[134:137], v[4:19]
	ds_read_b128 v[134:137], v133
	v_bitop3_b32 v133, v116, v213, 31 bitop3:0x6c
	v_lshl_add_u32 v133, v133, 4, v117
	v_bitop3_b32 v116, v116, v208, 31 bitop3:0x6c
	v_lshl_add_u32 v116, v116, 4, v117
	s_waitcnt lgkmcnt(0)
	v_mfma_f32_32x32x16_bf16 v[4:19], v[48:51], v[134:137], v[4:19]
	ds_read_b128 v[134:137], v133
	s_waitcnt lgkmcnt(0)
	v_mfma_f32_32x32x16_bf16 v[4:19], v[68:71], v[134:137], v[4:19]
	ds_read_b128 v[134:137], v116
	v_mov_b32_e32 v116, v1
	s_nop 0
	v_lshl_add_u32 v117, v116, 9, s5
	v_bitop3_b32 v133, v116, v212, 31 bitop3:0x6c
	s_waitcnt lgkmcnt(0)
	v_mfma_f32_32x32x16_bf16 v[4:19], v[56:59], v[134:137], v[4:19]
	v_lshl_add_u32 v133, v133, 4, v117
	ds_read_b128 v[134:137], v133
	v_bitop3_b32 v133, v116, v201, 31 bitop3:0x6c
	v_lshl_add_u32 v133, v133, 4, v117
	s_waitcnt lgkmcnt(0)
	v_mfma_f32_32x32x16_bf16 v[4:19], v[72:75], v[134:137], v[4:19]
	ds_read_b128 v[134:137], v133
	v_bitop3_b32 v133, v116, v210, 31 bitop3:0x6c
	v_lshl_add_u32 v133, v133, 4, v117
	v_bitop3_b32 v116, v116, v204, 31 bitop3:0x6c
	v_lshl_add_u32 v116, v116, 4, v117
	s_waitcnt lgkmcnt(0)
	v_mfma_f32_32x32x16_bf16 v[4:19], v[64:67], v[134:137], v[4:19]
	ds_read_b128 v[134:137], v133
	s_waitcnt lgkmcnt(0)
	v_mfma_f32_32x32x16_bf16 v[4:19], v[76:79], v[134:137], v[4:19]
	ds_read_b128 v[134:137], v116
	s_waitcnt lgkmcnt(0)
	v_mfma_f32_32x32x16_bf16 v[4:19], v[80:83], v[134:137], v[4:19]
	s_setprio 0
	s_nop 11
	v_mul_f32_e32 v116, v4, v168
	ds_bpermute_b32 v117, v153, v116
	s_and_saveexec_b64 s[0:1], vcc
	s_cbranch_execz .LBB0_1312
	s_waitcnt vmcnt(31)
	v_lshlrev_b32_e32 v134, 16, v180
	v_and_b32_e32 v135, 0xffff0000, v180
	s_waitcnt lgkmcnt(0)
	v_pk_mul_f32 v[116:117], v[116:117], v[134:135]
	s_nop 0
	v_and_b32_sdwa v133, v116, v227 dst_sel:DWORD dst_unused:UNUSED_PAD src0_sel:WORD_1 src1_sel:DWORD
	v_and_b32_sdwa v4, v117, v227 dst_sel:DWORD dst_unused:UNUSED_PAD src0_sel:WORD_1 src1_sel:DWORD
	v_add3_u32 v116, v116, v133, s97
	v_add3_u32 v4, v117, v4, s97
	v_lshrrev_b32_e32 v116, 16, v116
	v_and_or_b32 v4, v4, s85, v116
	global_store_dword v[84:85], v4, off offset:384

; __device__ __forceinline__ float bflo(unsigned w) { return __uint_as_float(w << 16); }
; __device__ __forceinline__ float bfhi(unsigned w) { return __uint_as_float(w & 0xffff0000u); }
; __device__ __forceinline__ unsigned pk2(float lo, float hi) { return f2bf(lo) | (f2bf(hi) << 16); }
; __device__ __forceinline__ int crow(int r, int hi) { return (r & 3) + 8 * (r >> 2) + 4 * hi; }
; __device__ __forceinline__ void unit(const bf16_t* proj, const bf16_t* mk, const bf16_t* mvt, bf16_t* Y3, int un, LAS unsigned char* lds) {
;     ...
;         for (int dbi = 0; dbi < 2; ++dbi) { const int db = hf * 2 + dbi; att::f32x16 o = att::f32x16{};
; #pragma unroll
;             for (int q4 = 0; q4 < 4; ++q4) { att::bf16x8 vf[4]; int rv = r32; asm volatile("" : "+v"(rv));
; #pragma unroll
;                 for (int i = 0; i < 4; ++i) vf[i] = frag(lds, db * 32 + rv, 2 * (q4 * 4 + i) + hi);
;                 asm volatile("" ::: "memory");
; #pragma unroll
;                 for (int i = 0; i < 4; ++i) o = __builtin_amdgcn_mfma_f32_32x32x16_bf16(pa[q4 * 4 + i], vf[i], o, 0, 0, 0); }
; #pragma unroll
;             for (int r = 0; r < 16; ++r) { const int bt = bt0 + att::crow(r, hi), col = h * 256 + db * 32 + r32; const float val = o[r] * rli[r], vn = __shfl_xor(val, 1);
;                 if ((r32 & 1) == 0) *(unsigned*)(Y3 + (size_t)bt * YS + col) = pk2(val * bflo(zz[dbi * 16 + r]), vn * bfhi(zz[dbi * 16 + r])); } } }
.LBB0_1342:
	s_or_b64 exec, exec, s[0:1]
	v_mov_b32_e32 v116, v1
	s_nop 0
	v_lshl_add_u32 v117, v116, 9, s4
	s_waitcnt lgkmcnt(0)
	v_bitop3_b32 v4, v116, v200, 31 bitop3:0x6c
	v_lshl_add_u32 v4, v4, 4, v117
	ds_read_b128 v[4:7], v4
	s_waitcnt lgkmcnt(0)
	s_setprio 1
	v_mfma_f32_32x32x16_bf16 v[4:19], v[28:31], v[4:7], 0
	v_bitop3_b32 v28, v116, v209, 31 bitop3:0x6c
	v_lshl_add_u32 v28, v28, 4, v117
	ds_read_b128 v[28:31], v28
	s_waitcnt lgkmcnt(0)
	v_mfma_f32_32x32x16_bf16 v[4:19], v[20:23], v[28:31], v[4:19]
	v_bitop3_b32 v20, v116, v218, 31 bitop3:0x6c
	v_lshl_add_u32 v20, v20, 4, v117
	ds_read_b128 v[20:23], v20
	v_mov_b32_e32 v28, v1
	s_waitcnt lgkmcnt(0)
	v_mfma_f32_32x32x16_bf16 v[4:19], v[36:39], v[20:23], v[4:19]
	v_bitop3_b32 v20, v116, v214, 31 bitop3:0x6c
	v_lshl_add_u32 v20, v20, 4, v117
	ds_read_b128 v[20:23], v20
	s_nop 0
	v_lshl_add_u32 v29, v28, 9, s4
	s_waitcnt lgkmcnt(0)
	v_mfma_f32_32x32x16_bf16 v[4:19], v[24:27], v[20:23], v[4:19]
	v_bitop3_b32 v20, v28, v217, 31 bitop3:0x6c
	v_lshl_add_u32 v20, v20, 4, v29
	ds_read_b128 v[20:23], v20
	v_mov_b32_e32 v24, v1
	s_waitcnt lgkmcnt(0)
	v_mfma_f32_32x32x16_bf16 v[4:19], v[44:47], v[20:23], v[4:19]
	v_bitop3_b32 v20, v28, v206, 31 bitop3:0x6c
	v_lshl_add_u32 v20, v20, 4, v29
	ds_read_b128 v[20:23], v20
	s_waitcnt lgkmcnt(0)
	v_mfma_f32_32x32x16_bf16 v[4:19], v[32:35], v[20:23], v[4:19]
	v_bitop3_b32 v20, v28, v216, 31 bitop3:0x6c
	v_lshl_add_u32 v20, v20, 4, v29
	ds_read_b128 v[20:23], v20
	s_waitcnt lgkmcnt(0)
	v_mfma_f32_32x32x16_bf16 v[4:19], v[52:55], v[20:23], v[4:19]
	v_bitop3_b32 v20, v28, v211, 31 bitop3:0x6c
	v_lshl_add_u32 v20, v20, 4, v29
	ds_read_b128 v[20:23], v20
	s_nop 0
	v_lshl_add_u32 v25, v24, 9, s4
	s_waitcnt lgkmcnt(0)
	v_mfma_f32_32x32x16_bf16 v[4:19], v[40:43], v[20:23], v[4:19]
	v_bitop3_b32 v20, v24, v215, 31 bitop3:0x6c
	v_lshl_add_u32 v20, v20, 4, v25
	ds_read_b128 v[20:23], v20
	s_waitcnt lgkmcnt(0)
	v_mfma_f32_32x32x16_bf16 v[4:19], v[60:63], v[20:23], v[4:19]
	v_bitop3_b32 v20, v24, v202, 31 bitop3:0x6c
	v_lshl_add_u32 v20, v20, 4, v25
	ds_read_b128 v[20:23], v20
	s_waitcnt lgkmcnt(0)
	v_mfma_f32_32x32x16_bf16 v[4:19], v[48:51], v[20:23], v[4:19]
	v_bitop3_b32 v20, v24, v213, 31 bitop3:0x6c
	v_lshl_add_u32 v20, v20, 4, v25
	ds_read_b128 v[20:23], v20
	s_waitcnt lgkmcnt(0)
	v_mfma_f32_32x32x16_bf16 v[4:19], v[68:71], v[20:23], v[4:19]
	v_bitop3_b32 v20, v24, v208, 31 bitop3:0x6c
	v_lshl_add_u32 v20, v20, 4, v25
	ds_read_b128 v[20:23], v20
	s_nop 0
	v_lshl_add_u32 v24, v1, 9, s4
	s_waitcnt lgkmcnt(0)
	v_mfma_f32_32x32x16_bf16 v[4:19], v[56:59], v[20:23], v[4:19]
	v_bitop3_b32 v20, v1, v212, 31 bitop3:0x6c
	v_lshl_add_u32 v20, v20, 4, v24
	ds_read_b128 v[20:23], v20
	s_waitcnt lgkmcnt(0)
	v_mfma_f32_32x32x16_bf16 v[4:19], v[72:75], v[20:23], v[4:19]
	v_bitop3_b32 v20, v1, v201, 31 bitop3:0x6c
	v_lshl_add_u32 v20, v20, 4, v24
	ds_read_b128 v[20:23], v20
	s_waitcnt lgkmcnt(0)
	v_mfma_f32_32x32x16_bf16 v[4:19], v[64:67], v[20:23], v[4:19]
	v_bitop3_b32 v20, v1, v210, 31 bitop3:0x6c
	v_lshl_add_u32 v20, v20, 4, v24
	ds_read_b128 v[20:23], v20
	v_bitop3_b32 v1, v1, v204, 31 bitop3:0x6c
	v_lshl_add_u32 v1, v1, 4, v24
	s_waitcnt lgkmcnt(0)
	v_mfma_f32_32x32x16_bf16 v[4:19], v[76:79], v[20:23], v[4:19]
	ds_read_b128 v[20:23], v1
	s_waitcnt lgkmcnt(0)
	v_mfma_f32_32x32x16_bf16 v[4:19], v[80:83], v[20:23], v[4:19]
	s_setprio 0
	s_nop 11
	v_mul_f32_e32 v20, v4, v168
	ds_bpermute_b32 v21, v153, v20
	s_and_saveexec_b64 s[0:1], vcc
	s_cbranch_execz .LBB0_1344
	s_waitcnt vmcnt(24)
	v_lshlrev_b32_e32 v22, 16, v151
	v_and_b32_e32 v23, 0xffff0000, v151
	s_waitcnt lgkmcnt(0)
	v_pk_mul_f32 v[20:21], v[20:21], v[22:23]
	s_nop 0
	v_and_b32_sdwa v4, v20, v227 dst_sel:DWORD dst_unused:UNUSED_PAD src0_sel:WORD_1 src1_sel:DWORD
	v_and_b32_sdwa v1, v21, v227 dst_sel:DWORD dst_unused:UNUSED_PAD src0_sel:WORD_1 src1_sel:DWORD
	v_add3_u32 v4, v20, v4, s97
	v_add3_u32 v1, v21, v1, s97
	v_lshrrev_b32_e32 v4, 16, v4
	v_and_or_b32 v1, v1, s85, v4
	global_store_dword v[84:85], v1, off offset:448
